# speedup vs baseline: 1.0466x; 1.0024x over previous
_Z4k_k2ILb0EEvPKDF16_S1_PKfS3_S3_S1_S1_PfS3_S3_S1_PDF16_PKiS4_S4_:
	s_load_dwordx2 s[24:25], s[0:1], 0x58
	s_load_dwordx8 s[4:11], s[0:1], 0x38
	s_load_dwordx4 s[20:23], s[0:1], 0x0
	s_load_dwordx8 s[12:19], s[0:1], 0x18
	s_load_dwordx2 s[54:55], s[0:1], 0x10
	s_lshl_b32 s3, s2, 5
	s_and_b32 s3, s3, 0xe0
	s_lshr_b32 s26, s2, 3
	s_or_b32 s3, s3, s26
	s_movk_i32 s26, 0x100
	s_lshl_b32 s28, s3, 5
	v_cmp_gt_u32_e32 vcc, s26, v0
	v_mov_b32_e32 v67, 0
	v_lshlrev_b32_e32 v66, 4, v0
	s_lshl_b32 s0, s3, 1
	s_and_b32 s26, s0, 0xffffffe
	s_mov_b32 s27, 0
	s_waitcnt lgkmcnt(0)
	v_lshl_add_u64 v[2:3], s[16:17], 0, v[66:67]
	s_lshl_b64 s[0:1], s[26:27], 13
	s_or_b32 s26, s26, 1
	v_lshl_add_u64 v[4:5], v[2:3], 0, s[0:1]
	s_lshl_b64 s[0:1], s[26:27], 13
	v_lshl_add_u64 v[2:3], v[2:3], 0, s[0:1]
	global_load_dwordx4 v[68:71], v[4:5], off
	global_load_dwordx4 v[72:75], v[2:3], off
	v_lshl_add_u64 v[2:3], s[12:13], 0, v[66:67]
	s_movk_i32 s29, 0x2000
	v_add_co_u32_e32 v4, vcc, s29, v2
	s_movk_i32 s52, 0x4000
	s_nop 0
	v_addc_co_u32_e32 v5, vcc, 0, v3, vcc
	v_add_co_u32_e32 v18, vcc, s52, v2
	s_movk_i32 s33, 0x6000
	s_nop 0
	v_addc_co_u32_e32 v19, vcc, 0, v3, vcc
	s_lshl_b32 s26, s3, 2
	global_load_dwordx4 v[14:17], v66, s[12:13]
	global_load_dwordx4 v[10:13], v[4:5], off
	global_load_dwordx4 v[6:9], v[18:19], off
	v_add_co_u32_e32 v18, vcc, s33, v2
	s_add_u32 s0, s24, 0x800000
	s_nop 0
	v_addc_co_u32_e32 v19, vcc, 0, v3, vcc
	s_addc_u32 s1, s25, 0
	s_lshl_b64 s[12:13], s[26:27], 13
	v_lshlrev_b32_e32 v20, 2, v0
	global_load_dwordx4 v[2:5], v[18:19], off
	global_load_dword v1, v20, s[14:15]
	v_or_b32_e32 v18, s12, v66
	v_mov_b32_e32 v19, s13
	s_or_b32 s12, s26, 1
	s_mov_b32 s13, s27
	s_lshl_b64 s[12:13], s[12:13], 13
	v_lshl_add_u64 v[76:77], s[22:23], 0, v[18:19]
	v_lshl_add_u64 v[78:79], s[20:21], 0, v[18:19]
	v_lshl_add_u64 v[80:81], s[0:1], 0, v[18:19]
	v_or_b32_e32 v18, s12, v66
	v_mov_b32_e32 v19, s13
	s_or_b32 s12, s26, 2
	s_mov_b32 s13, s27
	s_lshl_b64 s[12:13], s[12:13], 13
	s_or_b32 s26, s26, 3
	v_lshl_add_u64 v[82:83], s[22:23], 0, v[18:19]
	v_lshl_add_u64 v[84:85], s[20:21], 0, v[18:19]
	v_lshl_add_u64 v[86:87], s[0:1], 0, v[18:19]
	v_or_b32_e32 v18, s12, v66
	v_mov_b32_e32 v19, s13
	s_lshl_b64 s[12:13], s[26:27], 13
	v_lshl_add_u64 v[88:89], s[22:23], 0, v[18:19]
	v_lshl_add_u64 v[90:91], s[20:21], 0, v[18:19]
	v_lshl_add_u64 v[92:93], s[0:1], 0, v[18:19]
	v_or_b32_e32 v18, s12, v66
	v_mov_b32_e32 v19, s13
	v_lshl_add_u64 v[94:95], s[22:23], 0, v[18:19]
	v_lshl_add_u64 v[96:97], s[20:21], 0, v[18:19]
	v_lshl_add_u64 v[98:99], s[0:1], 0, v[18:19]
	global_load_dwordx4 v[62:65], v[76:77], off
	global_load_dwordx4 v[54:57], v[78:79], off
	global_load_dwordx4 v[58:61], v[80:81], off
	v_mov_b64_e32 v[212:213], v[82:83]
	v_mov_b64_e32 v[214:215], v[84:85]
	v_mov_b64_e32 v[216:217], v[86:87]
	v_mov_b64_e32 v[218:219], v[88:89]
	v_mov_b64_e32 v[220:221], v[90:91]
	v_mov_b64_e32 v[222:223], v[92:93]
	v_mov_b64_e32 v[224:225], v[94:95]
	v_mov_b64_e32 v[226:227], v[96:97]
	v_mov_b64_e32 v[228:229], v[98:99]
	s_lshl_b32 s30, s28, 7
	s_add_u32 s54, s54, s30
	s_addc_u32 s55, s55, 0
	s_load_dwordx16 s[36:51], s[54:55], 0x0
	s_load_dwordx16 s[72:87], s[54:55], 0x40
	s_load_dwordx16 s[56:71], s[54:55], 0x80
	s_load_dwordx8 s[88:95], s[54:55], 0xc0
	s_load_dwordx4 s[96:99], s[54:55], 0xe0
	s_load_dwordx4 s[20:23], s[54:55], 0xf0
	v_lshrrev_b32_e32 v196, 6, v0
	s_nop 1
	v_readfirstlane_b32 s16, v196
	s_nop 3
	s_lshl_b32 s16, s16, 9
	s_add_u32 s16, s54, s16
	s_addc_u32 s17, s55, 0
	s_load_dword s30, s[16:17], 0x0
	s_load_dword s30, s[16:17], 0x40
	s_load_dword s30, s[16:17], 0x80
	s_load_dword s30, s[16:17], 0xc0
	s_load_dword s30, s[16:17], 0x100
	s_load_dword s30, s[16:17], 0x140
	s_load_dword s30, s[16:17], 0x180
	s_load_dword s30, s[16:17], 0x1c0
	s_waitcnt vmcnt(9)
	v_cvt_f32_f16_e32 v134, v68
	v_cvt_f32_f16_sdwa v135, v68 dst_sel:DWORD dst_unused:UNUSED_PAD src0_sel:WORD_1
	v_cvt_f32_f16_e32 v136, v69
	v_cvt_f32_f16_sdwa v137, v69 dst_sel:DWORD dst_unused:UNUSED_PAD src0_sel:WORD_1
	v_cvt_f32_f16_e32 v138, v70
	v_cvt_f32_f16_sdwa v139, v70 dst_sel:DWORD dst_unused:UNUSED_PAD src0_sel:WORD_1
	v_cvt_f32_f16_e32 v140, v71
	v_cvt_f32_f16_sdwa v141, v71 dst_sel:DWORD dst_unused:UNUSED_PAD src0_sel:WORD_1
	s_waitcnt vmcnt(8)
	v_cvt_f32_f16_e32 v142, v72
	v_cvt_f32_f16_sdwa v143, v72 dst_sel:DWORD dst_unused:UNUSED_PAD src0_sel:WORD_1
	v_cvt_f32_f16_e32 v144, v73
	v_cvt_f32_f16_sdwa v145, v73 dst_sel:DWORD dst_unused:UNUSED_PAD src0_sel:WORD_1
	v_cvt_f32_f16_e32 v146, v74
	v_cvt_f32_f16_sdwa v147, v74 dst_sel:DWORD dst_unused:UNUSED_PAD src0_sel:WORD_1
	v_cvt_f32_f16_e32 v148, v75
	v_cvt_f32_f16_sdwa v149, v75 dst_sel:DWORD dst_unused:UNUSED_PAD src0_sel:WORD_1
	s_waitcnt lgkmcnt(0)
	v_lshlrev_b32_e32 v68, 1, v0
	s_waitcnt vmcnt(2)
	v_cvt_f32_f16_e32 v150, v62
	s_waitcnt vmcnt(1)
	v_cvt_f32_f16_e32 v69, v54
	v_pk_mul_f32 v[154:155], v[150:151], v[14:15] op_sel_hi:[0,1]
	v_exp_f32_e32 v154, v154
	v_exp_f32_e32 v155, v155
	v_pk_mul_f32 v[156:157], v[150:151], v[16:17] op_sel_hi:[0,1]
	v_exp_f32_e32 v156, v156
	v_exp_f32_e32 v157, v157
	v_mul_f32_e32 v152, v150, v69
	v_pk_mul_f32 v[134:135], v[154:155], v[134:135]
	v_pk_fma_f32 v[134:135], v[152:153], s[36:37], v[134:135] op_sel_hi:[0, 1, 1]
	v_pk_fma_f32 v[70:71], s[72:73], v[134:135], 0 op_sel_hi:[1, 1, 0]
	v_pk_mul_f32 v[86:87], v[156:157], v[136:137]
	s_nop 0
	v_pk_fma_f32 v[136:137], v[152:153], s[38:39], v[86:87] op_sel_hi:[0, 1, 1]
	v_pk_mul_f32 v[72:73], v[150:151], v[10:11] op_sel_hi:[0,1]
	v_exp_f32_e32 v72, v72
	v_exp_f32_e32 v73, v73
	v_pk_mul_f32 v[86:87], v[150:151], v[12:13] op_sel_hi:[0,1]
	v_exp_f32_e32 v86, v86
	v_exp_f32_e32 v87, v87
	v_pk_mul_f32 v[72:73], v[72:73], v[138:139]
	v_pk_fma_f32 v[70:71], s[74:75], v[136:137], v[70:71]
	v_pk_fma_f32 v[138:139], v[152:153], s[40:41], v[72:73] op_sel_hi:[0, 1, 1]
	v_pk_mul_f32 v[72:73], v[86:87], v[140:141]
	v_pk_mul_f32 v[74:75], v[150:151], v[8:9] op_sel_hi:[0,1]
	v_pk_fma_f32 v[140:141], v[152:153], s[42:43], v[72:73] op_sel_hi:[0, 1, 1]
	v_pk_mul_f32 v[72:73], v[150:151], v[6:7] op_sel_hi:[0,1]
	v_exp_f32_e32 v72, v72
	v_exp_f32_e32 v73, v73
	v_exp_f32_e32 v74, v74
	v_exp_f32_e32 v75, v75
	v_pk_fma_f32 v[70:71], s[76:77], v[138:139], v[70:71]
	v_pk_mul_f32 v[72:73], v[72:73], v[142:143]
	v_pk_fma_f32 v[70:71], s[78:79], v[140:141], v[70:71]
	v_pk_fma_f32 v[142:143], v[152:153], s[44:45], v[72:73] op_sel_hi:[0, 1, 1]
	v_pk_mul_f32 v[72:73], v[74:75], v[144:145]
	v_pk_mul_f32 v[74:75], v[150:151], v[4:5] op_sel_hi:[0,1]
	v_pk_fma_f32 v[144:145], v[152:153], s[46:47], v[72:73] op_sel_hi:[0, 1, 1]
	v_pk_mul_f32 v[72:73], v[150:151], v[2:3] op_sel_hi:[0,1]
	v_exp_f32_e32 v72, v72
	v_exp_f32_e32 v73, v73
	v_exp_f32_e32 v74, v74
	v_exp_f32_e32 v75, v75
	v_pk_fma_f32 v[70:71], s[80:81], v[142:143], v[70:71]
	v_pk_mul_f32 v[72:73], v[72:73], v[146:147]
	v_pk_fma_f32 v[70:71], s[82:83], v[144:145], v[70:71]
	v_pk_fma_f32 v[146:147], v[152:153], s[48:49], v[72:73] op_sel_hi:[0, 1, 1]
	v_pk_mul_f32 v[72:73], v[74:75], v[148:149]
	v_pk_fma_f32 v[70:71], s[84:85], v[146:147], v[70:71]
	v_pk_fma_f32 v[148:149], v[152:153], s[50:51], v[72:73] op_sel_hi:[0, 1, 1]
	v_pk_fma_f32 v[70:71], s[86:87], v[148:149], v[70:71]
	s_nop 0
	v_add_f32_e32 v69, v70, v71
	v_fma_mix_f32 v69, v1, v54, v69 op_sel_hi:[0,1,0]
	s_waitcnt vmcnt(0)
	v_fma_mixlo_f16 v69, v69, v58, 0 op_sel_hi:[0,1,0]
	ds_write_b16 v68, v69 offset:4096
	global_load_dwordx4 v[50:53], v[212:213], off
	global_load_dwordx4 v[42:45], v[214:215], off
	global_load_dwordx4 v[46:49], v[216:217], off
	global_load_dwordx4 v[38:41], v[218:219], off
	global_load_dwordx4 v[30:33], v[220:221], off
	global_load_dwordx4 v[34:37], v[222:223], off
	global_load_dwordx4 v[26:29], v[224:225], off
	global_load_dwordx4 v[18:21], v[226:227], off
	global_load_dwordx4 v[22:25], v[228:229], off
	s_waitcnt lgkmcnt(0)
	s_load_dwordx16 s[36:51], s[54:55], 0x100
	s_load_dwordx16 s[72:87], s[54:55], 0x140
	v_cvt_f32_f16_sdwa v62, v62 dst_sel:DWORD dst_unused:UNUSED_PAD src0_sel:WORD_1
	v_cvt_f32_f16_sdwa v69, v54 dst_sel:DWORD dst_unused:UNUSED_PAD src0_sel:WORD_1
	v_pk_mul_f32 v[152:153], v[62:63], v[14:15] op_sel_hi:[0,1]
	v_exp_f32_e32 v152, v152
	v_exp_f32_e32 v153, v153
	v_pk_mul_f32 v[154:155], v[62:63], v[16:17] op_sel_hi:[0,1]
	v_exp_f32_e32 v154, v154
	v_exp_f32_e32 v155, v155
	v_mul_f32_e32 v150, v62, v69
	v_pk_mul_f32 v[134:135], v[152:153], v[134:135]
	v_pk_fma_f32 v[134:135], v[150:151], s[56:57], v[134:135] op_sel_hi:[0, 1, 1]
	v_pk_fma_f32 v[102:103], s[88:89], v[134:135], 0 op_sel_hi:[1, 1, 0]
	v_pk_mul_f32 v[118:119], v[154:155], v[136:137]
	s_nop 0
	v_pk_fma_f32 v[136:137], v[150:151], s[58:59], v[118:119] op_sel_hi:[0, 1, 1]
	v_pk_mul_f32 v[104:105], v[62:63], v[10:11] op_sel_hi:[0,1]
	v_exp_f32_e32 v104, v104
	v_exp_f32_e32 v105, v105
	v_pk_mul_f32 v[118:119], v[62:63], v[12:13] op_sel_hi:[0,1]
	v_exp_f32_e32 v118, v118
	v_exp_f32_e32 v119, v119
	v_pk_mul_f32 v[104:105], v[104:105], v[138:139]
	v_pk_fma_f32 v[102:103], s[90:91], v[136:137], v[102:103]
	v_pk_fma_f32 v[138:139], v[150:151], s[60:61], v[104:105] op_sel_hi:[0, 1, 1]
	v_pk_mul_f32 v[104:105], v[118:119], v[140:141]
	v_pk_mul_f32 v[106:107], v[62:63], v[8:9] op_sel_hi:[0,1]
	v_pk_fma_f32 v[140:141], v[150:151], s[62:63], v[104:105] op_sel_hi:[0, 1, 1]
	v_pk_mul_f32 v[104:105], v[62:63], v[6:7] op_sel_hi:[0,1]
	v_exp_f32_e32 v104, v104
	v_exp_f32_e32 v105, v105
	v_exp_f32_e32 v106, v106
	v_exp_f32_e32 v107, v107
	v_pk_fma_f32 v[102:103], s[92:93], v[138:139], v[102:103]
	v_pk_mul_f32 v[104:105], v[104:105], v[142:143]
	v_pk_fma_f32 v[102:103], s[94:95], v[140:141], v[102:103]
	v_pk_fma_f32 v[142:143], v[150:151], s[64:65], v[104:105] op_sel_hi:[0, 1, 1]
	v_pk_mul_f32 v[104:105], v[106:107], v[144:145]
	v_pk_mul_f32 v[106:107], v[62:63], v[4:5] op_sel_hi:[0,1]
	v_pk_fma_f32 v[144:145], v[150:151], s[66:67], v[104:105] op_sel_hi:[0, 1, 1]
	v_pk_mul_f32 v[104:105], v[62:63], v[2:3] op_sel_hi:[0,1]
	v_exp_f32_e32 v104, v104
	v_exp_f32_e32 v105, v105
	v_exp_f32_e32 v106, v106
	v_exp_f32_e32 v107, v107
	v_pk_fma_f32 v[102:103], s[96:97], v[142:143], v[102:103]
	v_pk_mul_f32 v[104:105], v[104:105], v[146:147]
	v_pk_fma_f32 v[102:103], s[98:99], v[144:145], v[102:103]
	v_pk_fma_f32 v[146:147], v[150:151], s[68:69], v[104:105] op_sel_hi:[0, 1, 1]
	v_pk_mul_f32 v[104:105], v[106:107], v[148:149]
	v_pk_fma_f32 v[102:103], s[20:21], v[146:147], v[102:103]
	v_pk_fma_f32 v[148:149], v[150:151], s[70:71], v[104:105] op_sel_hi:[0, 1, 1]
	v_pk_fma_f32 v[102:103], s[22:23], v[148:149], v[102:103]
	s_nop 0
	v_add_f32_e32 v62, v102, v103
	v_fma_mix_f32 v54, v1, v54, v62 op_sel:[0,1,0] op_sel_hi:[0,1,0]
	v_fma_mixlo_f16 v54, v54, v58, 0 op_sel:[0,1,0] op_sel_hi:[0,1,0]
	ds_write_b16 v68, v54 offset:5136
	s_waitcnt lgkmcnt(0)
	s_load_dwordx16 s[56:71], s[54:55], 0x180
	s_load_dwordx8 s[88:95], s[54:55], 0x1c0
	s_load_dwordx4 s[96:99], s[54:55], 0x1e0
	s_load_dwordx4 s[20:23], s[54:55], 0x1f0
	v_cvt_f32_f16_e32 v54, v63
	v_cvt_f32_f16_e32 v58, v55
	v_pk_mul_f32 v[150:151], v[54:55], v[14:15] op_sel_hi:[0,1]
	v_exp_f32_e32 v150, v150
	v_exp_f32_e32 v151, v151
	v_pk_mul_f32 v[152:153], v[54:55], v[16:17] op_sel_hi:[0,1]
	v_exp_f32_e32 v152, v152
	v_exp_f32_e32 v153, v153
	v_mul_f32_e32 v58, v54, v58
	v_pk_mul_f32 v[134:135], v[150:151], v[134:135]
	v_pk_fma_f32 v[134:135], v[58:59], s[36:37], v[134:135] op_sel_hi:[0, 1, 1]
	v_pk_fma_f32 v[70:71], s[72:73], v[134:135], 0 op_sel_hi:[1, 1, 0]
	v_pk_mul_f32 v[86:87], v[152:153], v[136:137]
	s_nop 0
	v_pk_fma_f32 v[136:137], v[58:59], s[38:39], v[86:87] op_sel_hi:[0, 1, 1]
	v_pk_mul_f32 v[72:73], v[54:55], v[10:11] op_sel_hi:[0,1]
	v_exp_f32_e32 v72, v72
	v_exp_f32_e32 v73, v73
	v_pk_mul_f32 v[86:87], v[54:55], v[12:13] op_sel_hi:[0,1]
	v_exp_f32_e32 v86, v86
	v_exp_f32_e32 v87, v87
	v_pk_mul_f32 v[72:73], v[72:73], v[138:139]
	v_pk_fma_f32 v[70:71], s[74:75], v[136:137], v[70:71]
	v_pk_fma_f32 v[138:139], v[58:59], s[40:41], v[72:73] op_sel_hi:[0, 1, 1]
	v_pk_mul_f32 v[72:73], v[86:87], v[140:141]
	v_pk_mul_f32 v[74:75], v[54:55], v[8:9] op_sel_hi:[0,1]
	v_pk_fma_f32 v[140:141], v[58:59], s[42:43], v[72:73] op_sel_hi:[0, 1, 1]
	v_pk_mul_f32 v[72:73], v[54:55], v[6:7] op_sel_hi:[0,1]
	v_exp_f32_e32 v72, v72
	v_exp_f32_e32 v73, v73
	v_exp_f32_e32 v74, v74
	v_exp_f32_e32 v75, v75
	v_pk_fma_f32 v[70:71], s[76:77], v[138:139], v[70:71]
	v_pk_mul_f32 v[72:73], v[72:73], v[142:143]
	v_pk_fma_f32 v[70:71], s[78:79], v[140:141], v[70:71]
	v_pk_fma_f32 v[142:143], v[58:59], s[44:45], v[72:73] op_sel_hi:[0, 1, 1]
	v_pk_mul_f32 v[72:73], v[74:75], v[144:145]
	v_pk_mul_f32 v[74:75], v[54:55], v[4:5] op_sel_hi:[0,1]
	v_pk_fma_f32 v[144:145], v[58:59], s[46:47], v[72:73] op_sel_hi:[0, 1, 1]
	v_pk_mul_f32 v[72:73], v[54:55], v[2:3] op_sel_hi:[0,1]
	v_exp_f32_e32 v72, v72
	v_exp_f32_e32 v73, v73
	v_exp_f32_e32 v74, v74
	v_exp_f32_e32 v75, v75
	v_pk_fma_f32 v[70:71], s[80:81], v[142:143], v[70:71]
	v_pk_mul_f32 v[72:73], v[72:73], v[146:147]
	v_pk_fma_f32 v[70:71], s[82:83], v[144:145], v[70:71]
	v_pk_fma_f32 v[146:147], v[58:59], s[48:49], v[72:73] op_sel_hi:[0, 1, 1]
	v_pk_mul_f32 v[72:73], v[74:75], v[148:149]
	v_pk_fma_f32 v[70:71], s[84:85], v[146:147], v[70:71]
	v_pk_fma_f32 v[148:149], v[58:59], s[50:51], v[72:73] op_sel_hi:[0, 1, 1]
	v_pk_fma_f32 v[70:71], s[86:87], v[148:149], v[70:71]
	s_nop 0
	v_add_f32_e32 v54, v70, v71
	v_fma_mix_f32 v54, v1, v55, v54 op_sel_hi:[0,1,0]
	v_fma_mixlo_f16 v54, v54, v59, 0 op_sel_hi:[0,1,0]
	ds_write_b16 v68, v54 offset:6176
	s_waitcnt lgkmcnt(0)
	s_load_dwordx16 s[36:51], s[54:55], 0x200
	s_load_dwordx16 s[72:87], s[54:55], 0x240
	v_cvt_f32_f16_sdwa v54, v63 dst_sel:DWORD dst_unused:UNUSED_PAD src0_sel:WORD_1
	v_cvt_f32_f16_sdwa v58, v55 dst_sel:DWORD dst_unused:UNUSED_PAD src0_sel:WORD_1
	v_pk_mul_f32 v[62:63], v[54:55], v[14:15] op_sel_hi:[0,1]
	v_exp_f32_e32 v62, v62
	v_exp_f32_e32 v63, v63
	v_pk_mul_f32 v[150:151], v[54:55], v[16:17] op_sel_hi:[0,1]
	v_exp_f32_e32 v150, v150
	v_exp_f32_e32 v151, v151
	v_mul_f32_e32 v58, v54, v58
	v_pk_mul_f32 v[62:63], v[62:63], v[134:135]
	v_pk_fma_f32 v[62:63], v[58:59], s[56:57], v[62:63] op_sel_hi:[0, 1, 1]
	v_pk_fma_f32 v[102:103], s[88:89], v[62:63], 0 op_sel_hi:[1, 1, 0]
	v_pk_mul_f32 v[118:119], v[150:151], v[136:137]
	s_nop 0
	v_pk_fma_f32 v[134:135], v[58:59], s[58:59], v[118:119] op_sel_hi:[0, 1, 1]
	v_pk_mul_f32 v[104:105], v[54:55], v[10:11] op_sel_hi:[0,1]
	v_exp_f32_e32 v104, v104
	v_exp_f32_e32 v105, v105
	v_pk_mul_f32 v[118:119], v[54:55], v[12:13] op_sel_hi:[0,1]
	v_exp_f32_e32 v118, v118
	v_exp_f32_e32 v119, v119
	v_pk_mul_f32 v[104:105], v[104:105], v[138:139]
	v_pk_fma_f32 v[102:103], s[90:91], v[134:135], v[102:103]
	v_pk_fma_f32 v[136:137], v[58:59], s[60:61], v[104:105] op_sel_hi:[0, 1, 1]
	v_pk_mul_f32 v[104:105], v[118:119], v[140:141]
	v_pk_mul_f32 v[106:107], v[54:55], v[8:9] op_sel_hi:[0,1]
	v_pk_fma_f32 v[138:139], v[58:59], s[62:63], v[104:105] op_sel_hi:[0, 1, 1]
	v_pk_mul_f32 v[104:105], v[54:55], v[6:7] op_sel_hi:[0,1]
	v_exp_f32_e32 v104, v104
	v_exp_f32_e32 v105, v105
	v_exp_f32_e32 v106, v106
	v_exp_f32_e32 v107, v107
	v_pk_fma_f32 v[102:103], s[92:93], v[136:137], v[102:103]
	v_pk_mul_f32 v[104:105], v[104:105], v[142:143]
	v_pk_fma_f32 v[102:103], s[94:95], v[138:139], v[102:103]
	v_pk_fma_f32 v[140:141], v[58:59], s[64:65], v[104:105] op_sel_hi:[0, 1, 1]
	v_pk_mul_f32 v[104:105], v[106:107], v[144:145]
	v_pk_mul_f32 v[106:107], v[54:55], v[4:5] op_sel_hi:[0,1]
	v_pk_fma_f32 v[142:143], v[58:59], s[66:67], v[104:105] op_sel_hi:[0, 1, 1]
	v_pk_mul_f32 v[104:105], v[54:55], v[2:3] op_sel_hi:[0,1]
	v_exp_f32_e32 v104, v104
	v_exp_f32_e32 v105, v105
	v_exp_f32_e32 v106, v106
	v_exp_f32_e32 v107, v107
	v_pk_fma_f32 v[102:103], s[96:97], v[140:141], v[102:103]
	v_pk_mul_f32 v[104:105], v[104:105], v[146:147]
	v_pk_fma_f32 v[102:103], s[98:99], v[142:143], v[102:103]
	v_pk_fma_f32 v[144:145], v[58:59], s[68:69], v[104:105] op_sel_hi:[0, 1, 1]
	v_pk_mul_f32 v[104:105], v[106:107], v[148:149]
	v_pk_fma_f32 v[102:103], s[20:21], v[144:145], v[102:103]
	v_pk_fma_f32 v[146:147], v[58:59], s[70:71], v[104:105] op_sel_hi:[0, 1, 1]
	v_pk_fma_f32 v[102:103], s[22:23], v[146:147], v[102:103]
	s_nop 0
	v_add_f32_e32 v54, v102, v103
	v_fma_mix_f32 v54, v1, v55, v54 op_sel:[0,1,0] op_sel_hi:[0,1,0]
	v_fma_mixlo_f16 v54, v54, v59, 0 op_sel:[0,1,0] op_sel_hi:[0,1,0]
	ds_write_b16 v68, v54 offset:7216
	s_waitcnt lgkmcnt(0)
	s_load_dwordx16 s[56:71], s[54:55], 0x280
	s_load_dwordx8 s[88:95], s[54:55], 0x2c0
	s_load_dwordx4 s[96:99], s[54:55], 0x2e0
	s_load_dwordx4 s[20:23], s[54:55], 0x2f0
	v_cvt_f32_f16_e32 v54, v64
	v_cvt_f32_f16_e32 v55, v56
	v_pk_mul_f32 v[148:149], v[54:55], v[14:15] op_sel_hi:[0,1]
	v_exp_f32_e32 v148, v148
	v_exp_f32_e32 v149, v149
	v_pk_mul_f32 v[150:151], v[54:55], v[16:17] op_sel_hi:[0,1]
	v_exp_f32_e32 v150, v150
	v_exp_f32_e32 v151, v151
	v_mul_f32_e32 v58, v54, v55
	v_pk_mul_f32 v[62:63], v[148:149], v[62:63]
	v_pk_fma_f32 v[62:63], v[58:59], s[36:37], v[62:63] op_sel_hi:[0, 1, 1]
	v_pk_fma_f32 v[70:71], s[72:73], v[62:63], 0 op_sel_hi:[1, 1, 0]
	v_pk_mul_f32 v[86:87], v[150:151], v[134:135]
	s_nop 0
	v_pk_fma_f32 v[134:135], v[58:59], s[38:39], v[86:87] op_sel_hi:[0, 1, 1]
	v_pk_mul_f32 v[72:73], v[54:55], v[10:11] op_sel_hi:[0,1]
	v_exp_f32_e32 v72, v72
	v_exp_f32_e32 v73, v73
	v_pk_mul_f32 v[86:87], v[54:55], v[12:13] op_sel_hi:[0,1]
	v_exp_f32_e32 v86, v86
	v_exp_f32_e32 v87, v87
	v_pk_mul_f32 v[72:73], v[72:73], v[136:137]
	v_pk_fma_f32 v[70:71], s[74:75], v[134:135], v[70:71]
	v_pk_fma_f32 v[136:137], v[58:59], s[40:41], v[72:73] op_sel_hi:[0, 1, 1]
	v_pk_mul_f32 v[72:73], v[86:87], v[138:139]
	v_pk_mul_f32 v[74:75], v[54:55], v[8:9] op_sel_hi:[0,1]
	v_pk_fma_f32 v[138:139], v[58:59], s[42:43], v[72:73] op_sel_hi:[0, 1, 1]
	v_pk_mul_f32 v[72:73], v[54:55], v[6:7] op_sel_hi:[0,1]
	v_exp_f32_e32 v72, v72
	v_exp_f32_e32 v73, v73
	v_exp_f32_e32 v74, v74
	v_exp_f32_e32 v75, v75
	v_pk_fma_f32 v[70:71], s[76:77], v[136:137], v[70:71]
	v_pk_mul_f32 v[72:73], v[72:73], v[140:141]
	v_pk_fma_f32 v[70:71], s[78:79], v[138:139], v[70:71]
	v_pk_fma_f32 v[140:141], v[58:59], s[44:45], v[72:73] op_sel_hi:[0, 1, 1]
	v_pk_mul_f32 v[72:73], v[74:75], v[142:143]
	v_pk_fma_f32 v[70:71], s[80:81], v[140:141], v[70:71]
	v_pk_fma_f32 v[142:143], v[58:59], s[46:47], v[72:73] op_sel_hi:[0, 1, 1]
	v_pk_mul_f32 v[72:73], v[54:55], v[2:3] op_sel_hi:[0,1]
	v_exp_f32_e32 v72, v72
	v_exp_f32_e32 v73, v73
	v_pk_mul_f32 v[54:55], v[54:55], v[4:5] op_sel_hi:[0,1]
	v_exp_f32_e32 v54, v54
	v_exp_f32_e32 v55, v55
	v_pk_mul_f32 v[72:73], v[72:73], v[144:145]
	v_pk_fma_f32 v[70:71], s[82:83], v[142:143], v[70:71]
	v_pk_fma_f32 v[144:145], v[58:59], s[48:49], v[72:73] op_sel_hi:[0, 1, 1]
	v_pk_mul_f32 v[54:55], v[54:55], v[146:147]
	v_pk_fma_f32 v[70:71], s[84:85], v[144:145], v[70:71]
	v_pk_fma_f32 v[54:55], v[58:59], s[50:51], v[54:55] op_sel_hi:[0, 1, 1]
	v_pk_fma_f32 v[58:59], s[86:87], v[54:55], v[70:71]
	s_nop 0
	v_add_f32_e32 v58, v58, v59
	v_fma_mix_f32 v58, v1, v56, v58 op_sel_hi:[0,1,0]
	v_fma_mixlo_f16 v58, v58, v60, 0 op_sel_hi:[0,1,0]
	ds_write_b16 v68, v58 offset:8256
	s_waitcnt lgkmcnt(0)
	s_load_dwordx16 s[36:51], s[54:55], 0x300
	s_load_dwordx16 s[72:87], s[54:55], 0x340
	v_cvt_f32_f16_sdwa v58, v64 dst_sel:DWORD dst_unused:UNUSED_PAD src0_sel:WORD_1
	v_cvt_f32_f16_sdwa v59, v56 dst_sel:DWORD dst_unused:UNUSED_PAD src0_sel:WORD_1
	v_pk_mul_f32 v[146:147], v[58:59], v[14:15] op_sel_hi:[0,1]
	v_exp_f32_e32 v146, v146
	v_exp_f32_e32 v147, v147
	v_pk_mul_f32 v[148:149], v[58:59], v[16:17] op_sel_hi:[0,1]
	v_exp_f32_e32 v148, v148
	v_exp_f32_e32 v149, v149
	v_mul_f32_e32 v64, v58, v59
	v_pk_mul_f32 v[62:63], v[146:147], v[62:63]
	v_pk_fma_f32 v[62:63], v[64:65], s[56:57], v[62:63] op_sel_hi:[0, 1, 1]
	v_pk_fma_f32 v[102:103], s[88:89], v[62:63], 0 op_sel_hi:[1, 1, 0]
	v_pk_mul_f32 v[118:119], v[148:149], v[134:135]
	s_nop 0
	v_pk_fma_f32 v[134:135], v[64:65], s[58:59], v[118:119] op_sel_hi:[0, 1, 1]
	v_pk_mul_f32 v[104:105], v[58:59], v[10:11] op_sel_hi:[0,1]
	v_exp_f32_e32 v104, v104
	v_exp_f32_e32 v105, v105
	v_pk_mul_f32 v[118:119], v[58:59], v[12:13] op_sel_hi:[0,1]
	v_exp_f32_e32 v118, v118
	v_exp_f32_e32 v119, v119
	v_pk_mul_f32 v[104:105], v[104:105], v[136:137]
	v_pk_fma_f32 v[102:103], s[90:91], v[134:135], v[102:103]
	v_pk_fma_f32 v[136:137], v[64:65], s[60:61], v[104:105] op_sel_hi:[0, 1, 1]
	v_pk_mul_f32 v[104:105], v[118:119], v[138:139]
	v_pk_mul_f32 v[106:107], v[58:59], v[8:9] op_sel_hi:[0,1]
	v_pk_fma_f32 v[138:139], v[64:65], s[62:63], v[104:105] op_sel_hi:[0, 1, 1]
	v_pk_mul_f32 v[104:105], v[58:59], v[6:7] op_sel_hi:[0,1]
	v_exp_f32_e32 v104, v104
	v_exp_f32_e32 v105, v105
	v_exp_f32_e32 v106, v106
	v_exp_f32_e32 v107, v107
	v_pk_fma_f32 v[102:103], s[92:93], v[136:137], v[102:103]
	v_pk_mul_f32 v[104:105], v[104:105], v[140:141]
	v_pk_fma_f32 v[102:103], s[94:95], v[138:139], v[102:103]
	v_pk_fma_f32 v[140:141], v[64:65], s[64:65], v[104:105] op_sel_hi:[0, 1, 1]
	v_pk_mul_f32 v[104:105], v[106:107], v[142:143]
	v_pk_fma_f32 v[102:103], s[96:97], v[140:141], v[102:103]
	v_pk_fma_f32 v[142:143], v[64:65], s[66:67], v[104:105] op_sel_hi:[0, 1, 1]
	v_pk_mul_f32 v[104:105], v[58:59], v[2:3] op_sel_hi:[0,1]
	v_exp_f32_e32 v104, v104
	v_exp_f32_e32 v105, v105
	v_pk_mul_f32 v[58:59], v[58:59], v[4:5] op_sel_hi:[0,1]
	v_exp_f32_e32 v58, v58
	v_exp_f32_e32 v59, v59
	v_pk_mul_f32 v[104:105], v[104:105], v[144:145]
	v_pk_fma_f32 v[102:103], s[98:99], v[142:143], v[102:103]
	v_pk_fma_f32 v[144:145], v[64:65], s[68:69], v[104:105] op_sel_hi:[0, 1, 1]
	v_pk_mul_f32 v[54:55], v[58:59], v[54:55]
	v_pk_fma_f32 v[102:103], s[20:21], v[144:145], v[102:103]
	v_pk_fma_f32 v[54:55], v[64:65], s[70:71], v[54:55] op_sel_hi:[0, 1, 1]
	v_pk_fma_f32 v[58:59], s[22:23], v[54:55], v[102:103]
	s_nop 0
	v_add_f32_e32 v58, v58, v59
	v_fma_mix_f32 v56, v1, v56, v58 op_sel:[0,1,0] op_sel_hi:[0,1,0]
	v_fma_mixlo_f16 v56, v56, v60, 0 op_sel:[0,1,0] op_sel_hi:[0,1,0]
	ds_write_b16 v68, v56 offset:9296
	s_waitcnt lgkmcnt(0)
	s_load_dwordx16 s[56:71], s[54:55], 0x380
	s_load_dwordx8 s[88:95], s[54:55], 0x3c0
	s_load_dwordx4 s[96:99], s[54:55], 0x3e0
	s_load_dwordx4 s[20:23], s[54:55], 0x3f0
	v_cvt_f32_f16_e32 v56, v65
	v_cvt_f32_f16_e32 v58, v57
	v_pk_mul_f32 v[146:147], v[56:57], v[14:15] op_sel_hi:[0,1]
	v_exp_f32_e32 v146, v146
	v_exp_f32_e32 v147, v147
	v_pk_mul_f32 v[148:149], v[56:57], v[16:17] op_sel_hi:[0,1]
	v_exp_f32_e32 v148, v148
	v_exp_f32_e32 v149, v149
	v_mul_f32_e32 v58, v56, v58
	v_pk_mul_f32 v[62:63], v[146:147], v[62:63]
	v_pk_fma_f32 v[62:63], v[58:59], s[36:37], v[62:63] op_sel_hi:[0, 1, 1]
	v_pk_fma_f32 v[70:71], s[72:73], v[62:63], 0 op_sel_hi:[1, 1, 0]
	v_pk_mul_f32 v[86:87], v[148:149], v[134:135]
	s_nop 0
	v_pk_fma_f32 v[134:135], v[58:59], s[38:39], v[86:87] op_sel_hi:[0, 1, 1]
	v_pk_mul_f32 v[72:73], v[56:57], v[10:11] op_sel_hi:[0,1]
	v_exp_f32_e32 v72, v72
	v_exp_f32_e32 v73, v73
	v_pk_mul_f32 v[86:87], v[56:57], v[12:13] op_sel_hi:[0,1]
	v_exp_f32_e32 v86, v86
	v_exp_f32_e32 v87, v87
	v_pk_mul_f32 v[72:73], v[72:73], v[136:137]
	v_pk_fma_f32 v[70:71], s[74:75], v[134:135], v[70:71]
	v_pk_fma_f32 v[136:137], v[58:59], s[40:41], v[72:73] op_sel_hi:[0, 1, 1]
	v_pk_mul_f32 v[72:73], v[86:87], v[138:139]
	v_pk_mul_f32 v[74:75], v[56:57], v[8:9] op_sel_hi:[0,1]
	v_pk_fma_f32 v[138:139], v[58:59], s[42:43], v[72:73] op_sel_hi:[0, 1, 1]
	v_pk_mul_f32 v[72:73], v[56:57], v[6:7] op_sel_hi:[0,1]
	v_exp_f32_e32 v72, v72
	v_exp_f32_e32 v73, v73
	v_exp_f32_e32 v74, v74
	v_exp_f32_e32 v75, v75
	v_pk_fma_f32 v[70:71], s[76:77], v[136:137], v[70:71]
	v_pk_mul_f32 v[72:73], v[72:73], v[140:141]
	v_pk_fma_f32 v[70:71], s[78:79], v[138:139], v[70:71]
	v_pk_fma_f32 v[140:141], v[58:59], s[44:45], v[72:73] op_sel_hi:[0, 1, 1]
	v_pk_mul_f32 v[72:73], v[74:75], v[142:143]
	v_pk_mul_f32 v[74:75], v[56:57], v[4:5] op_sel_hi:[0,1]
	v_pk_fma_f32 v[142:143], v[58:59], s[46:47], v[72:73] op_sel_hi:[0, 1, 1]
	v_pk_mul_f32 v[72:73], v[56:57], v[2:3] op_sel_hi:[0,1]
	v_exp_f32_e32 v72, v72
	v_exp_f32_e32 v73, v73
	v_exp_f32_e32 v74, v74
	v_exp_f32_e32 v75, v75
	v_pk_fma_f32 v[70:71], s[80:81], v[140:141], v[70:71]
	v_pk_mul_f32 v[72:73], v[72:73], v[144:145]
	v_pk_fma_f32 v[70:71], s[82:83], v[142:143], v[70:71]
	v_pk_fma_f32 v[144:145], v[58:59], s[48:49], v[72:73] op_sel_hi:[0, 1, 1]
	v_pk_mul_f32 v[54:55], v[74:75], v[54:55]
	v_pk_fma_f32 v[70:71], s[84:85], v[144:145], v[70:71]
	v_pk_fma_f32 v[54:55], v[58:59], s[50:51], v[54:55] op_sel_hi:[0, 1, 1]
	v_pk_fma_f32 v[58:59], s[86:87], v[54:55], v[70:71]
	s_nop 0
	v_add_f32_e32 v56, v58, v59
	v_fma_mix_f32 v56, v1, v57, v56 op_sel_hi:[0,1,0]
	v_fma_mixlo_f16 v56, v56, v61, 0 op_sel_hi:[0,1,0]
	ds_write_b16 v68, v56 offset:10336
	s_waitcnt lgkmcnt(0)
	s_load_dwordx16 s[36:51], s[54:55], 0x400
	s_load_dwordx16 s[72:87], s[54:55], 0x440
	v_cvt_f32_f16_sdwa v56, v65 dst_sel:DWORD dst_unused:UNUSED_PAD src0_sel:WORD_1
	v_cvt_f32_f16_sdwa v58, v57 dst_sel:DWORD dst_unused:UNUSED_PAD src0_sel:WORD_1
	v_pk_mul_f32 v[64:65], v[56:57], v[14:15] op_sel_hi:[0,1]
	v_pk_mul_f32 v[146:147], v[56:57], v[16:17] op_sel_hi:[0,1]
	v_exp_f32_e32 v64, v64
	v_exp_f32_e32 v65, v65
	v_exp_f32_e32 v146, v146
	v_exp_f32_e32 v147, v147
	v_mul_f32_e32 v58, v56, v58
	v_pk_mul_f32 v[62:63], v[64:65], v[62:63]
	v_pk_mul_f32 v[64:65], v[146:147], v[134:135]
	v_pk_fma_f32 v[134:135], v[58:59], s[58:59], v[64:65] op_sel_hi:[0, 1, 1]
	v_pk_mul_f32 v[64:65], v[56:57], v[10:11] op_sel_hi:[0,1]
	v_pk_fma_f32 v[148:149], v[58:59], s[56:57], v[62:63] op_sel_hi:[0, 1, 1]
	v_exp_f32_e32 v64, v64
	v_exp_f32_e32 v65, v65
	v_pk_mul_f32 v[102:103], v[56:57], v[12:13] op_sel_hi:[0,1]
	v_exp_f32_e32 v102, v102
	v_exp_f32_e32 v103, v103
	v_pk_fma_f32 v[62:63], s[88:89], v[148:149], 0 op_sel_hi:[1, 1, 0]
	v_pk_mul_f32 v[64:65], v[64:65], v[136:137]
	v_pk_fma_f32 v[62:63], s[90:91], v[134:135], v[62:63]
	v_pk_fma_f32 v[136:137], v[58:59], s[60:61], v[64:65] op_sel_hi:[0, 1, 1]
	v_pk_mul_f32 v[64:65], v[102:103], v[138:139]
	v_pk_fma_f32 v[62:63], s[92:93], v[136:137], v[62:63]
	v_pk_fma_f32 v[122:123], v[58:59], s[62:63], v[64:65] op_sel_hi:[0, 1, 1]
	v_pk_mul_f32 v[64:65], v[56:57], v[6:7] op_sel_hi:[0,1]
	v_exp_f32_e32 v64, v64
	v_exp_f32_e32 v65, v65
	v_pk_mul_f32 v[102:103], v[56:57], v[8:9] op_sel_hi:[0,1]
	v_exp_f32_e32 v102, v102
	v_exp_f32_e32 v103, v103
	v_pk_mul_f32 v[64:65], v[64:65], v[140:141]
	v_pk_fma_f32 v[62:63], s[94:95], v[122:123], v[62:63]
	v_pk_fma_f32 v[124:125], v[58:59], s[64:65], v[64:65] op_sel_hi:[0, 1, 1]
	v_pk_mul_f32 v[64:65], v[102:103], v[142:143]
	v_pk_fma_f32 v[62:63], s[96:97], v[124:125], v[62:63]
	v_pk_fma_f32 v[126:127], v[58:59], s[66:67], v[64:65] op_sel_hi:[0, 1, 1]
	v_pk_mul_f32 v[64:65], v[56:57], v[2:3] op_sel_hi:[0,1]
	v_exp_f32_e32 v64, v64
	v_exp_f32_e32 v65, v65
	v_pk_mul_f32 v[102:103], v[56:57], v[4:5] op_sel_hi:[0,1]
	v_exp_f32_e32 v102, v102
	v_exp_f32_e32 v103, v103
	v_pk_mul_f32 v[64:65], v[64:65], v[144:145]
	v_pk_fma_f32 v[62:63], s[98:99], v[126:127], v[62:63]
	v_pk_fma_f32 v[128:129], v[58:59], s[68:69], v[64:65] op_sel_hi:[0, 1, 1]
	v_pk_mul_f32 v[54:55], v[102:103], v[54:55]
	v_pk_fma_f32 v[62:63], s[20:21], v[128:129], v[62:63]
	v_pk_fma_f32 v[130:131], v[58:59], s[70:71], v[54:55] op_sel_hi:[0, 1, 1]
	v_pk_fma_f32 v[54:55], s[22:23], v[130:131], v[62:63]
	s_nop 0
	v_add_f32_e32 v54, v54, v55
	v_fma_mix_f32 v54, v1, v57, v54 op_sel:[0,1,0] op_sel_hi:[0,1,0]
	v_fma_mixlo_f16 v54, v54, v61, 0 op_sel:[0,1,0] op_sel_hi:[0,1,0]
	ds_write_b16 v68, v54 offset:11376
	s_waitcnt lgkmcnt(0)
	s_load_dwordx16 s[56:71], s[54:55], 0x480
	s_load_dwordx8 s[88:95], s[54:55], 0x4c0
	s_load_dwordx4 s[96:99], s[54:55], 0x4e0
	s_load_dwordx4 s[20:23], s[54:55], 0x4f0
	s_waitcnt vmcnt(8)
	v_cvt_f32_f16_e32 v132, v50
	s_waitcnt vmcnt(7)
	v_cvt_f32_f16_e32 v69, v42
	v_pk_mul_f32 v[140:141], v[132:133], v[14:15] op_sel_hi:[0,1]
	v_exp_f32_e32 v140, v140
	v_exp_f32_e32 v141, v141
	v_pk_mul_f32 v[142:143], v[132:133], v[16:17] op_sel_hi:[0,1]
	v_exp_f32_e32 v142, v142
	v_exp_f32_e32 v143, v143
	v_mul_f32_e32 v138, v132, v69
	v_pk_mul_f32 v[140:141], v[140:141], v[148:149]
	v_pk_fma_f32 v[140:141], v[138:139], s[36:37], v[140:141] op_sel_hi:[0, 1, 1]
	v_pk_fma_f32 v[70:71], s[72:73], v[140:141], 0 op_sel_hi:[1, 1, 0]
	v_pk_mul_f32 v[86:87], v[142:143], v[134:135]
	s_nop 0
	v_pk_fma_f32 v[134:135], v[138:139], s[38:39], v[86:87] op_sel_hi:[0, 1, 1]
	v_pk_mul_f32 v[72:73], v[132:133], v[10:11] op_sel_hi:[0,1]
	v_exp_f32_e32 v72, v72
	v_exp_f32_e32 v73, v73
	v_pk_mul_f32 v[86:87], v[132:133], v[12:13] op_sel_hi:[0,1]
	v_exp_f32_e32 v86, v86
	v_exp_f32_e32 v87, v87
	v_pk_mul_f32 v[72:73], v[72:73], v[136:137]
	v_pk_fma_f32 v[70:71], s[74:75], v[134:135], v[70:71]
	v_pk_fma_f32 v[136:137], v[138:139], s[40:41], v[72:73] op_sel_hi:[0, 1, 1]
	v_pk_mul_f32 v[72:73], v[86:87], v[122:123]
	v_pk_mul_f32 v[74:75], v[132:133], v[8:9] op_sel_hi:[0,1]
	v_pk_fma_f32 v[122:123], v[138:139], s[42:43], v[72:73] op_sel_hi:[0, 1, 1]
	v_pk_mul_f32 v[72:73], v[132:133], v[6:7] op_sel_hi:[0,1]
	v_exp_f32_e32 v72, v72
	v_exp_f32_e32 v73, v73
	v_exp_f32_e32 v74, v74
	v_exp_f32_e32 v75, v75
	v_pk_fma_f32 v[70:71], s[76:77], v[136:137], v[70:71]
	v_pk_mul_f32 v[72:73], v[72:73], v[124:125]
	v_pk_fma_f32 v[70:71], s[78:79], v[122:123], v[70:71]
	v_pk_fma_f32 v[124:125], v[138:139], s[44:45], v[72:73] op_sel_hi:[0, 1, 1]
	v_pk_mul_f32 v[72:73], v[74:75], v[126:127]
	v_pk_mul_f32 v[74:75], v[132:133], v[4:5] op_sel_hi:[0,1]
	v_pk_fma_f32 v[126:127], v[138:139], s[46:47], v[72:73] op_sel_hi:[0, 1, 1]
	v_pk_mul_f32 v[72:73], v[132:133], v[2:3] op_sel_hi:[0,1]
	v_exp_f32_e32 v72, v72
	v_exp_f32_e32 v73, v73
	v_exp_f32_e32 v74, v74
	v_exp_f32_e32 v75, v75
	v_pk_fma_f32 v[70:71], s[80:81], v[124:125], v[70:71]
	v_pk_mul_f32 v[72:73], v[72:73], v[128:129]
	v_pk_fma_f32 v[70:71], s[82:83], v[126:127], v[70:71]
	v_pk_fma_f32 v[128:129], v[138:139], s[48:49], v[72:73] op_sel_hi:[0, 1, 1]
	v_pk_mul_f32 v[72:73], v[74:75], v[130:131]
	v_pk_fma_f32 v[70:71], s[84:85], v[128:129], v[70:71]
	v_pk_fma_f32 v[130:131], v[138:139], s[50:51], v[72:73] op_sel_hi:[0, 1, 1]
	v_pk_fma_f32 v[70:71], s[86:87], v[130:131], v[70:71]
	s_nop 0
	v_add_f32_e32 v69, v70, v71
	v_fma_mix_f32 v69, v1, v42, v69 op_sel_hi:[0,1,0]
	s_waitcnt vmcnt(6)
	v_fma_mixlo_f16 v69, v69, v46, 0 op_sel_hi:[0,1,0]
	ds_write_b16 v68, v69 offset:12416
	s_waitcnt lgkmcnt(0)
	s_load_dwordx16 s[36:51], s[54:55], 0x500
	s_load_dwordx16 s[72:87], s[54:55], 0x540
	v_cvt_f32_f16_sdwa v50, v50 dst_sel:DWORD dst_unused:UNUSED_PAD src0_sel:WORD_1
	v_cvt_f32_f16_sdwa v69, v42 dst_sel:DWORD dst_unused:UNUSED_PAD src0_sel:WORD_1
	v_pk_mul_f32 v[138:139], v[50:51], v[14:15] op_sel_hi:[0,1]
	v_exp_f32_e32 v138, v138
	v_exp_f32_e32 v139, v139
	v_pk_mul_f32 v[142:143], v[50:51], v[16:17] op_sel_hi:[0,1]
	v_exp_f32_e32 v142, v142
	v_exp_f32_e32 v143, v143
	v_mul_f32_e32 v132, v50, v69
	v_pk_mul_f32 v[138:139], v[138:139], v[140:141]
	v_pk_fma_f32 v[138:139], v[132:133], s[56:57], v[138:139] op_sel_hi:[0, 1, 1]
	v_pk_fma_f32 v[54:55], s[88:89], v[138:139], 0 op_sel_hi:[1, 1, 0]
	v_pk_mul_f32 v[106:107], v[142:143], v[134:135]
	s_nop 0
	v_pk_fma_f32 v[134:135], v[132:133], s[58:59], v[106:107] op_sel_hi:[0, 1, 1]
	v_pk_mul_f32 v[56:57], v[50:51], v[10:11] op_sel_hi:[0,1]
	v_exp_f32_e32 v56, v56
	v_exp_f32_e32 v57, v57
	v_pk_mul_f32 v[106:107], v[50:51], v[12:13] op_sel_hi:[0,1]
	v_exp_f32_e32 v106, v106
	v_exp_f32_e32 v107, v107
	v_pk_mul_f32 v[56:57], v[56:57], v[136:137]
	v_pk_fma_f32 v[54:55], s[90:91], v[134:135], v[54:55]
	v_pk_fma_f32 v[136:137], v[132:133], s[60:61], v[56:57] op_sel_hi:[0, 1, 1]
	v_pk_mul_f32 v[56:57], v[106:107], v[122:123]
	v_pk_mul_f32 v[58:59], v[50:51], v[8:9] op_sel_hi:[0,1]
	v_pk_fma_f32 v[122:123], v[132:133], s[62:63], v[56:57] op_sel_hi:[0, 1, 1]
	v_pk_mul_f32 v[56:57], v[50:51], v[6:7] op_sel_hi:[0,1]
	v_exp_f32_e32 v56, v56
	v_exp_f32_e32 v57, v57
	v_exp_f32_e32 v58, v58
	v_exp_f32_e32 v59, v59
	v_pk_fma_f32 v[54:55], s[92:93], v[136:137], v[54:55]
	v_pk_mul_f32 v[56:57], v[56:57], v[124:125]
	v_pk_fma_f32 v[54:55], s[94:95], v[122:123], v[54:55]
	v_pk_fma_f32 v[124:125], v[132:133], s[64:65], v[56:57] op_sel_hi:[0, 1, 1]
	v_pk_mul_f32 v[56:57], v[58:59], v[126:127]
	v_pk_mul_f32 v[58:59], v[50:51], v[4:5] op_sel_hi:[0,1]
	v_pk_fma_f32 v[126:127], v[132:133], s[66:67], v[56:57] op_sel_hi:[0, 1, 1]
	v_pk_mul_f32 v[56:57], v[50:51], v[2:3] op_sel_hi:[0,1]
	v_exp_f32_e32 v56, v56
	v_exp_f32_e32 v57, v57
	v_exp_f32_e32 v58, v58
	v_exp_f32_e32 v59, v59
	v_pk_fma_f32 v[54:55], s[96:97], v[124:125], v[54:55]
	v_pk_mul_f32 v[56:57], v[56:57], v[128:129]
	v_pk_fma_f32 v[54:55], s[98:99], v[126:127], v[54:55]
	v_pk_fma_f32 v[128:129], v[132:133], s[68:69], v[56:57] op_sel_hi:[0, 1, 1]
	v_pk_mul_f32 v[56:57], v[58:59], v[130:131]
	v_pk_fma_f32 v[54:55], s[20:21], v[128:129], v[54:55]
	v_pk_fma_f32 v[130:131], v[132:133], s[70:71], v[56:57] op_sel_hi:[0, 1, 1]
	v_pk_fma_f32 v[54:55], s[22:23], v[130:131], v[54:55]
	s_nop 0
	v_add_f32_e32 v50, v54, v55
	v_fma_mix_f32 v42, v1, v42, v50 op_sel:[0,1,0] op_sel_hi:[0,1,0]
	v_fma_mixlo_f16 v42, v42, v46, 0 op_sel:[0,1,0] op_sel_hi:[0,1,0]
	ds_write_b16 v68, v42 offset:13456
	s_waitcnt lgkmcnt(0)
	s_load_dwordx16 s[56:71], s[54:55], 0x580
	s_load_dwordx8 s[88:95], s[54:55], 0x5c0
	s_load_dwordx4 s[96:99], s[54:55], 0x5e0
	s_load_dwordx4 s[20:23], s[54:55], 0x5f0
	v_cvt_f32_f16_e32 v42, v51
	v_cvt_f32_f16_e32 v46, v43
	v_pk_mul_f32 v[132:133], v[42:43], v[14:15] op_sel_hi:[0,1]
	v_exp_f32_e32 v132, v132
	v_exp_f32_e32 v133, v133
	v_pk_mul_f32 v[140:141], v[42:43], v[16:17] op_sel_hi:[0,1]
	v_exp_f32_e32 v140, v140
	v_exp_f32_e32 v141, v141
	v_mul_f32_e32 v46, v42, v46
	v_pk_mul_f32 v[132:133], v[132:133], v[138:139]
	v_pk_fma_f32 v[132:133], v[46:47], s[36:37], v[132:133] op_sel_hi:[0, 1, 1]
	v_pk_fma_f32 v[70:71], s[72:73], v[132:133], 0 op_sel_hi:[1, 1, 0]
	v_pk_mul_f32 v[86:87], v[140:141], v[134:135]
	s_nop 0
	v_pk_fma_f32 v[134:135], v[46:47], s[38:39], v[86:87] op_sel_hi:[0, 1, 1]
	v_pk_mul_f32 v[72:73], v[42:43], v[10:11] op_sel_hi:[0,1]
	v_exp_f32_e32 v72, v72
	v_exp_f32_e32 v73, v73
	v_pk_mul_f32 v[86:87], v[42:43], v[12:13] op_sel_hi:[0,1]
	v_exp_f32_e32 v86, v86
	v_exp_f32_e32 v87, v87
	v_pk_mul_f32 v[72:73], v[72:73], v[136:137]
	v_pk_fma_f32 v[70:71], s[74:75], v[134:135], v[70:71]
	v_pk_fma_f32 v[136:137], v[46:47], s[40:41], v[72:73] op_sel_hi:[0, 1, 1]
	v_pk_mul_f32 v[72:73], v[86:87], v[122:123]
	v_pk_mul_f32 v[74:75], v[42:43], v[8:9] op_sel_hi:[0,1]
	v_pk_fma_f32 v[122:123], v[46:47], s[42:43], v[72:73] op_sel_hi:[0, 1, 1]
	v_pk_mul_f32 v[72:73], v[42:43], v[6:7] op_sel_hi:[0,1]
	v_exp_f32_e32 v72, v72
	v_exp_f32_e32 v73, v73
	v_exp_f32_e32 v74, v74
	v_exp_f32_e32 v75, v75
	v_pk_fma_f32 v[70:71], s[76:77], v[136:137], v[70:71]
	v_pk_mul_f32 v[72:73], v[72:73], v[124:125]
	v_pk_fma_f32 v[70:71], s[78:79], v[122:123], v[70:71]
	v_pk_fma_f32 v[124:125], v[46:47], s[44:45], v[72:73] op_sel_hi:[0, 1, 1]
	v_pk_mul_f32 v[72:73], v[74:75], v[126:127]
	v_pk_mul_f32 v[74:75], v[42:43], v[4:5] op_sel_hi:[0,1]
	v_pk_fma_f32 v[126:127], v[46:47], s[46:47], v[72:73] op_sel_hi:[0, 1, 1]
	v_pk_mul_f32 v[72:73], v[42:43], v[2:3] op_sel_hi:[0,1]
	v_exp_f32_e32 v72, v72
	v_exp_f32_e32 v73, v73
	v_exp_f32_e32 v74, v74
	v_exp_f32_e32 v75, v75
	v_pk_fma_f32 v[70:71], s[80:81], v[124:125], v[70:71]
	v_pk_mul_f32 v[72:73], v[72:73], v[128:129]
	v_pk_fma_f32 v[70:71], s[82:83], v[126:127], v[70:71]
	v_pk_fma_f32 v[128:129], v[46:47], s[48:49], v[72:73] op_sel_hi:[0, 1, 1]
	v_pk_mul_f32 v[72:73], v[74:75], v[130:131]
	v_pk_fma_f32 v[70:71], s[84:85], v[128:129], v[70:71]
	v_pk_fma_f32 v[130:131], v[46:47], s[50:51], v[72:73] op_sel_hi:[0, 1, 1]
	v_pk_fma_f32 v[70:71], s[86:87], v[130:131], v[70:71]
	s_nop 0
	v_add_f32_e32 v42, v70, v71
	v_fma_mix_f32 v42, v1, v43, v42 op_sel_hi:[0,1,0]
	v_fma_mixlo_f16 v42, v42, v47, 0 op_sel_hi:[0,1,0]
	ds_write_b16 v68, v42 offset:14496
	s_waitcnt lgkmcnt(0)
	s_load_dwordx16 s[36:51], s[54:55], 0x600
	s_load_dwordx16 s[72:87], s[54:55], 0x640
	v_cvt_f32_f16_sdwa v42, v51 dst_sel:DWORD dst_unused:UNUSED_PAD src0_sel:WORD_1
	v_cvt_f32_f16_sdwa v46, v43 dst_sel:DWORD dst_unused:UNUSED_PAD src0_sel:WORD_1
	v_pk_mul_f32 v[50:51], v[42:43], v[14:15] op_sel_hi:[0,1]
	v_exp_f32_e32 v50, v50
	v_exp_f32_e32 v51, v51
	v_pk_mul_f32 v[138:139], v[42:43], v[16:17] op_sel_hi:[0,1]
	v_exp_f32_e32 v138, v138
	v_exp_f32_e32 v139, v139
	v_mul_f32_e32 v46, v42, v46
	v_pk_mul_f32 v[50:51], v[50:51], v[132:133]
	v_pk_fma_f32 v[50:51], v[46:47], s[56:57], v[50:51] op_sel_hi:[0, 1, 1]
	v_pk_fma_f32 v[54:55], s[88:89], v[50:51], 0 op_sel_hi:[1, 1, 0]
	v_pk_mul_f32 v[106:107], v[138:139], v[134:135]
	s_nop 0
	v_pk_fma_f32 v[132:133], v[46:47], s[58:59], v[106:107] op_sel_hi:[0, 1, 1]
	v_pk_mul_f32 v[56:57], v[42:43], v[10:11] op_sel_hi:[0,1]
	v_exp_f32_e32 v56, v56
	v_exp_f32_e32 v57, v57
	v_pk_mul_f32 v[106:107], v[42:43], v[12:13] op_sel_hi:[0,1]
	v_exp_f32_e32 v106, v106
	v_exp_f32_e32 v107, v107
	v_pk_mul_f32 v[56:57], v[56:57], v[136:137]
	v_pk_fma_f32 v[54:55], s[90:91], v[132:133], v[54:55]
	v_pk_fma_f32 v[134:135], v[46:47], s[60:61], v[56:57] op_sel_hi:[0, 1, 1]
	v_pk_mul_f32 v[56:57], v[106:107], v[122:123]
	v_pk_mul_f32 v[58:59], v[42:43], v[8:9] op_sel_hi:[0,1]
	v_pk_fma_f32 v[122:123], v[46:47], s[62:63], v[56:57] op_sel_hi:[0, 1, 1]
	v_pk_mul_f32 v[56:57], v[42:43], v[6:7] op_sel_hi:[0,1]
	v_exp_f32_e32 v56, v56
	v_exp_f32_e32 v57, v57
	v_exp_f32_e32 v58, v58
	v_exp_f32_e32 v59, v59
	v_pk_fma_f32 v[54:55], s[92:93], v[134:135], v[54:55]
	v_pk_mul_f32 v[56:57], v[56:57], v[124:125]
	v_pk_fma_f32 v[54:55], s[94:95], v[122:123], v[54:55]
	v_pk_fma_f32 v[124:125], v[46:47], s[64:65], v[56:57] op_sel_hi:[0, 1, 1]
	v_pk_mul_f32 v[56:57], v[58:59], v[126:127]
	v_pk_mul_f32 v[58:59], v[42:43], v[4:5] op_sel_hi:[0,1]
	v_pk_fma_f32 v[126:127], v[46:47], s[66:67], v[56:57] op_sel_hi:[0, 1, 1]
	v_pk_mul_f32 v[56:57], v[42:43], v[2:3] op_sel_hi:[0,1]
	v_exp_f32_e32 v56, v56
	v_exp_f32_e32 v57, v57
	v_exp_f32_e32 v58, v58
	v_exp_f32_e32 v59, v59
	v_pk_fma_f32 v[54:55], s[96:97], v[124:125], v[54:55]
	v_pk_mul_f32 v[56:57], v[56:57], v[128:129]
	v_pk_fma_f32 v[54:55], s[98:99], v[126:127], v[54:55]
	v_pk_fma_f32 v[128:129], v[46:47], s[68:69], v[56:57] op_sel_hi:[0, 1, 1]
	v_pk_mul_f32 v[56:57], v[58:59], v[130:131]
	v_pk_fma_f32 v[54:55], s[20:21], v[128:129], v[54:55]
	v_pk_fma_f32 v[130:131], v[46:47], s[70:71], v[56:57] op_sel_hi:[0, 1, 1]
	v_pk_fma_f32 v[54:55], s[22:23], v[130:131], v[54:55]
	s_nop 0
	v_add_f32_e32 v42, v54, v55
	v_fma_mix_f32 v42, v1, v43, v42 op_sel:[0,1,0] op_sel_hi:[0,1,0]
	v_fma_mixlo_f16 v42, v42, v47, 0 op_sel:[0,1,0] op_sel_hi:[0,1,0]
	ds_write_b16 v68, v42 offset:15536
	s_waitcnt lgkmcnt(0)
	s_load_dwordx16 s[56:71], s[54:55], 0x680
	s_load_dwordx8 s[88:95], s[54:55], 0x6c0
	s_load_dwordx4 s[96:99], s[54:55], 0x6e0
	s_load_dwordx4 s[20:23], s[54:55], 0x6f0
	v_cvt_f32_f16_e32 v42, v52
	v_cvt_f32_f16_e32 v43, v44
	v_pk_mul_f32 v[136:137], v[42:43], v[14:15] op_sel_hi:[0,1]
	v_exp_f32_e32 v136, v136
	v_exp_f32_e32 v137, v137
	v_pk_mul_f32 v[138:139], v[42:43], v[16:17] op_sel_hi:[0,1]
	v_exp_f32_e32 v138, v138
	v_exp_f32_e32 v139, v139
	v_mul_f32_e32 v46, v42, v43
	v_pk_mul_f32 v[50:51], v[136:137], v[50:51]
	v_pk_fma_f32 v[50:51], v[46:47], s[36:37], v[50:51] op_sel_hi:[0, 1, 1]
	v_pk_fma_f32 v[70:71], s[72:73], v[50:51], 0 op_sel_hi:[1, 1, 0]
	v_pk_mul_f32 v[86:87], v[138:139], v[132:133]
	s_nop 0
	v_pk_fma_f32 v[132:133], v[46:47], s[38:39], v[86:87] op_sel_hi:[0, 1, 1]
	v_pk_mul_f32 v[72:73], v[42:43], v[10:11] op_sel_hi:[0,1]
	v_exp_f32_e32 v72, v72
	v_exp_f32_e32 v73, v73
	v_pk_mul_f32 v[86:87], v[42:43], v[12:13] op_sel_hi:[0,1]
	v_exp_f32_e32 v86, v86
	v_exp_f32_e32 v87, v87
	v_pk_mul_f32 v[72:73], v[72:73], v[134:135]
	v_pk_fma_f32 v[70:71], s[74:75], v[132:133], v[70:71]
	v_pk_fma_f32 v[134:135], v[46:47], s[40:41], v[72:73] op_sel_hi:[0, 1, 1]
	v_pk_mul_f32 v[72:73], v[86:87], v[122:123]
	v_pk_mul_f32 v[74:75], v[42:43], v[8:9] op_sel_hi:[0,1]
	v_pk_fma_f32 v[122:123], v[46:47], s[42:43], v[72:73] op_sel_hi:[0, 1, 1]
	v_pk_mul_f32 v[72:73], v[42:43], v[6:7] op_sel_hi:[0,1]
	v_exp_f32_e32 v72, v72
	v_exp_f32_e32 v73, v73
	v_exp_f32_e32 v74, v74
	v_exp_f32_e32 v75, v75
	v_pk_fma_f32 v[70:71], s[76:77], v[134:135], v[70:71]
	v_pk_mul_f32 v[72:73], v[72:73], v[124:125]
	v_pk_fma_f32 v[70:71], s[78:79], v[122:123], v[70:71]
	v_pk_fma_f32 v[124:125], v[46:47], s[44:45], v[72:73] op_sel_hi:[0, 1, 1]
	v_pk_mul_f32 v[72:73], v[74:75], v[126:127]
	v_pk_fma_f32 v[70:71], s[80:81], v[124:125], v[70:71]
	v_pk_fma_f32 v[126:127], v[46:47], s[46:47], v[72:73] op_sel_hi:[0, 1, 1]
	v_pk_mul_f32 v[72:73], v[42:43], v[2:3] op_sel_hi:[0,1]
	v_exp_f32_e32 v72, v72
	v_exp_f32_e32 v73, v73
	v_pk_mul_f32 v[42:43], v[42:43], v[4:5] op_sel_hi:[0,1]
	v_exp_f32_e32 v42, v42
	v_exp_f32_e32 v43, v43
	v_pk_mul_f32 v[72:73], v[72:73], v[128:129]
	v_pk_fma_f32 v[70:71], s[82:83], v[126:127], v[70:71]
	v_pk_fma_f32 v[128:129], v[46:47], s[48:49], v[72:73] op_sel_hi:[0, 1, 1]
	v_pk_mul_f32 v[42:43], v[42:43], v[130:131]
	v_pk_fma_f32 v[70:71], s[84:85], v[128:129], v[70:71]
	v_pk_fma_f32 v[42:43], v[46:47], s[50:51], v[42:43] op_sel_hi:[0, 1, 1]
	v_pk_fma_f32 v[46:47], s[86:87], v[42:43], v[70:71]
	s_nop 0
	v_add_f32_e32 v46, v46, v47
	v_fma_mix_f32 v46, v1, v44, v46 op_sel_hi:[0,1,0]
	v_fma_mixlo_f16 v46, v46, v48, 0 op_sel_hi:[0,1,0]
	ds_write_b16 v68, v46 offset:16576
	s_waitcnt lgkmcnt(0)
	s_load_dwordx16 s[36:51], s[54:55], 0x700
	s_load_dwordx16 s[72:87], s[54:55], 0x740
	v_cvt_f32_f16_sdwa v46, v52 dst_sel:DWORD dst_unused:UNUSED_PAD src0_sel:WORD_1
	v_cvt_f32_f16_sdwa v47, v44 dst_sel:DWORD dst_unused:UNUSED_PAD src0_sel:WORD_1
	v_pk_mul_f32 v[130:131], v[46:47], v[14:15] op_sel_hi:[0,1]
	v_exp_f32_e32 v130, v130
	v_exp_f32_e32 v131, v131
	v_pk_mul_f32 v[136:137], v[46:47], v[16:17] op_sel_hi:[0,1]
	v_exp_f32_e32 v136, v136
	v_exp_f32_e32 v137, v137
	v_mul_f32_e32 v52, v46, v47
	v_pk_mul_f32 v[50:51], v[130:131], v[50:51]
	v_pk_fma_f32 v[50:51], v[52:53], s[56:57], v[50:51] op_sel_hi:[0, 1, 1]
	v_pk_fma_f32 v[54:55], s[88:89], v[50:51], 0 op_sel_hi:[1, 1, 0]
	v_pk_mul_f32 v[106:107], v[136:137], v[132:133]
	s_nop 0
	v_pk_fma_f32 v[130:131], v[52:53], s[58:59], v[106:107] op_sel_hi:[0, 1, 1]
	v_pk_mul_f32 v[56:57], v[46:47], v[10:11] op_sel_hi:[0,1]
	v_exp_f32_e32 v56, v56
	v_exp_f32_e32 v57, v57
	v_pk_mul_f32 v[106:107], v[46:47], v[12:13] op_sel_hi:[0,1]
	v_exp_f32_e32 v106, v106
	v_exp_f32_e32 v107, v107
	v_pk_mul_f32 v[56:57], v[56:57], v[134:135]
	v_pk_fma_f32 v[54:55], s[90:91], v[130:131], v[54:55]
	v_pk_fma_f32 v[132:133], v[52:53], s[60:61], v[56:57] op_sel_hi:[0, 1, 1]
	v_pk_mul_f32 v[56:57], v[106:107], v[122:123]
	v_pk_mul_f32 v[58:59], v[46:47], v[8:9] op_sel_hi:[0,1]
	v_pk_fma_f32 v[122:123], v[52:53], s[62:63], v[56:57] op_sel_hi:[0, 1, 1]
	v_pk_mul_f32 v[56:57], v[46:47], v[6:7] op_sel_hi:[0,1]
	v_exp_f32_e32 v56, v56
	v_exp_f32_e32 v57, v57
	v_exp_f32_e32 v58, v58
	v_exp_f32_e32 v59, v59
	v_pk_fma_f32 v[54:55], s[92:93], v[132:133], v[54:55]
	v_pk_mul_f32 v[56:57], v[56:57], v[124:125]
	v_pk_fma_f32 v[54:55], s[94:95], v[122:123], v[54:55]
	v_pk_fma_f32 v[124:125], v[52:53], s[64:65], v[56:57] op_sel_hi:[0, 1, 1]
	v_pk_mul_f32 v[56:57], v[58:59], v[126:127]
	v_pk_fma_f32 v[54:55], s[96:97], v[124:125], v[54:55]
	v_pk_fma_f32 v[126:127], v[52:53], s[66:67], v[56:57] op_sel_hi:[0, 1, 1]
	v_pk_mul_f32 v[56:57], v[46:47], v[2:3] op_sel_hi:[0,1]
	v_exp_f32_e32 v56, v56
	v_exp_f32_e32 v57, v57
	v_pk_mul_f32 v[46:47], v[46:47], v[4:5] op_sel_hi:[0,1]
	v_exp_f32_e32 v46, v46
	v_exp_f32_e32 v47, v47
	v_pk_mul_f32 v[56:57], v[56:57], v[128:129]
	v_pk_fma_f32 v[54:55], s[98:99], v[126:127], v[54:55]
	v_pk_fma_f32 v[128:129], v[52:53], s[68:69], v[56:57] op_sel_hi:[0, 1, 1]
	v_pk_mul_f32 v[42:43], v[46:47], v[42:43]
	v_pk_fma_f32 v[54:55], s[20:21], v[128:129], v[54:55]
	v_pk_fma_f32 v[42:43], v[52:53], s[70:71], v[42:43] op_sel_hi:[0, 1, 1]
	v_pk_fma_f32 v[46:47], s[22:23], v[42:43], v[54:55]
	s_nop 0
	v_add_f32_e32 v46, v46, v47
	v_fma_mix_f32 v44, v1, v44, v46 op_sel:[0,1,0] op_sel_hi:[0,1,0]
	v_fma_mixlo_f16 v44, v44, v48, 0 op_sel:[0,1,0] op_sel_hi:[0,1,0]
	ds_write_b16 v68, v44 offset:17616
	s_waitcnt lgkmcnt(0)
	s_load_dwordx16 s[56:71], s[54:55], 0x780
	s_load_dwordx8 s[88:95], s[54:55], 0x7c0
	s_load_dwordx4 s[96:99], s[54:55], 0x7e0
	s_load_dwordx4 s[20:23], s[54:55], 0x7f0
	v_cvt_f32_f16_e32 v44, v53
	v_cvt_f32_f16_e32 v46, v45
	v_pk_mul_f32 v[134:135], v[44:45], v[14:15] op_sel_hi:[0,1]
	v_exp_f32_e32 v134, v134
	v_exp_f32_e32 v135, v135
	v_pk_mul_f32 v[136:137], v[44:45], v[16:17] op_sel_hi:[0,1]
	v_exp_f32_e32 v136, v136
	v_exp_f32_e32 v137, v137
	v_mul_f32_e32 v46, v44, v46
	v_pk_mul_f32 v[50:51], v[134:135], v[50:51]
	v_pk_fma_f32 v[50:51], v[46:47], s[36:37], v[50:51] op_sel_hi:[0, 1, 1]
	v_pk_fma_f32 v[70:71], s[72:73], v[50:51], 0 op_sel_hi:[1, 1, 0]
	v_pk_mul_f32 v[86:87], v[136:137], v[130:131]
	s_nop 0
	v_pk_fma_f32 v[130:131], v[46:47], s[38:39], v[86:87] op_sel_hi:[0, 1, 1]
	v_pk_mul_f32 v[72:73], v[44:45], v[10:11] op_sel_hi:[0,1]
	v_exp_f32_e32 v72, v72
	v_exp_f32_e32 v73, v73
	v_pk_mul_f32 v[86:87], v[44:45], v[12:13] op_sel_hi:[0,1]
	v_exp_f32_e32 v86, v86
	v_exp_f32_e32 v87, v87
	v_pk_mul_f32 v[72:73], v[72:73], v[132:133]
	v_pk_fma_f32 v[70:71], s[74:75], v[130:131], v[70:71]
	v_pk_fma_f32 v[132:133], v[46:47], s[40:41], v[72:73] op_sel_hi:[0, 1, 1]
	v_pk_mul_f32 v[72:73], v[86:87], v[122:123]
	v_pk_mul_f32 v[74:75], v[44:45], v[8:9] op_sel_hi:[0,1]
	v_pk_fma_f32 v[122:123], v[46:47], s[42:43], v[72:73] op_sel_hi:[0, 1, 1]
	v_pk_mul_f32 v[72:73], v[44:45], v[6:7] op_sel_hi:[0,1]
	v_exp_f32_e32 v72, v72
	v_exp_f32_e32 v73, v73
	v_exp_f32_e32 v74, v74
	v_exp_f32_e32 v75, v75
	v_pk_fma_f32 v[70:71], s[76:77], v[132:133], v[70:71]
	v_pk_mul_f32 v[72:73], v[72:73], v[124:125]
	v_pk_fma_f32 v[70:71], s[78:79], v[122:123], v[70:71]
	v_pk_fma_f32 v[124:125], v[46:47], s[44:45], v[72:73] op_sel_hi:[0, 1, 1]
	v_pk_mul_f32 v[72:73], v[74:75], v[126:127]
	v_pk_mul_f32 v[74:75], v[44:45], v[4:5] op_sel_hi:[0,1]
	v_pk_fma_f32 v[126:127], v[46:47], s[46:47], v[72:73] op_sel_hi:[0, 1, 1]
	v_pk_mul_f32 v[72:73], v[44:45], v[2:3] op_sel_hi:[0,1]
	v_exp_f32_e32 v72, v72
	v_exp_f32_e32 v73, v73
	v_exp_f32_e32 v74, v74
	v_exp_f32_e32 v75, v75
	v_pk_fma_f32 v[70:71], s[80:81], v[124:125], v[70:71]
	v_pk_mul_f32 v[72:73], v[72:73], v[128:129]
	v_pk_fma_f32 v[70:71], s[82:83], v[126:127], v[70:71]
	v_pk_fma_f32 v[128:129], v[46:47], s[48:49], v[72:73] op_sel_hi:[0, 1, 1]
	v_pk_mul_f32 v[42:43], v[74:75], v[42:43]
	v_pk_fma_f32 v[70:71], s[84:85], v[128:129], v[70:71]
	v_pk_fma_f32 v[42:43], v[46:47], s[50:51], v[42:43] op_sel_hi:[0, 1, 1]
	v_pk_fma_f32 v[46:47], s[86:87], v[42:43], v[70:71]
	s_nop 0
	v_add_f32_e32 v44, v46, v47
	v_fma_mix_f32 v44, v1, v45, v44 op_sel_hi:[0,1,0]
	v_fma_mixlo_f16 v44, v44, v49, 0 op_sel_hi:[0,1,0]
	ds_write_b16 v68, v44 offset:18656
	s_waitcnt lgkmcnt(0)
	s_load_dwordx16 s[36:51], s[54:55], 0x800
	s_load_dwordx16 s[72:87], s[54:55], 0x840
	v_cvt_f32_f16_sdwa v44, v53 dst_sel:DWORD dst_unused:UNUSED_PAD src0_sel:WORD_1
	v_cvt_f32_f16_sdwa v46, v45 dst_sel:DWORD dst_unused:UNUSED_PAD src0_sel:WORD_1
	v_pk_mul_f32 v[52:53], v[44:45], v[14:15] op_sel_hi:[0,1]
	v_pk_mul_f32 v[134:135], v[44:45], v[16:17] op_sel_hi:[0,1]
	v_exp_f32_e32 v52, v52
	v_exp_f32_e32 v53, v53
	v_exp_f32_e32 v134, v134
	v_exp_f32_e32 v135, v135
	v_mul_f32_e32 v46, v44, v46
	v_pk_mul_f32 v[50:51], v[52:53], v[50:51]
	v_pk_mul_f32 v[52:53], v[134:135], v[130:131]
	v_pk_fma_f32 v[130:131], v[46:47], s[58:59], v[52:53] op_sel_hi:[0, 1, 1]
	v_pk_mul_f32 v[52:53], v[44:45], v[10:11] op_sel_hi:[0,1]
	v_pk_fma_f32 v[136:137], v[46:47], s[56:57], v[50:51] op_sel_hi:[0, 1, 1]
	v_exp_f32_e32 v52, v52
	v_exp_f32_e32 v53, v53
	v_pk_mul_f32 v[54:55], v[44:45], v[12:13] op_sel_hi:[0,1]
	v_exp_f32_e32 v54, v54
	v_exp_f32_e32 v55, v55
	v_pk_fma_f32 v[50:51], s[88:89], v[136:137], 0 op_sel_hi:[1, 1, 0]
	v_pk_mul_f32 v[52:53], v[52:53], v[132:133]
	v_pk_fma_f32 v[50:51], s[90:91], v[130:131], v[50:51]
	v_pk_fma_f32 v[132:133], v[46:47], s[60:61], v[52:53] op_sel_hi:[0, 1, 1]
	v_pk_mul_f32 v[52:53], v[54:55], v[122:123]
	v_pk_fma_f32 v[50:51], s[92:93], v[132:133], v[50:51]
	v_pk_fma_f32 v[110:111], v[46:47], s[62:63], v[52:53] op_sel_hi:[0, 1, 1]
	v_pk_mul_f32 v[52:53], v[44:45], v[6:7] op_sel_hi:[0,1]
	v_exp_f32_e32 v52, v52
	v_exp_f32_e32 v53, v53
	v_pk_mul_f32 v[54:55], v[44:45], v[8:9] op_sel_hi:[0,1]
	v_exp_f32_e32 v54, v54
	v_exp_f32_e32 v55, v55
	v_pk_mul_f32 v[52:53], v[52:53], v[124:125]
	v_pk_fma_f32 v[50:51], s[94:95], v[110:111], v[50:51]
	v_pk_fma_f32 v[112:113], v[46:47], s[64:65], v[52:53] op_sel_hi:[0, 1, 1]
	v_pk_mul_f32 v[52:53], v[54:55], v[126:127]
	v_pk_fma_f32 v[50:51], s[96:97], v[112:113], v[50:51]
	v_pk_fma_f32 v[114:115], v[46:47], s[66:67], v[52:53] op_sel_hi:[0, 1, 1]
	v_pk_mul_f32 v[52:53], v[44:45], v[2:3] op_sel_hi:[0,1]
	v_exp_f32_e32 v52, v52
	v_exp_f32_e32 v53, v53
	v_pk_mul_f32 v[54:55], v[44:45], v[4:5] op_sel_hi:[0,1]
	v_exp_f32_e32 v54, v54
	v_exp_f32_e32 v55, v55
	v_pk_mul_f32 v[52:53], v[52:53], v[128:129]
	v_pk_fma_f32 v[50:51], s[98:99], v[114:115], v[50:51]
	v_pk_fma_f32 v[116:117], v[46:47], s[68:69], v[52:53] op_sel_hi:[0, 1, 1]
	v_pk_mul_f32 v[42:43], v[54:55], v[42:43]
	v_pk_fma_f32 v[50:51], s[20:21], v[116:117], v[50:51]
	v_pk_fma_f32 v[118:119], v[46:47], s[70:71], v[42:43] op_sel_hi:[0, 1, 1]
	v_pk_fma_f32 v[42:43], s[22:23], v[118:119], v[50:51]
	s_nop 0
	v_add_f32_e32 v42, v42, v43
	v_fma_mix_f32 v42, v1, v45, v42 op_sel:[0,1,0] op_sel_hi:[0,1,0]
	v_fma_mixlo_f16 v42, v42, v49, 0 op_sel:[0,1,0] op_sel_hi:[0,1,0]
	ds_write_b16 v68, v42 offset:19696
	s_waitcnt lgkmcnt(0)
	s_load_dwordx16 s[56:71], s[54:55], 0x880
	s_load_dwordx8 s[88:95], s[54:55], 0x8c0
	s_load_dwordx4 s[96:99], s[54:55], 0x8e0
	s_load_dwordx4 s[20:23], s[54:55], 0x8f0
	s_waitcnt vmcnt(5)
	v_cvt_f32_f16_e32 v120, v38
	s_waitcnt vmcnt(4)
	v_cvt_f32_f16_e32 v69, v30
	v_pk_mul_f32 v[124:125], v[120:121], v[14:15] op_sel_hi:[0,1]
	v_exp_f32_e32 v124, v124
	v_exp_f32_e32 v125, v125
	v_pk_mul_f32 v[126:127], v[120:121], v[16:17] op_sel_hi:[0,1]
	v_exp_f32_e32 v126, v126
	v_exp_f32_e32 v127, v127
	v_mul_f32_e32 v122, v120, v69
	v_pk_mul_f32 v[124:125], v[124:125], v[136:137]
	v_pk_fma_f32 v[124:125], v[122:123], s[36:37], v[124:125] op_sel_hi:[0, 1, 1]
	v_pk_fma_f32 v[70:71], s[72:73], v[124:125], 0 op_sel_hi:[1, 1, 0]
	v_pk_mul_f32 v[86:87], v[126:127], v[130:131]
	s_nop 0
	v_pk_fma_f32 v[126:127], v[122:123], s[38:39], v[86:87] op_sel_hi:[0, 1, 1]
	v_pk_mul_f32 v[72:73], v[120:121], v[10:11] op_sel_hi:[0,1]
	v_exp_f32_e32 v72, v72
	v_exp_f32_e32 v73, v73
	v_pk_mul_f32 v[86:87], v[120:121], v[12:13] op_sel_hi:[0,1]
	v_exp_f32_e32 v86, v86
	v_exp_f32_e32 v87, v87
	v_pk_mul_f32 v[72:73], v[72:73], v[132:133]
	v_pk_fma_f32 v[70:71], s[74:75], v[126:127], v[70:71]
	v_pk_fma_f32 v[128:129], v[122:123], s[40:41], v[72:73] op_sel_hi:[0, 1, 1]
	v_pk_mul_f32 v[72:73], v[86:87], v[110:111]
	v_pk_mul_f32 v[74:75], v[120:121], v[8:9] op_sel_hi:[0,1]
	v_pk_fma_f32 v[110:111], v[122:123], s[42:43], v[72:73] op_sel_hi:[0, 1, 1]
	v_pk_mul_f32 v[72:73], v[120:121], v[6:7] op_sel_hi:[0,1]
	v_exp_f32_e32 v72, v72
	v_exp_f32_e32 v73, v73
	v_exp_f32_e32 v74, v74
	v_exp_f32_e32 v75, v75
	v_pk_fma_f32 v[70:71], s[76:77], v[128:129], v[70:71]
	v_pk_mul_f32 v[72:73], v[72:73], v[112:113]
	v_pk_fma_f32 v[70:71], s[78:79], v[110:111], v[70:71]
	v_pk_fma_f32 v[112:113], v[122:123], s[44:45], v[72:73] op_sel_hi:[0, 1, 1]
	v_pk_mul_f32 v[72:73], v[74:75], v[114:115]
	v_pk_mul_f32 v[74:75], v[120:121], v[4:5] op_sel_hi:[0,1]
	v_pk_fma_f32 v[114:115], v[122:123], s[46:47], v[72:73] op_sel_hi:[0, 1, 1]
	v_pk_mul_f32 v[72:73], v[120:121], v[2:3] op_sel_hi:[0,1]
	v_exp_f32_e32 v72, v72
	v_exp_f32_e32 v73, v73
	v_exp_f32_e32 v74, v74
	v_exp_f32_e32 v75, v75
	v_pk_fma_f32 v[70:71], s[80:81], v[112:113], v[70:71]
	v_pk_mul_f32 v[72:73], v[72:73], v[116:117]
	v_pk_fma_f32 v[70:71], s[82:83], v[114:115], v[70:71]
	v_pk_fma_f32 v[116:117], v[122:123], s[48:49], v[72:73] op_sel_hi:[0, 1, 1]
	v_pk_mul_f32 v[72:73], v[74:75], v[118:119]
	v_pk_fma_f32 v[70:71], s[84:85], v[116:117], v[70:71]
	v_pk_fma_f32 v[118:119], v[122:123], s[50:51], v[72:73] op_sel_hi:[0, 1, 1]
	v_pk_fma_f32 v[70:71], s[86:87], v[118:119], v[70:71]
	s_nop 0
	v_add_f32_e32 v69, v70, v71
	v_fma_mix_f32 v69, v1, v30, v69 op_sel_hi:[0,1,0]
	s_waitcnt vmcnt(3)
	v_fma_mixlo_f16 v69, v69, v34, 0 op_sel_hi:[0,1,0]
	ds_write_b16 v68, v69 offset:20736
	s_waitcnt lgkmcnt(0)
	s_load_dwordx16 s[36:51], s[54:55], 0x900
	s_load_dwordx16 s[72:87], s[54:55], 0x940
	v_cvt_f32_f16_sdwa v38, v38 dst_sel:DWORD dst_unused:UNUSED_PAD src0_sel:WORD_1
	v_cvt_f32_f16_sdwa v69, v30 dst_sel:DWORD dst_unused:UNUSED_PAD src0_sel:WORD_1
	v_pk_mul_f32 v[122:123], v[38:39], v[14:15] op_sel_hi:[0,1]
	v_exp_f32_e32 v122, v122
	v_exp_f32_e32 v123, v123
	v_pk_mul_f32 v[130:131], v[38:39], v[16:17] op_sel_hi:[0,1]
	v_exp_f32_e32 v130, v130
	v_exp_f32_e32 v131, v131
	v_mul_f32_e32 v120, v38, v69
	v_pk_mul_f32 v[122:123], v[122:123], v[124:125]
	v_pk_fma_f32 v[122:123], v[120:121], s[56:57], v[122:123] op_sel_hi:[0, 1, 1]
	v_pk_fma_f32 v[42:43], s[88:89], v[122:123], 0 op_sel_hi:[1, 1, 0]
	v_pk_mul_f32 v[58:59], v[130:131], v[126:127]
	s_nop 0
	v_pk_fma_f32 v[124:125], v[120:121], s[58:59], v[58:59] op_sel_hi:[0, 1, 1]
	v_pk_mul_f32 v[44:45], v[38:39], v[10:11] op_sel_hi:[0,1]
	v_exp_f32_e32 v44, v44
	v_exp_f32_e32 v45, v45
	v_pk_mul_f32 v[58:59], v[38:39], v[12:13] op_sel_hi:[0,1]
	v_exp_f32_e32 v58, v58
	v_exp_f32_e32 v59, v59
	v_pk_mul_f32 v[44:45], v[44:45], v[128:129]
	v_pk_fma_f32 v[42:43], s[90:91], v[124:125], v[42:43]
	v_pk_fma_f32 v[126:127], v[120:121], s[60:61], v[44:45] op_sel_hi:[0, 1, 1]
	v_pk_mul_f32 v[44:45], v[58:59], v[110:111]
	v_pk_mul_f32 v[46:47], v[38:39], v[8:9] op_sel_hi:[0,1]
	v_pk_fma_f32 v[110:111], v[120:121], s[62:63], v[44:45] op_sel_hi:[0, 1, 1]
	v_pk_mul_f32 v[44:45], v[38:39], v[6:7] op_sel_hi:[0,1]
	v_exp_f32_e32 v44, v44
	v_exp_f32_e32 v45, v45
	v_exp_f32_e32 v46, v46
	v_exp_f32_e32 v47, v47
	v_pk_fma_f32 v[42:43], s[92:93], v[126:127], v[42:43]
	v_pk_mul_f32 v[44:45], v[44:45], v[112:113]
	v_pk_fma_f32 v[42:43], s[94:95], v[110:111], v[42:43]
	v_pk_fma_f32 v[112:113], v[120:121], s[64:65], v[44:45] op_sel_hi:[0, 1, 1]
	v_pk_mul_f32 v[44:45], v[46:47], v[114:115]
	v_pk_mul_f32 v[46:47], v[38:39], v[4:5] op_sel_hi:[0,1]
	v_pk_fma_f32 v[114:115], v[120:121], s[66:67], v[44:45] op_sel_hi:[0, 1, 1]
	v_pk_mul_f32 v[44:45], v[38:39], v[2:3] op_sel_hi:[0,1]
	v_exp_f32_e32 v44, v44
	v_exp_f32_e32 v45, v45
	v_exp_f32_e32 v46, v46
	v_exp_f32_e32 v47, v47
	v_pk_fma_f32 v[42:43], s[96:97], v[112:113], v[42:43]
	v_pk_mul_f32 v[44:45], v[44:45], v[116:117]
	v_pk_fma_f32 v[42:43], s[98:99], v[114:115], v[42:43]
	v_pk_fma_f32 v[116:117], v[120:121], s[68:69], v[44:45] op_sel_hi:[0, 1, 1]
	v_pk_mul_f32 v[44:45], v[46:47], v[118:119]
	v_pk_fma_f32 v[42:43], s[20:21], v[116:117], v[42:43]
	v_pk_fma_f32 v[118:119], v[120:121], s[70:71], v[44:45] op_sel_hi:[0, 1, 1]
	v_pk_fma_f32 v[42:43], s[22:23], v[118:119], v[42:43]
	s_nop 0
	v_add_f32_e32 v38, v42, v43
	v_fma_mix_f32 v30, v1, v30, v38 op_sel:[0,1,0] op_sel_hi:[0,1,0]
	v_fma_mixlo_f16 v30, v30, v34, 0 op_sel:[0,1,0] op_sel_hi:[0,1,0]
	ds_write_b16 v68, v30 offset:21776
	s_waitcnt lgkmcnt(0)
	s_load_dwordx16 s[56:71], s[54:55], 0x980
	s_load_dwordx8 s[88:95], s[54:55], 0x9c0
	s_load_dwordx4 s[96:99], s[54:55], 0x9e0
	s_load_dwordx4 s[20:23], s[54:55], 0x9f0
	v_cvt_f32_f16_e32 v30, v39
	v_cvt_f32_f16_e32 v34, v31
	v_pk_mul_f32 v[120:121], v[30:31], v[14:15] op_sel_hi:[0,1]
	v_exp_f32_e32 v120, v120
	v_exp_f32_e32 v121, v121
	v_pk_mul_f32 v[128:129], v[30:31], v[16:17] op_sel_hi:[0,1]
	v_exp_f32_e32 v128, v128
	v_exp_f32_e32 v129, v129
	v_mul_f32_e32 v34, v30, v34
	v_pk_mul_f32 v[120:121], v[120:121], v[122:123]
	v_pk_fma_f32 v[120:121], v[34:35], s[36:37], v[120:121] op_sel_hi:[0, 1, 1]
	v_pk_fma_f32 v[70:71], s[72:73], v[120:121], 0 op_sel_hi:[1, 1, 0]
	v_pk_mul_f32 v[86:87], v[128:129], v[124:125]
	s_nop 0
	v_pk_fma_f32 v[122:123], v[34:35], s[38:39], v[86:87] op_sel_hi:[0, 1, 1]
	v_pk_mul_f32 v[72:73], v[30:31], v[10:11] op_sel_hi:[0,1]
	v_exp_f32_e32 v72, v72
	v_exp_f32_e32 v73, v73
	v_pk_mul_f32 v[86:87], v[30:31], v[12:13] op_sel_hi:[0,1]
	v_exp_f32_e32 v86, v86
	v_exp_f32_e32 v87, v87
	v_pk_mul_f32 v[72:73], v[72:73], v[126:127]
	v_pk_fma_f32 v[70:71], s[74:75], v[122:123], v[70:71]
	v_pk_fma_f32 v[124:125], v[34:35], s[40:41], v[72:73] op_sel_hi:[0, 1, 1]
	v_pk_mul_f32 v[72:73], v[86:87], v[110:111]
	v_pk_mul_f32 v[74:75], v[30:31], v[8:9] op_sel_hi:[0,1]
	v_pk_fma_f32 v[110:111], v[34:35], s[42:43], v[72:73] op_sel_hi:[0, 1, 1]
	v_pk_mul_f32 v[72:73], v[30:31], v[6:7] op_sel_hi:[0,1]
	v_exp_f32_e32 v72, v72
	v_exp_f32_e32 v73, v73
	v_exp_f32_e32 v74, v74
	v_exp_f32_e32 v75, v75
	v_pk_fma_f32 v[70:71], s[76:77], v[124:125], v[70:71]
	v_pk_mul_f32 v[72:73], v[72:73], v[112:113]
	v_pk_fma_f32 v[70:71], s[78:79], v[110:111], v[70:71]
	v_pk_fma_f32 v[112:113], v[34:35], s[44:45], v[72:73] op_sel_hi:[0, 1, 1]
	v_pk_mul_f32 v[72:73], v[74:75], v[114:115]
	v_pk_mul_f32 v[74:75], v[30:31], v[4:5] op_sel_hi:[0,1]
	v_pk_fma_f32 v[114:115], v[34:35], s[46:47], v[72:73] op_sel_hi:[0, 1, 1]
	v_pk_mul_f32 v[72:73], v[30:31], v[2:3] op_sel_hi:[0,1]
	v_exp_f32_e32 v72, v72
	v_exp_f32_e32 v73, v73
	v_exp_f32_e32 v74, v74
	v_exp_f32_e32 v75, v75
	v_pk_fma_f32 v[70:71], s[80:81], v[112:113], v[70:71]
	v_pk_mul_f32 v[72:73], v[72:73], v[116:117]
	v_pk_fma_f32 v[70:71], s[82:83], v[114:115], v[70:71]
	v_pk_fma_f32 v[116:117], v[34:35], s[48:49], v[72:73] op_sel_hi:[0, 1, 1]
	v_pk_mul_f32 v[72:73], v[74:75], v[118:119]
	v_pk_fma_f32 v[70:71], s[84:85], v[116:117], v[70:71]
	v_pk_fma_f32 v[118:119], v[34:35], s[50:51], v[72:73] op_sel_hi:[0, 1, 1]
	v_pk_fma_f32 v[70:71], s[86:87], v[118:119], v[70:71]
	s_nop 0
	v_add_f32_e32 v30, v70, v71
	v_fma_mix_f32 v30, v1, v31, v30 op_sel_hi:[0,1,0]
	v_fma_mixlo_f16 v30, v30, v35, 0 op_sel_hi:[0,1,0]
	ds_write_b16 v68, v30 offset:22816
	s_waitcnt lgkmcnt(0)
	s_load_dwordx16 s[36:51], s[54:55], 0xa00
	s_load_dwordx16 s[72:87], s[54:55], 0xa40
	v_cvt_f32_f16_sdwa v30, v39 dst_sel:DWORD dst_unused:UNUSED_PAD src0_sel:WORD_1
	v_cvt_f32_f16_sdwa v34, v31 dst_sel:DWORD dst_unused:UNUSED_PAD src0_sel:WORD_1
	v_pk_mul_f32 v[38:39], v[30:31], v[14:15] op_sel_hi:[0,1]
	v_exp_f32_e32 v38, v38
	v_exp_f32_e32 v39, v39
	v_pk_mul_f32 v[126:127], v[30:31], v[16:17] op_sel_hi:[0,1]
	v_exp_f32_e32 v126, v126
	v_exp_f32_e32 v127, v127
	v_mul_f32_e32 v34, v30, v34
	v_pk_mul_f32 v[38:39], v[38:39], v[120:121]
	v_pk_fma_f32 v[38:39], v[34:35], s[56:57], v[38:39] op_sel_hi:[0, 1, 1]
	v_pk_fma_f32 v[42:43], s[88:89], v[38:39], 0 op_sel_hi:[1, 1, 0]
	v_pk_mul_f32 v[58:59], v[126:127], v[122:123]
	s_nop 0
	v_pk_fma_f32 v[120:121], v[34:35], s[58:59], v[58:59] op_sel_hi:[0, 1, 1]
	v_pk_mul_f32 v[44:45], v[30:31], v[10:11] op_sel_hi:[0,1]
	v_exp_f32_e32 v44, v44
	v_exp_f32_e32 v45, v45
	v_pk_mul_f32 v[58:59], v[30:31], v[12:13] op_sel_hi:[0,1]
	v_exp_f32_e32 v58, v58
	v_exp_f32_e32 v59, v59
	v_pk_mul_f32 v[44:45], v[44:45], v[124:125]
	v_pk_fma_f32 v[42:43], s[90:91], v[120:121], v[42:43]
	v_pk_fma_f32 v[122:123], v[34:35], s[60:61], v[44:45] op_sel_hi:[0, 1, 1]
	v_pk_mul_f32 v[44:45], v[58:59], v[110:111]
	v_pk_mul_f32 v[46:47], v[30:31], v[8:9] op_sel_hi:[0,1]
	v_pk_fma_f32 v[110:111], v[34:35], s[62:63], v[44:45] op_sel_hi:[0, 1, 1]
	v_pk_mul_f32 v[44:45], v[30:31], v[6:7] op_sel_hi:[0,1]
	v_exp_f32_e32 v44, v44
	v_exp_f32_e32 v45, v45
	v_exp_f32_e32 v46, v46
	v_exp_f32_e32 v47, v47
	v_pk_fma_f32 v[42:43], s[92:93], v[122:123], v[42:43]
	v_pk_mul_f32 v[44:45], v[44:45], v[112:113]
	v_pk_fma_f32 v[42:43], s[94:95], v[110:111], v[42:43]
	v_pk_fma_f32 v[112:113], v[34:35], s[64:65], v[44:45] op_sel_hi:[0, 1, 1]
	v_pk_mul_f32 v[44:45], v[46:47], v[114:115]
	v_pk_mul_f32 v[46:47], v[30:31], v[4:5] op_sel_hi:[0,1]
	v_pk_fma_f32 v[114:115], v[34:35], s[66:67], v[44:45] op_sel_hi:[0, 1, 1]
	v_pk_mul_f32 v[44:45], v[30:31], v[2:3] op_sel_hi:[0,1]
	v_exp_f32_e32 v44, v44
	v_exp_f32_e32 v45, v45
	v_exp_f32_e32 v46, v46
	v_exp_f32_e32 v47, v47
	v_pk_fma_f32 v[42:43], s[96:97], v[112:113], v[42:43]
	v_pk_mul_f32 v[44:45], v[44:45], v[116:117]
	v_pk_fma_f32 v[42:43], s[98:99], v[114:115], v[42:43]
	v_pk_fma_f32 v[116:117], v[34:35], s[68:69], v[44:45] op_sel_hi:[0, 1, 1]
	v_pk_mul_f32 v[44:45], v[46:47], v[118:119]
	v_pk_fma_f32 v[42:43], s[20:21], v[116:117], v[42:43]
	v_pk_fma_f32 v[118:119], v[34:35], s[70:71], v[44:45] op_sel_hi:[0, 1, 1]
	v_pk_fma_f32 v[42:43], s[22:23], v[118:119], v[42:43]
	s_nop 0
	v_add_f32_e32 v30, v42, v43
	v_fma_mix_f32 v30, v1, v31, v30 op_sel:[0,1,0] op_sel_hi:[0,1,0]
	v_fma_mixlo_f16 v30, v30, v35, 0 op_sel:[0,1,0] op_sel_hi:[0,1,0]
	ds_write_b16 v68, v30 offset:23856
	s_waitcnt lgkmcnt(0)
	s_load_dwordx16 s[56:71], s[54:55], 0xa80
	s_load_dwordx8 s[88:95], s[54:55], 0xac0
	s_load_dwordx4 s[96:99], s[54:55], 0xae0
	s_load_dwordx4 s[20:23], s[54:55], 0xaf0
	v_cvt_f32_f16_e32 v30, v40
	v_cvt_f32_f16_e32 v31, v32
	v_pk_mul_f32 v[124:125], v[30:31], v[14:15] op_sel_hi:[0,1]
	v_exp_f32_e32 v124, v124
	v_exp_f32_e32 v125, v125
	v_pk_mul_f32 v[126:127], v[30:31], v[16:17] op_sel_hi:[0,1]
	v_exp_f32_e32 v126, v126
	v_exp_f32_e32 v127, v127
	v_mul_f32_e32 v34, v30, v31
	v_pk_mul_f32 v[38:39], v[124:125], v[38:39]
	v_pk_fma_f32 v[38:39], v[34:35], s[36:37], v[38:39] op_sel_hi:[0, 1, 1]
	v_pk_fma_f32 v[70:71], s[72:73], v[38:39], 0 op_sel_hi:[1, 1, 0]
	v_pk_mul_f32 v[86:87], v[126:127], v[120:121]
	s_nop 0
	v_pk_fma_f32 v[120:121], v[34:35], s[38:39], v[86:87] op_sel_hi:[0, 1, 1]
	v_pk_mul_f32 v[72:73], v[30:31], v[10:11] op_sel_hi:[0,1]
	v_exp_f32_e32 v72, v72
	v_exp_f32_e32 v73, v73
	v_pk_mul_f32 v[86:87], v[30:31], v[12:13] op_sel_hi:[0,1]
	v_exp_f32_e32 v86, v86
	v_exp_f32_e32 v87, v87
	v_pk_mul_f32 v[72:73], v[72:73], v[122:123]
	v_pk_fma_f32 v[70:71], s[74:75], v[120:121], v[70:71]
	v_pk_fma_f32 v[122:123], v[34:35], s[40:41], v[72:73] op_sel_hi:[0, 1, 1]
	v_pk_mul_f32 v[72:73], v[86:87], v[110:111]
	v_pk_mul_f32 v[74:75], v[30:31], v[8:9] op_sel_hi:[0,1]
	v_pk_fma_f32 v[110:111], v[34:35], s[42:43], v[72:73] op_sel_hi:[0, 1, 1]
	v_pk_mul_f32 v[72:73], v[30:31], v[6:7] op_sel_hi:[0,1]
	v_exp_f32_e32 v72, v72
	v_exp_f32_e32 v73, v73
	v_exp_f32_e32 v74, v74
	v_exp_f32_e32 v75, v75
	v_pk_fma_f32 v[70:71], s[76:77], v[122:123], v[70:71]
	v_pk_mul_f32 v[72:73], v[72:73], v[112:113]
	v_pk_fma_f32 v[70:71], s[78:79], v[110:111], v[70:71]
	v_pk_fma_f32 v[112:113], v[34:35], s[44:45], v[72:73] op_sel_hi:[0, 1, 1]
	v_pk_mul_f32 v[72:73], v[74:75], v[114:115]
	v_pk_fma_f32 v[70:71], s[80:81], v[112:113], v[70:71]
	v_pk_fma_f32 v[114:115], v[34:35], s[46:47], v[72:73] op_sel_hi:[0, 1, 1]
	v_pk_mul_f32 v[72:73], v[30:31], v[2:3] op_sel_hi:[0,1]
	v_exp_f32_e32 v72, v72
	v_exp_f32_e32 v73, v73
	v_pk_mul_f32 v[30:31], v[30:31], v[4:5] op_sel_hi:[0,1]
	v_exp_f32_e32 v30, v30
	v_exp_f32_e32 v31, v31
	v_pk_mul_f32 v[72:73], v[72:73], v[116:117]
	v_pk_fma_f32 v[70:71], s[82:83], v[114:115], v[70:71]
	v_pk_fma_f32 v[116:117], v[34:35], s[48:49], v[72:73] op_sel_hi:[0, 1, 1]
	v_pk_mul_f32 v[30:31], v[30:31], v[118:119]
	v_pk_fma_f32 v[70:71], s[84:85], v[116:117], v[70:71]
	v_pk_fma_f32 v[30:31], v[34:35], s[50:51], v[30:31] op_sel_hi:[0, 1, 1]
	v_pk_fma_f32 v[34:35], s[86:87], v[30:31], v[70:71]
	s_nop 0
	v_add_f32_e32 v34, v34, v35
	v_fma_mix_f32 v34, v1, v32, v34 op_sel_hi:[0,1,0]
	v_fma_mixlo_f16 v34, v34, v36, 0 op_sel_hi:[0,1,0]
	ds_write_b16 v68, v34 offset:24896
	s_waitcnt lgkmcnt(0)
	s_load_dwordx16 s[36:51], s[54:55], 0xb00
	s_load_dwordx16 s[72:87], s[54:55], 0xb40
	v_cvt_f32_f16_sdwa v34, v40 dst_sel:DWORD dst_unused:UNUSED_PAD src0_sel:WORD_1
	v_cvt_f32_f16_sdwa v35, v32 dst_sel:DWORD dst_unused:UNUSED_PAD src0_sel:WORD_1
	v_pk_mul_f32 v[118:119], v[34:35], v[14:15] op_sel_hi:[0,1]
	v_exp_f32_e32 v118, v118
	v_exp_f32_e32 v119, v119
	v_pk_mul_f32 v[124:125], v[34:35], v[16:17] op_sel_hi:[0,1]
	v_exp_f32_e32 v124, v124
	v_exp_f32_e32 v125, v125
	v_mul_f32_e32 v40, v34, v35
	v_pk_mul_f32 v[38:39], v[118:119], v[38:39]
	v_pk_fma_f32 v[38:39], v[40:41], s[56:57], v[38:39] op_sel_hi:[0, 1, 1]
	v_pk_fma_f32 v[42:43], s[88:89], v[38:39], 0 op_sel_hi:[1, 1, 0]
	v_pk_mul_f32 v[58:59], v[124:125], v[120:121]
	s_nop 0
	v_pk_fma_f32 v[118:119], v[40:41], s[58:59], v[58:59] op_sel_hi:[0, 1, 1]
	v_pk_mul_f32 v[44:45], v[34:35], v[10:11] op_sel_hi:[0,1]
	v_exp_f32_e32 v44, v44
	v_exp_f32_e32 v45, v45
	v_pk_mul_f32 v[58:59], v[34:35], v[12:13] op_sel_hi:[0,1]
	v_exp_f32_e32 v58, v58
	v_exp_f32_e32 v59, v59
	v_pk_mul_f32 v[44:45], v[44:45], v[122:123]
	v_pk_fma_f32 v[42:43], s[90:91], v[118:119], v[42:43]
	v_pk_fma_f32 v[120:121], v[40:41], s[60:61], v[44:45] op_sel_hi:[0, 1, 1]
	v_pk_mul_f32 v[44:45], v[58:59], v[110:111]
	v_pk_mul_f32 v[46:47], v[34:35], v[8:9] op_sel_hi:[0,1]
	v_pk_fma_f32 v[110:111], v[40:41], s[62:63], v[44:45] op_sel_hi:[0, 1, 1]
	v_pk_mul_f32 v[44:45], v[34:35], v[6:7] op_sel_hi:[0,1]
	v_exp_f32_e32 v44, v44
	v_exp_f32_e32 v45, v45
	v_exp_f32_e32 v46, v46
	v_exp_f32_e32 v47, v47
	v_pk_fma_f32 v[42:43], s[92:93], v[120:121], v[42:43]
	v_pk_mul_f32 v[44:45], v[44:45], v[112:113]
	v_pk_fma_f32 v[42:43], s[94:95], v[110:111], v[42:43]
	v_pk_fma_f32 v[112:113], v[40:41], s[64:65], v[44:45] op_sel_hi:[0, 1, 1]
	v_pk_mul_f32 v[44:45], v[46:47], v[114:115]
	v_pk_fma_f32 v[42:43], s[96:97], v[112:113], v[42:43]
	v_pk_fma_f32 v[114:115], v[40:41], s[66:67], v[44:45] op_sel_hi:[0, 1, 1]
	v_pk_mul_f32 v[44:45], v[34:35], v[2:3] op_sel_hi:[0,1]
	v_exp_f32_e32 v44, v44
	v_exp_f32_e32 v45, v45
	v_pk_mul_f32 v[34:35], v[34:35], v[4:5] op_sel_hi:[0,1]
	v_exp_f32_e32 v34, v34
	v_exp_f32_e32 v35, v35
	v_pk_mul_f32 v[44:45], v[44:45], v[116:117]
	v_pk_fma_f32 v[42:43], s[98:99], v[114:115], v[42:43]
	v_pk_fma_f32 v[116:117], v[40:41], s[68:69], v[44:45] op_sel_hi:[0, 1, 1]
	v_pk_mul_f32 v[30:31], v[34:35], v[30:31]
	v_pk_fma_f32 v[42:43], s[20:21], v[116:117], v[42:43]
	v_pk_fma_f32 v[30:31], v[40:41], s[70:71], v[30:31] op_sel_hi:[0, 1, 1]
	v_pk_fma_f32 v[34:35], s[22:23], v[30:31], v[42:43]
	s_nop 0
	v_add_f32_e32 v34, v34, v35
	v_fma_mix_f32 v32, v1, v32, v34 op_sel:[0,1,0] op_sel_hi:[0,1,0]
	v_fma_mixlo_f16 v32, v32, v36, 0 op_sel:[0,1,0] op_sel_hi:[0,1,0]
	ds_write_b16 v68, v32 offset:25936
	s_waitcnt lgkmcnt(0)
	s_load_dwordx16 s[56:71], s[54:55], 0xb80
	s_load_dwordx8 s[88:95], s[54:55], 0xbc0
	s_load_dwordx4 s[96:99], s[54:55], 0xbe0
	s_load_dwordx4 s[20:23], s[54:55], 0xbf0
	v_cvt_f32_f16_e32 v32, v41
	v_cvt_f32_f16_e32 v34, v33
	v_pk_mul_f32 v[122:123], v[32:33], v[14:15] op_sel_hi:[0,1]
	v_exp_f32_e32 v122, v122
	v_exp_f32_e32 v123, v123
	v_pk_mul_f32 v[124:125], v[32:33], v[16:17] op_sel_hi:[0,1]
	v_exp_f32_e32 v124, v124
	v_exp_f32_e32 v125, v125
	v_mul_f32_e32 v34, v32, v34
	v_pk_mul_f32 v[38:39], v[122:123], v[38:39]
	v_pk_fma_f32 v[38:39], v[34:35], s[36:37], v[38:39] op_sel_hi:[0, 1, 1]
	v_pk_fma_f32 v[70:71], s[72:73], v[38:39], 0 op_sel_hi:[1, 1, 0]
	v_pk_mul_f32 v[86:87], v[124:125], v[118:119]
	s_nop 0
	v_pk_fma_f32 v[118:119], v[34:35], s[38:39], v[86:87] op_sel_hi:[0, 1, 1]
	v_pk_mul_f32 v[72:73], v[32:33], v[10:11] op_sel_hi:[0,1]
	v_exp_f32_e32 v72, v72
	v_exp_f32_e32 v73, v73
	v_pk_mul_f32 v[86:87], v[32:33], v[12:13] op_sel_hi:[0,1]
	v_exp_f32_e32 v86, v86
	v_exp_f32_e32 v87, v87
	v_pk_mul_f32 v[72:73], v[72:73], v[120:121]
	v_pk_fma_f32 v[70:71], s[74:75], v[118:119], v[70:71]
	v_pk_fma_f32 v[120:121], v[34:35], s[40:41], v[72:73] op_sel_hi:[0, 1, 1]
	v_pk_mul_f32 v[72:73], v[86:87], v[110:111]
	v_pk_mul_f32 v[74:75], v[32:33], v[8:9] op_sel_hi:[0,1]
	v_pk_fma_f32 v[110:111], v[34:35], s[42:43], v[72:73] op_sel_hi:[0, 1, 1]
	v_pk_mul_f32 v[72:73], v[32:33], v[6:7] op_sel_hi:[0,1]
	v_exp_f32_e32 v72, v72
	v_exp_f32_e32 v73, v73
	v_exp_f32_e32 v74, v74
	v_exp_f32_e32 v75, v75
	v_pk_fma_f32 v[70:71], s[76:77], v[120:121], v[70:71]
	v_pk_mul_f32 v[72:73], v[72:73], v[112:113]
	v_pk_fma_f32 v[70:71], s[78:79], v[110:111], v[70:71]
	v_pk_fma_f32 v[112:113], v[34:35], s[44:45], v[72:73] op_sel_hi:[0, 1, 1]
	v_pk_mul_f32 v[72:73], v[74:75], v[114:115]
	v_pk_mul_f32 v[74:75], v[32:33], v[4:5] op_sel_hi:[0,1]
	v_pk_fma_f32 v[114:115], v[34:35], s[46:47], v[72:73] op_sel_hi:[0, 1, 1]
	v_pk_mul_f32 v[72:73], v[32:33], v[2:3] op_sel_hi:[0,1]
	v_exp_f32_e32 v72, v72
	v_exp_f32_e32 v73, v73
	v_exp_f32_e32 v74, v74
	v_exp_f32_e32 v75, v75
	v_pk_fma_f32 v[70:71], s[80:81], v[112:113], v[70:71]
	v_pk_mul_f32 v[72:73], v[72:73], v[116:117]
	v_pk_fma_f32 v[70:71], s[82:83], v[114:115], v[70:71]
	v_pk_fma_f32 v[116:117], v[34:35], s[48:49], v[72:73] op_sel_hi:[0, 1, 1]
	v_pk_mul_f32 v[30:31], v[74:75], v[30:31]
	v_pk_fma_f32 v[70:71], s[84:85], v[116:117], v[70:71]
	v_pk_fma_f32 v[30:31], v[34:35], s[50:51], v[30:31] op_sel_hi:[0, 1, 1]
	v_pk_fma_f32 v[34:35], s[86:87], v[30:31], v[70:71]
	s_nop 0
	v_add_f32_e32 v32, v34, v35
	v_fma_mix_f32 v32, v1, v33, v32 op_sel_hi:[0,1,0]
	v_fma_mixlo_f16 v32, v32, v37, 0 op_sel_hi:[0,1,0]
	ds_write_b16 v68, v32 offset:26976
	s_waitcnt lgkmcnt(0)
	s_load_dwordx16 s[36:51], s[54:55], 0xc00
	s_load_dwordx16 s[72:87], s[54:55], 0xc40
	v_cvt_f32_f16_sdwa v32, v41 dst_sel:DWORD dst_unused:UNUSED_PAD src0_sel:WORD_1
	v_cvt_f32_f16_sdwa v34, v33 dst_sel:DWORD dst_unused:UNUSED_PAD src0_sel:WORD_1
	v_pk_mul_f32 v[40:41], v[32:33], v[14:15] op_sel_hi:[0,1]
	v_pk_mul_f32 v[122:123], v[32:33], v[16:17] op_sel_hi:[0,1]
	v_exp_f32_e32 v40, v40
	v_exp_f32_e32 v41, v41
	v_exp_f32_e32 v122, v122
	v_exp_f32_e32 v123, v123
	v_mul_f32_e32 v34, v32, v34
	v_pk_mul_f32 v[38:39], v[40:41], v[38:39]
	v_pk_mul_f32 v[40:41], v[122:123], v[118:119]
	v_pk_fma_f32 v[118:119], v[34:35], s[58:59], v[40:41] op_sel_hi:[0, 1, 1]
	v_pk_mul_f32 v[40:41], v[32:33], v[10:11] op_sel_hi:[0,1]
	v_pk_fma_f32 v[124:125], v[34:35], s[56:57], v[38:39] op_sel_hi:[0, 1, 1]
	v_exp_f32_e32 v40, v40
	v_exp_f32_e32 v41, v41
	v_pk_mul_f32 v[42:43], v[32:33], v[12:13] op_sel_hi:[0,1]
	v_exp_f32_e32 v42, v42
	v_exp_f32_e32 v43, v43
	v_pk_fma_f32 v[38:39], s[88:89], v[124:125], 0 op_sel_hi:[1, 1, 0]
	v_pk_mul_f32 v[40:41], v[40:41], v[120:121]
	v_pk_fma_f32 v[38:39], s[90:91], v[118:119], v[38:39]
	v_pk_fma_f32 v[120:121], v[34:35], s[60:61], v[40:41] op_sel_hi:[0, 1, 1]
	v_pk_mul_f32 v[40:41], v[42:43], v[110:111]
	v_pk_fma_f32 v[38:39], s[92:93], v[120:121], v[38:39]
	v_pk_fma_f32 v[62:63], v[34:35], s[62:63], v[40:41] op_sel_hi:[0, 1, 1]
	v_pk_mul_f32 v[40:41], v[32:33], v[6:7] op_sel_hi:[0,1]
	v_exp_f32_e32 v40, v40
	v_exp_f32_e32 v41, v41
	v_pk_mul_f32 v[42:43], v[32:33], v[8:9] op_sel_hi:[0,1]
	v_exp_f32_e32 v42, v42
	v_exp_f32_e32 v43, v43
	v_pk_mul_f32 v[40:41], v[40:41], v[112:113]
	v_pk_fma_f32 v[38:39], s[94:95], v[62:63], v[38:39]
	v_pk_fma_f32 v[64:65], v[34:35], s[64:65], v[40:41] op_sel_hi:[0, 1, 1]
	v_pk_mul_f32 v[40:41], v[42:43], v[114:115]
	v_pk_fma_f32 v[38:39], s[96:97], v[64:65], v[38:39]
	v_pk_fma_f32 v[102:103], v[34:35], s[66:67], v[40:41] op_sel_hi:[0, 1, 1]
	v_pk_mul_f32 v[40:41], v[32:33], v[2:3] op_sel_hi:[0,1]
	v_exp_f32_e32 v40, v40
	v_exp_f32_e32 v41, v41
	v_pk_mul_f32 v[42:43], v[32:33], v[4:5] op_sel_hi:[0,1]
	v_exp_f32_e32 v42, v42
	v_exp_f32_e32 v43, v43
	v_pk_mul_f32 v[40:41], v[40:41], v[116:117]
	v_pk_fma_f32 v[38:39], s[98:99], v[102:103], v[38:39]
	v_pk_fma_f32 v[104:105], v[34:35], s[68:69], v[40:41] op_sel_hi:[0, 1, 1]
	v_pk_mul_f32 v[30:31], v[42:43], v[30:31]
	v_pk_fma_f32 v[38:39], s[20:21], v[104:105], v[38:39]
	v_pk_fma_f32 v[106:107], v[34:35], s[70:71], v[30:31] op_sel_hi:[0, 1, 1]
	v_pk_fma_f32 v[30:31], s[22:23], v[106:107], v[38:39]
	s_nop 0
	v_add_f32_e32 v30, v30, v31
	v_fma_mix_f32 v30, v1, v33, v30 op_sel:[0,1,0] op_sel_hi:[0,1,0]
	v_fma_mixlo_f16 v30, v30, v37, 0 op_sel:[0,1,0] op_sel_hi:[0,1,0]
	ds_write_b16 v68, v30 offset:28016
	s_waitcnt lgkmcnt(0)
	s_load_dwordx16 s[56:71], s[54:55], 0xc80
	s_load_dwordx8 s[88:95], s[54:55], 0xcc0
	s_load_dwordx4 s[96:99], s[54:55], 0xce0
	s_load_dwordx4 s[20:23], s[54:55], 0xcf0
	s_waitcnt vmcnt(2)
	v_cvt_f32_f16_e32 v108, v26
	s_waitcnt vmcnt(1)
	v_cvt_f32_f16_e32 v69, v18
	v_pk_mul_f32 v[112:113], v[108:109], v[14:15] op_sel_hi:[0,1]
	v_exp_f32_e32 v112, v112
	v_exp_f32_e32 v113, v113
	v_pk_mul_f32 v[114:115], v[108:109], v[16:17] op_sel_hi:[0,1]
	v_exp_f32_e32 v114, v114
	v_exp_f32_e32 v115, v115
	v_mul_f32_e32 v110, v108, v69
	v_pk_mul_f32 v[112:113], v[112:113], v[124:125]
	v_pk_fma_f32 v[112:113], v[110:111], s[36:37], v[112:113] op_sel_hi:[0, 1, 1]
	v_pk_fma_f32 v[70:71], s[72:73], v[112:113], 0 op_sel_hi:[1, 1, 0]
	v_pk_mul_f32 v[86:87], v[114:115], v[118:119]
	s_nop 0
	v_pk_fma_f32 v[114:115], v[110:111], s[38:39], v[86:87] op_sel_hi:[0, 1, 1]
	v_pk_mul_f32 v[72:73], v[108:109], v[10:11] op_sel_hi:[0,1]
	v_exp_f32_e32 v72, v72
	v_exp_f32_e32 v73, v73
	v_pk_mul_f32 v[86:87], v[108:109], v[12:13] op_sel_hi:[0,1]
	v_exp_f32_e32 v86, v86
	v_exp_f32_e32 v87, v87
	v_pk_mul_f32 v[72:73], v[72:73], v[120:121]
	v_pk_fma_f32 v[70:71], s[74:75], v[114:115], v[70:71]
	v_pk_fma_f32 v[116:117], v[110:111], s[40:41], v[72:73] op_sel_hi:[0, 1, 1]
	v_pk_mul_f32 v[62:63], v[86:87], v[62:63]
	v_pk_fma_f32 v[70:71], s[76:77], v[116:117], v[70:71]
	v_pk_fma_f32 v[118:119], v[110:111], s[42:43], v[62:63] op_sel_hi:[0, 1, 1]
	v_pk_fma_f32 v[62:63], s[78:79], v[118:119], v[70:71]
	v_pk_mul_f32 v[70:71], v[108:109], v[6:7] op_sel_hi:[0,1]
	v_exp_f32_e32 v70, v70
	v_exp_f32_e32 v71, v71
	v_pk_mul_f32 v[72:73], v[108:109], v[8:9] op_sel_hi:[0,1]
	v_exp_f32_e32 v72, v72
	v_exp_f32_e32 v73, v73
	v_pk_mul_f32 v[64:65], v[70:71], v[64:65]
	v_pk_mul_f32 v[70:71], v[108:109], v[4:5] op_sel_hi:[0,1]
	v_pk_fma_f32 v[120:121], v[110:111], s[44:45], v[64:65] op_sel_hi:[0, 1, 1]
	v_pk_mul_f32 v[64:65], v[72:73], v[102:103]
	v_exp_f32_e32 v70, v70
	v_pk_fma_f32 v[102:103], v[110:111], s[46:47], v[64:65] op_sel_hi:[0, 1, 1]
	v_pk_mul_f32 v[64:65], v[108:109], v[2:3] op_sel_hi:[0,1]
	v_exp_f32_e32 v64, v64
	v_exp_f32_e32 v65, v65
	v_exp_f32_e32 v71, v71
	v_pk_fma_f32 v[62:63], s[80:81], v[120:121], v[62:63]
	v_pk_mul_f32 v[64:65], v[64:65], v[104:105]
	v_pk_fma_f32 v[62:63], s[82:83], v[102:103], v[62:63]
	v_pk_fma_f32 v[104:105], v[110:111], s[48:49], v[64:65] op_sel_hi:[0, 1, 1]
	v_pk_mul_f32 v[64:65], v[70:71], v[106:107]
	v_pk_fma_f32 v[62:63], s[84:85], v[104:105], v[62:63]
	v_pk_fma_f32 v[98:99], v[110:111], s[50:51], v[64:65] op_sel_hi:[0, 1, 1]
	v_pk_fma_f32 v[62:63], s[86:87], v[98:99], v[62:63]
	s_nop 0
	v_add_f32_e32 v62, v62, v63
	v_fma_mix_f32 v62, v1, v18, v62 op_sel_hi:[0,1,0]
	s_waitcnt vmcnt(0)
	v_fma_mixlo_f16 v62, v62, v22, 0 op_sel_hi:[0,1,0]
	ds_write_b16 v68, v62 offset:29056
	v_lshrrev_b32_e32 v196, 6, v0
	v_and_b32_e32 v197, 48, v0
	v_lshl_or_b32 v196, v196, 7, v197
	v_and_b32_e32 v197, 15, v0
	v_or_b32_e32 v197, s28, v197
	v_lshl_or_b32 v196, v197, 10, v196
	v_add_u32_e32 v197, 0x4000, v196
	global_load_dwordx4 v[180:183], v196, s[4:5]
	global_load_dwordx4 v[184:187], v196, s[4:5] offset:64
	global_load_dwordx4 v[188:191], v197, s[4:5]
	global_load_dwordx4 v[192:195], v197, s[4:5] offset:64
	v_and_b32_e32 v196, 63, v0
	v_lshlrev_b32_e32 v196, 4, v196
	global_load_dwordx4 v[204:207], v196, s[6:7]
	global_load_dwordx4 v[208:211], v196, s[8:9]
	s_waitcnt lgkmcnt(0)
	s_load_dwordx16 s[36:51], s[54:55], 0xd00
	s_load_dwordx16 s[72:87], s[54:55], 0xd40
	v_cvt_f32_f16_sdwa v26, v26 dst_sel:DWORD dst_unused:UNUSED_PAD src0_sel:WORD_1
	v_cvt_f32_f16_sdwa v69, v18 dst_sel:DWORD dst_unused:UNUSED_PAD src0_sel:WORD_1
	v_pk_mul_f32 v[106:107], v[26:27], v[14:15] op_sel_hi:[0,1]
	v_exp_f32_e32 v106, v106
	v_exp_f32_e32 v107, v107
	v_pk_mul_f32 v[108:109], v[26:27], v[16:17] op_sel_hi:[0,1]
	v_exp_f32_e32 v108, v108
	v_exp_f32_e32 v109, v109
	v_mul_f32_e32 v100, v26, v69
	v_pk_mul_f32 v[106:107], v[106:107], v[112:113]
	v_pk_fma_f32 v[106:107], v[100:101], s[56:57], v[106:107] op_sel_hi:[0, 1, 1]
	v_pk_fma_f32 v[30:31], s[88:89], v[106:107], 0 op_sel_hi:[1, 1, 0]
	v_pk_mul_f32 v[46:47], v[108:109], v[114:115]
	s_nop 0
	v_pk_fma_f32 v[108:109], v[100:101], s[58:59], v[46:47] op_sel_hi:[0, 1, 1]
	v_pk_mul_f32 v[32:33], v[26:27], v[10:11] op_sel_hi:[0,1]
	v_exp_f32_e32 v32, v32
	v_exp_f32_e32 v33, v33
	v_pk_mul_f32 v[46:47], v[26:27], v[12:13] op_sel_hi:[0,1]
	v_exp_f32_e32 v46, v46
	v_exp_f32_e32 v47, v47
	v_pk_mul_f32 v[32:33], v[32:33], v[116:117]
	v_pk_fma_f32 v[30:31], s[90:91], v[108:109], v[30:31]
	v_pk_fma_f32 v[110:111], v[100:101], s[60:61], v[32:33] op_sel_hi:[0, 1, 1]
	v_pk_mul_f32 v[32:33], v[46:47], v[118:119]
	v_pk_mul_f32 v[34:35], v[26:27], v[8:9] op_sel_hi:[0,1]
	v_pk_fma_f32 v[112:113], v[100:101], s[62:63], v[32:33] op_sel_hi:[0, 1, 1]
	v_pk_mul_f32 v[32:33], v[26:27], v[6:7] op_sel_hi:[0,1]
	v_exp_f32_e32 v32, v32
	v_exp_f32_e32 v33, v33
	v_exp_f32_e32 v34, v34
	v_exp_f32_e32 v35, v35
	v_pk_fma_f32 v[30:31], s[92:93], v[110:111], v[30:31]
	v_pk_mul_f32 v[32:33], v[32:33], v[120:121]
	v_pk_fma_f32 v[30:31], s[94:95], v[112:113], v[30:31]
	v_pk_fma_f32 v[114:115], v[100:101], s[64:65], v[32:33] op_sel_hi:[0, 1, 1]
	v_pk_mul_f32 v[32:33], v[34:35], v[102:103]
	v_pk_mul_f32 v[34:35], v[26:27], v[4:5] op_sel_hi:[0,1]
	v_pk_fma_f32 v[102:103], v[100:101], s[66:67], v[32:33] op_sel_hi:[0, 1, 1]
	v_pk_mul_f32 v[32:33], v[26:27], v[2:3] op_sel_hi:[0,1]
	v_exp_f32_e32 v32, v32
	v_exp_f32_e32 v33, v33
	v_exp_f32_e32 v34, v34
	v_exp_f32_e32 v35, v35
	v_pk_fma_f32 v[30:31], s[96:97], v[114:115], v[30:31]
	v_pk_mul_f32 v[32:33], v[32:33], v[104:105]
	v_pk_fma_f32 v[30:31], s[98:99], v[102:103], v[30:31]
	v_pk_fma_f32 v[104:105], v[100:101], s[68:69], v[32:33] op_sel_hi:[0, 1, 1]
	v_pk_mul_f32 v[32:33], v[34:35], v[98:99]
	v_pk_fma_f32 v[30:31], s[20:21], v[104:105], v[30:31]
	v_pk_fma_f32 v[98:99], v[100:101], s[70:71], v[32:33] op_sel_hi:[0, 1, 1]
	v_pk_fma_f32 v[30:31], s[22:23], v[98:99], v[30:31]
	s_nop 0
	v_add_f32_e32 v26, v30, v31
	v_fma_mix_f32 v18, v1, v18, v26 op_sel:[0,1,0] op_sel_hi:[0,1,0]
	v_fma_mixlo_f16 v18, v18, v22, 0 op_sel:[0,1,0] op_sel_hi:[0,1,0]
	ds_write_b16 v68, v18 offset:30096
	s_waitcnt lgkmcnt(0)
	s_load_dwordx16 s[56:71], s[54:55], 0xd80
	s_load_dwordx8 s[88:95], s[54:55], 0xdc0
	s_load_dwordx4 s[96:99], s[54:55], 0xde0
	s_load_dwordx4 s[20:23], s[54:55], 0xdf0
	v_cvt_f32_f16_e32 v18, v27
	v_cvt_f32_f16_e32 v22, v19
	v_pk_mul_f32 v[100:101], v[18:19], v[14:15] op_sel_hi:[0,1]
	v_exp_f32_e32 v100, v100
	v_exp_f32_e32 v101, v101
	v_pk_mul_f32 v[116:117], v[18:19], v[16:17] op_sel_hi:[0,1]
	v_exp_f32_e32 v116, v116
	v_exp_f32_e32 v117, v117
	v_mul_f32_e32 v22, v18, v22
	v_pk_mul_f32 v[100:101], v[100:101], v[106:107]
	v_pk_fma_f32 v[100:101], v[22:23], s[36:37], v[100:101] op_sel_hi:[0, 1, 1]
	v_pk_fma_f32 v[62:63], s[72:73], v[100:101], 0 op_sel_hi:[1, 1, 0]
	v_pk_mul_f32 v[82:83], v[116:117], v[108:109]
	s_nop 0
	v_pk_fma_f32 v[106:107], v[22:23], s[38:39], v[82:83] op_sel_hi:[0, 1, 1]
	v_pk_mul_f32 v[64:65], v[18:19], v[10:11] op_sel_hi:[0,1]
	v_exp_f32_e32 v64, v64
	v_exp_f32_e32 v65, v65
	v_pk_mul_f32 v[82:83], v[18:19], v[12:13] op_sel_hi:[0,1]
	v_exp_f32_e32 v82, v82
	v_exp_f32_e32 v83, v83
	v_pk_mul_f32 v[64:65], v[64:65], v[110:111]
	v_pk_fma_f32 v[62:63], s[74:75], v[106:107], v[62:63]
	v_pk_fma_f32 v[108:109], v[22:23], s[40:41], v[64:65] op_sel_hi:[0, 1, 1]
	v_pk_mul_f32 v[64:65], v[82:83], v[112:113]
	v_pk_mul_f32 v[70:71], v[18:19], v[8:9] op_sel_hi:[0,1]
	v_pk_fma_f32 v[110:111], v[22:23], s[42:43], v[64:65] op_sel_hi:[0, 1, 1]
	v_pk_mul_f32 v[64:65], v[18:19], v[6:7] op_sel_hi:[0,1]
	v_exp_f32_e32 v64, v64
	v_exp_f32_e32 v65, v65
	v_exp_f32_e32 v70, v70
	v_exp_f32_e32 v71, v71
	v_pk_fma_f32 v[62:63], s[76:77], v[108:109], v[62:63]
	v_pk_mul_f32 v[64:65], v[64:65], v[114:115]
	v_pk_fma_f32 v[62:63], s[78:79], v[110:111], v[62:63]
	v_pk_fma_f32 v[112:113], v[22:23], s[44:45], v[64:65] op_sel_hi:[0, 1, 1]
	v_pk_mul_f32 v[64:65], v[70:71], v[102:103]
	v_pk_mul_f32 v[70:71], v[18:19], v[4:5] op_sel_hi:[0,1]
	v_pk_fma_f32 v[102:103], v[22:23], s[46:47], v[64:65] op_sel_hi:[0, 1, 1]
	v_pk_mul_f32 v[64:65], v[18:19], v[2:3] op_sel_hi:[0,1]
	v_exp_f32_e32 v64, v64
	v_exp_f32_e32 v65, v65
	v_exp_f32_e32 v70, v70
	v_exp_f32_e32 v71, v71
	v_pk_fma_f32 v[62:63], s[80:81], v[112:113], v[62:63]
	v_pk_mul_f32 v[64:65], v[64:65], v[104:105]
	v_pk_fma_f32 v[62:63], s[82:83], v[102:103], v[62:63]
	v_pk_fma_f32 v[104:105], v[22:23], s[48:49], v[64:65] op_sel_hi:[0, 1, 1]
	v_pk_mul_f32 v[64:65], v[70:71], v[98:99]
	v_pk_fma_f32 v[62:63], s[84:85], v[104:105], v[62:63]
	v_pk_fma_f32 v[98:99], v[22:23], s[50:51], v[64:65] op_sel_hi:[0, 1, 1]
	v_pk_fma_f32 v[62:63], s[86:87], v[98:99], v[62:63]
	s_nop 0
	v_add_f32_e32 v18, v62, v63
	v_fma_mix_f32 v18, v1, v19, v18 op_sel_hi:[0,1,0]
	v_fma_mixlo_f16 v18, v18, v23, 0 op_sel_hi:[0,1,0]
	ds_write_b16 v68, v18 offset:31136
	s_waitcnt lgkmcnt(0)
	s_load_dwordx16 s[36:51], s[54:55], 0xe00
	s_load_dwordx16 s[72:87], s[54:55], 0xe40
	v_cvt_f32_f16_sdwa v18, v27 dst_sel:DWORD dst_unused:UNUSED_PAD src0_sel:WORD_1
	v_cvt_f32_f16_sdwa v22, v19 dst_sel:DWORD dst_unused:UNUSED_PAD src0_sel:WORD_1
	v_pk_mul_f32 v[26:27], v[18:19], v[14:15] op_sel_hi:[0,1]
	v_exp_f32_e32 v26, v26
	v_exp_f32_e32 v27, v27
	v_pk_mul_f32 v[114:115], v[18:19], v[16:17] op_sel_hi:[0,1]
	v_exp_f32_e32 v114, v114
	v_exp_f32_e32 v115, v115
	v_mul_f32_e32 v22, v18, v22
	v_pk_mul_f32 v[26:27], v[26:27], v[100:101]
	v_pk_fma_f32 v[26:27], v[22:23], s[56:57], v[26:27] op_sel_hi:[0, 1, 1]
	v_pk_fma_f32 v[30:31], s[88:89], v[26:27], 0 op_sel_hi:[1, 1, 0]
	v_pk_mul_f32 v[46:47], v[114:115], v[106:107]
	s_nop 0
	v_pk_fma_f32 v[100:101], v[22:23], s[58:59], v[46:47] op_sel_hi:[0, 1, 1]
	v_pk_mul_f32 v[32:33], v[18:19], v[10:11] op_sel_hi:[0,1]
	v_exp_f32_e32 v32, v32
	v_exp_f32_e32 v33, v33
	v_pk_mul_f32 v[46:47], v[18:19], v[12:13] op_sel_hi:[0,1]
	v_exp_f32_e32 v46, v46
	v_exp_f32_e32 v47, v47
	v_pk_mul_f32 v[32:33], v[32:33], v[108:109]
	v_pk_fma_f32 v[30:31], s[90:91], v[100:101], v[30:31]
	v_pk_fma_f32 v[106:107], v[22:23], s[60:61], v[32:33] op_sel_hi:[0, 1, 1]
	v_pk_mul_f32 v[32:33], v[46:47], v[110:111]
	v_pk_mul_f32 v[34:35], v[18:19], v[8:9] op_sel_hi:[0,1]
	v_pk_fma_f32 v[108:109], v[22:23], s[62:63], v[32:33] op_sel_hi:[0, 1, 1]
	v_pk_mul_f32 v[32:33], v[18:19], v[6:7] op_sel_hi:[0,1]
	v_exp_f32_e32 v32, v32
	v_exp_f32_e32 v33, v33
	v_exp_f32_e32 v34, v34
	v_exp_f32_e32 v35, v35
	v_pk_fma_f32 v[30:31], s[92:93], v[106:107], v[30:31]
	v_pk_mul_f32 v[32:33], v[32:33], v[112:113]
	v_pk_fma_f32 v[30:31], s[94:95], v[108:109], v[30:31]
	v_pk_fma_f32 v[110:111], v[22:23], s[64:65], v[32:33] op_sel_hi:[0, 1, 1]
	v_pk_mul_f32 v[32:33], v[34:35], v[102:103]
	v_pk_mul_f32 v[34:35], v[18:19], v[4:5] op_sel_hi:[0,1]
	v_pk_fma_f32 v[102:103], v[22:23], s[66:67], v[32:33] op_sel_hi:[0, 1, 1]
	v_pk_mul_f32 v[32:33], v[18:19], v[2:3] op_sel_hi:[0,1]
	v_exp_f32_e32 v32, v32
	v_exp_f32_e32 v33, v33
	v_exp_f32_e32 v34, v34
	v_exp_f32_e32 v35, v35
	v_pk_fma_f32 v[30:31], s[96:97], v[110:111], v[30:31]
	v_pk_mul_f32 v[32:33], v[32:33], v[104:105]
	v_pk_fma_f32 v[30:31], s[98:99], v[102:103], v[30:31]
	v_pk_fma_f32 v[104:105], v[22:23], s[68:69], v[32:33] op_sel_hi:[0, 1, 1]
	v_pk_mul_f32 v[32:33], v[34:35], v[98:99]
	v_pk_fma_f32 v[30:31], s[20:21], v[104:105], v[30:31]
	v_pk_fma_f32 v[98:99], v[22:23], s[70:71], v[32:33] op_sel_hi:[0, 1, 1]
	v_pk_fma_f32 v[30:31], s[22:23], v[98:99], v[30:31]
	s_nop 0
	v_add_f32_e32 v18, v30, v31
	v_fma_mix_f32 v18, v1, v19, v18 op_sel:[0,1,0] op_sel_hi:[0,1,0]
	v_fma_mixlo_f16 v18, v18, v23, 0 op_sel:[0,1,0] op_sel_hi:[0,1,0]
	ds_write_b16 v68, v18 offset:32176
	s_waitcnt lgkmcnt(0)
	s_load_dwordx16 s[56:71], s[54:55], 0xe80
	s_load_dwordx8 s[88:95], s[54:55], 0xec0
	s_load_dwordx4 s[96:99], s[54:55], 0xee0
	s_load_dwordx4 s[20:23], s[54:55], 0xef0
	v_cvt_f32_f16_e32 v18, v28
	v_cvt_f32_f16_e32 v19, v20
	v_pk_mul_f32 v[112:113], v[18:19], v[14:15] op_sel_hi:[0,1]
	v_exp_f32_e32 v112, v112
	v_exp_f32_e32 v113, v113
	v_pk_mul_f32 v[114:115], v[18:19], v[16:17] op_sel_hi:[0,1]
	v_exp_f32_e32 v114, v114
	v_exp_f32_e32 v115, v115
	v_mul_f32_e32 v22, v18, v19
	v_pk_mul_f32 v[26:27], v[112:113], v[26:27]
	v_pk_fma_f32 v[26:27], v[22:23], s[36:37], v[26:27] op_sel_hi:[0, 1, 1]
	v_pk_fma_f32 v[62:63], s[72:73], v[26:27], 0 op_sel_hi:[1, 1, 0]
	v_pk_mul_f32 v[82:83], v[114:115], v[100:101]
	s_nop 0
	v_pk_fma_f32 v[100:101], v[22:23], s[38:39], v[82:83] op_sel_hi:[0, 1, 1]
	v_pk_mul_f32 v[64:65], v[18:19], v[10:11] op_sel_hi:[0,1]
	v_exp_f32_e32 v64, v64
	v_exp_f32_e32 v65, v65
	v_pk_mul_f32 v[82:83], v[18:19], v[12:13] op_sel_hi:[0,1]
	v_exp_f32_e32 v82, v82
	v_exp_f32_e32 v83, v83
	v_pk_mul_f32 v[64:65], v[64:65], v[106:107]
	v_pk_fma_f32 v[62:63], s[74:75], v[100:101], v[62:63]
	v_pk_fma_f32 v[106:107], v[22:23], s[40:41], v[64:65] op_sel_hi:[0, 1, 1]
	v_pk_mul_f32 v[64:65], v[82:83], v[108:109]
	v_pk_mul_f32 v[70:71], v[18:19], v[8:9] op_sel_hi:[0,1]
	v_pk_fma_f32 v[108:109], v[22:23], s[42:43], v[64:65] op_sel_hi:[0, 1, 1]
	v_pk_mul_f32 v[64:65], v[18:19], v[6:7] op_sel_hi:[0,1]
	v_exp_f32_e32 v64, v64
	v_exp_f32_e32 v65, v65
	v_exp_f32_e32 v70, v70
	v_exp_f32_e32 v71, v71
	v_pk_fma_f32 v[62:63], s[76:77], v[106:107], v[62:63]
	v_pk_mul_f32 v[64:65], v[64:65], v[110:111]
	v_pk_fma_f32 v[62:63], s[78:79], v[108:109], v[62:63]
	v_pk_fma_f32 v[110:111], v[22:23], s[44:45], v[64:65] op_sel_hi:[0, 1, 1]
	v_pk_mul_f32 v[64:65], v[70:71], v[102:103]
	v_pk_fma_f32 v[62:63], s[80:81], v[110:111], v[62:63]
	v_pk_fma_f32 v[102:103], v[22:23], s[46:47], v[64:65] op_sel_hi:[0, 1, 1]
	v_pk_mul_f32 v[64:65], v[18:19], v[2:3] op_sel_hi:[0,1]
	v_exp_f32_e32 v64, v64
	v_exp_f32_e32 v65, v65
	v_pk_mul_f32 v[18:19], v[18:19], v[4:5] op_sel_hi:[0,1]
	v_exp_f32_e32 v18, v18
	v_exp_f32_e32 v19, v19
	v_pk_mul_f32 v[64:65], v[64:65], v[104:105]
	v_pk_fma_f32 v[62:63], s[82:83], v[102:103], v[62:63]
	v_pk_fma_f32 v[104:105], v[22:23], s[48:49], v[64:65] op_sel_hi:[0, 1, 1]
	v_pk_mul_f32 v[18:19], v[18:19], v[98:99]
	v_pk_fma_f32 v[62:63], s[84:85], v[104:105], v[62:63]
	v_pk_fma_f32 v[18:19], v[22:23], s[50:51], v[18:19] op_sel_hi:[0, 1, 1]
	v_pk_fma_f32 v[22:23], s[86:87], v[18:19], v[62:63]
	s_nop 0
	v_add_f32_e32 v22, v22, v23
	v_fma_mix_f32 v22, v1, v20, v22 op_sel_hi:[0,1,0]
	v_fma_mixlo_f16 v22, v22, v24, 0 op_sel_hi:[0,1,0]
	ds_write_b16 v68, v22 offset:33216
	s_waitcnt lgkmcnt(0)
	s_load_dwordx16 s[36:51], s[54:55], 0xf00
	s_load_dwordx16 s[72:87], s[54:55], 0xf40
	v_cvt_f32_f16_sdwa v22, v28 dst_sel:DWORD dst_unused:UNUSED_PAD src0_sel:WORD_1
	v_cvt_f32_f16_sdwa v23, v20 dst_sel:DWORD dst_unused:UNUSED_PAD src0_sel:WORD_1
	v_pk_mul_f32 v[98:99], v[22:23], v[14:15] op_sel_hi:[0,1]
	v_exp_f32_e32 v98, v98
	v_exp_f32_e32 v99, v99
	v_pk_mul_f32 v[112:113], v[22:23], v[16:17] op_sel_hi:[0,1]
	v_exp_f32_e32 v112, v112
	v_exp_f32_e32 v113, v113
	v_mul_f32_e32 v28, v22, v23
	v_pk_mul_f32 v[26:27], v[98:99], v[26:27]
	v_pk_fma_f32 v[26:27], v[28:29], s[56:57], v[26:27] op_sel_hi:[0, 1, 1]
	v_pk_fma_f32 v[30:31], s[88:89], v[26:27], 0 op_sel_hi:[1, 1, 0]
	v_pk_mul_f32 v[46:47], v[112:113], v[100:101]
	s_nop 0
	v_pk_fma_f32 v[98:99], v[28:29], s[58:59], v[46:47] op_sel_hi:[0, 1, 1]
	v_pk_mul_f32 v[32:33], v[22:23], v[10:11] op_sel_hi:[0,1]
	v_exp_f32_e32 v32, v32
	v_exp_f32_e32 v33, v33
	v_pk_mul_f32 v[46:47], v[22:23], v[12:13] op_sel_hi:[0,1]
	v_exp_f32_e32 v46, v46
	v_exp_f32_e32 v47, v47
	v_pk_mul_f32 v[32:33], v[32:33], v[106:107]
	v_pk_fma_f32 v[30:31], s[90:91], v[98:99], v[30:31]
	v_pk_fma_f32 v[100:101], v[28:29], s[60:61], v[32:33] op_sel_hi:[0, 1, 1]
	v_pk_mul_f32 v[32:33], v[46:47], v[108:109]
	v_pk_mul_f32 v[34:35], v[22:23], v[8:9] op_sel_hi:[0,1]
	v_pk_fma_f32 v[106:107], v[28:29], s[62:63], v[32:33] op_sel_hi:[0, 1, 1]
	v_pk_mul_f32 v[32:33], v[22:23], v[6:7] op_sel_hi:[0,1]
	v_exp_f32_e32 v32, v32
	v_exp_f32_e32 v33, v33
	v_exp_f32_e32 v34, v34
	v_exp_f32_e32 v35, v35
	v_pk_fma_f32 v[30:31], s[92:93], v[100:101], v[30:31]
	v_pk_mul_f32 v[32:33], v[32:33], v[110:111]
	v_pk_fma_f32 v[30:31], s[94:95], v[106:107], v[30:31]
	v_pk_fma_f32 v[108:109], v[28:29], s[64:65], v[32:33] op_sel_hi:[0, 1, 1]
	v_pk_mul_f32 v[32:33], v[34:35], v[102:103]
	v_pk_fma_f32 v[30:31], s[96:97], v[108:109], v[30:31]
	v_pk_fma_f32 v[102:103], v[28:29], s[66:67], v[32:33] op_sel_hi:[0, 1, 1]
	v_pk_mul_f32 v[32:33], v[22:23], v[2:3] op_sel_hi:[0,1]
	v_exp_f32_e32 v32, v32
	v_exp_f32_e32 v33, v33
	v_pk_mul_f32 v[22:23], v[22:23], v[4:5] op_sel_hi:[0,1]
	v_exp_f32_e32 v22, v22
	v_exp_f32_e32 v23, v23
	v_pk_mul_f32 v[32:33], v[32:33], v[104:105]
	v_pk_fma_f32 v[30:31], s[98:99], v[102:103], v[30:31]
	v_pk_fma_f32 v[104:105], v[28:29], s[68:69], v[32:33] op_sel_hi:[0, 1, 1]
	v_pk_mul_f32 v[18:19], v[22:23], v[18:19]
	v_pk_fma_f32 v[30:31], s[20:21], v[104:105], v[30:31]
	v_pk_fma_f32 v[18:19], v[28:29], s[70:71], v[18:19] op_sel_hi:[0, 1, 1]
	v_pk_fma_f32 v[22:23], s[22:23], v[18:19], v[30:31]
	s_nop 0
	v_add_f32_e32 v22, v22, v23
	v_fma_mix_f32 v20, v1, v20, v22 op_sel:[0,1,0] op_sel_hi:[0,1,0]
	v_fma_mixlo_f16 v20, v20, v24, 0 op_sel:[0,1,0] op_sel_hi:[0,1,0]
	ds_write_b16 v68, v20 offset:34256
	s_waitcnt lgkmcnt(0)
	s_load_dwordx16 s[56:71], s[54:55], 0xf80
	s_load_dwordx8 s[88:95], s[54:55], 0xfc0
	s_load_dwordx4 s[96:99], s[54:55], 0xfe0
	s_load_dwordx4 s[20:23], s[54:55], 0xff0
	v_cvt_f32_f16_e32 v20, v29
	v_cvt_f32_f16_e32 v22, v21
	v_pk_mul_f32 v[110:111], v[20:21], v[14:15] op_sel_hi:[0,1]
	v_exp_f32_e32 v110, v110
	v_exp_f32_e32 v111, v111
	v_pk_mul_f32 v[112:113], v[20:21], v[16:17] op_sel_hi:[0,1]
	v_exp_f32_e32 v112, v112
	v_exp_f32_e32 v113, v113
	v_mul_f32_e32 v22, v20, v22
	v_pk_mul_f32 v[26:27], v[110:111], v[26:27]
	v_pk_fma_f32 v[26:27], v[22:23], s[36:37], v[26:27] op_sel_hi:[0, 1, 1]
	v_pk_fma_f32 v[62:63], s[72:73], v[26:27], 0 op_sel_hi:[1, 1, 0]
	v_pk_mul_f32 v[82:83], v[112:113], v[98:99]
	s_nop 0
	v_pk_fma_f32 v[64:65], v[22:23], s[38:39], v[82:83] op_sel_hi:[0, 1, 1]
	v_pk_mul_f32 v[82:83], v[20:21], v[10:11] op_sel_hi:[0,1]
	v_pk_fma_f32 v[62:63], s[74:75], v[64:65], v[62:63]
	v_exp_f32_e32 v82, v82
	v_exp_f32_e32 v83, v83
	v_pk_mul_f32 v[84:85], v[20:21], v[12:13] op_sel_hi:[0,1]
	v_exp_f32_e32 v84, v84
	v_exp_f32_e32 v85, v85
	v_pk_mul_f32 v[82:83], v[82:83], v[100:101]
	s_nop 0
	v_pk_fma_f32 v[70:71], v[22:23], s[40:41], v[82:83] op_sel_hi:[0, 1, 1]
	v_pk_mul_f32 v[82:83], v[84:85], v[106:107]
	v_pk_mul_f32 v[84:85], v[20:21], v[8:9] op_sel_hi:[0,1]
	v_pk_fma_f32 v[72:73], v[22:23], s[42:43], v[82:83] op_sel_hi:[0, 1, 1]
	v_pk_mul_f32 v[82:83], v[20:21], v[6:7] op_sel_hi:[0,1]
	v_exp_f32_e32 v82, v82
	v_exp_f32_e32 v83, v83
	v_exp_f32_e32 v84, v84
	v_exp_f32_e32 v85, v85
	v_pk_fma_f32 v[62:63], s[76:77], v[70:71], v[62:63]
	v_pk_mul_f32 v[82:83], v[82:83], v[108:109]
	v_pk_fma_f32 v[62:63], s[78:79], v[72:73], v[62:63]
	v_pk_fma_f32 v[74:75], v[22:23], s[44:45], v[82:83] op_sel_hi:[0, 1, 1]
	v_pk_mul_f32 v[82:83], v[84:85], v[102:103]
	v_pk_mul_f32 v[84:85], v[20:21], v[4:5] op_sel_hi:[0,1]
	v_pk_fma_f32 v[76:77], v[22:23], s[46:47], v[82:83] op_sel_hi:[0, 1, 1]
	v_pk_mul_f32 v[82:83], v[20:21], v[2:3] op_sel_hi:[0,1]
	v_exp_f32_e32 v82, v82
	v_exp_f32_e32 v83, v83
	v_exp_f32_e32 v84, v84
	v_exp_f32_e32 v85, v85
	v_pk_fma_f32 v[62:63], s[80:81], v[74:75], v[62:63]
	v_pk_mul_f32 v[82:83], v[82:83], v[104:105]
	v_pk_fma_f32 v[62:63], s[82:83], v[76:77], v[62:63]
	v_pk_fma_f32 v[78:79], v[22:23], s[48:49], v[82:83] op_sel_hi:[0, 1, 1]
	v_pk_mul_f32 v[18:19], v[84:85], v[18:19]
	v_pk_fma_f32 v[62:63], s[84:85], v[78:79], v[62:63]
	v_pk_fma_f32 v[18:19], v[22:23], s[50:51], v[18:19] op_sel_hi:[0, 1, 1]
	v_pk_fma_f32 v[22:23], s[86:87], v[18:19], v[62:63]
	s_nop 0
	v_add_f32_e32 v20, v22, v23
	v_fma_mix_f32 v20, v1, v21, v20 op_sel_hi:[0,1,0]
	v_fma_mixlo_f16 v20, v20, v25, 0 op_sel_hi:[0,1,0]
	ds_write_b16 v68, v20 offset:35296
	v_cvt_f32_f16_sdwa v20, v29 dst_sel:DWORD dst_unused:UNUSED_PAD src0_sel:WORD_1
	v_cvt_f32_f16_sdwa v22, v21 dst_sel:DWORD dst_unused:UNUSED_PAD src0_sel:WORD_1
	v_pk_mul_f32 v[14:15], v[20:21], v[14:15] op_sel_hi:[0,1]
	v_exp_f32_e32 v14, v14
	v_exp_f32_e32 v15, v15
	v_pk_mul_f32 v[16:17], v[20:21], v[16:17] op_sel_hi:[0,1]
	v_exp_f32_e32 v16, v16
	v_exp_f32_e32 v17, v17
	v_pk_mul_f32 v[10:11], v[20:21], v[10:11] op_sel_hi:[0,1]
	v_exp_f32_e32 v10, v10
	v_exp_f32_e32 v11, v11
	v_pk_mul_f32 v[12:13], v[20:21], v[12:13] op_sel_hi:[0,1]
	v_exp_f32_e32 v12, v12
	v_exp_f32_e32 v13, v13
	v_pk_mul_f32 v[6:7], v[20:21], v[6:7] op_sel_hi:[0,1]
	v_mul_f32_e32 v22, v20, v22
	v_pk_mul_f32 v[14:15], v[14:15], v[26:27]
	v_exp_f32_e32 v6, v6
	v_exp_f32_e32 v7, v7
	v_pk_mul_f32 v[8:9], v[20:21], v[8:9] op_sel_hi:[0,1]
	v_pk_fma_f32 v[14:15], v[22:23], s[56:57], v[14:15] op_sel_hi:[0, 1, 1]
	v_pk_mul_f32 v[16:17], v[16:17], v[64:65]
	v_exp_f32_e32 v8, v8
	v_exp_f32_e32 v9, v9
	v_pk_mul_f32 v[2:3], v[20:21], v[2:3] op_sel_hi:[0,1]
	v_pk_fma_f32 v[14:15], s[88:89], v[14:15], 0 op_sel_hi:[1, 1, 0]
	v_pk_fma_f32 v[16:17], v[22:23], s[58:59], v[16:17] op_sel_hi:[0, 1, 1]
	v_pk_mul_f32 v[10:11], v[10:11], v[70:71]
	v_exp_f32_e32 v2, v2
	v_exp_f32_e32 v3, v3
	v_pk_mul_f32 v[4:5], v[20:21], v[4:5] op_sel_hi:[0,1]
	v_pk_fma_f32 v[14:15], s[90:91], v[16:17], v[14:15]
	v_pk_fma_f32 v[10:11], v[22:23], s[60:61], v[10:11] op_sel_hi:[0, 1, 1]
	v_pk_mul_f32 v[12:13], v[12:13], v[72:73]
	v_exp_f32_e32 v4, v4
	v_exp_f32_e32 v5, v5
	v_pk_fma_f32 v[10:11], s[92:93], v[10:11], v[14:15]
	v_pk_fma_f32 v[12:13], v[22:23], s[62:63], v[12:13] op_sel_hi:[0, 1, 1]
	v_pk_mul_f32 v[6:7], v[6:7], v[74:75]
	v_pk_fma_f32 v[10:11], s[94:95], v[12:13], v[10:11]
	v_pk_fma_f32 v[6:7], v[22:23], s[64:65], v[6:7] op_sel_hi:[0, 1, 1]
	v_pk_mul_f32 v[8:9], v[8:9], v[76:77]
	v_pk_fma_f32 v[6:7], s[96:97], v[6:7], v[10:11]
	v_pk_fma_f32 v[8:9], v[22:23], s[66:67], v[8:9] op_sel_hi:[0, 1, 1]
	v_pk_mul_f32 v[2:3], v[2:3], v[78:79]
	v_pk_fma_f32 v[6:7], s[98:99], v[8:9], v[6:7]
	v_pk_fma_f32 v[2:3], v[22:23], s[68:69], v[2:3] op_sel_hi:[0, 1, 1]
	v_pk_mul_f32 v[4:5], v[4:5], v[18:19]
	v_pk_fma_f32 v[2:3], s[20:21], v[2:3], v[6:7]
	v_pk_fma_f32 v[4:5], v[22:23], s[70:71], v[4:5] op_sel_hi:[0, 1, 1]
	v_pk_fma_f32 v[2:3], s[22:23], v[4:5], v[2:3]
	s_nop 0
	v_add_f32_e32 v2, v2, v3
	v_fma_mix_f32 v1, v1, v21, v2 op_sel:[0,1,0] op_sel_hi:[0,1,0]
	v_fma_mixlo_f16 v1, v1, v25, 0 op_sel:[0,1,0] op_sel_hi:[0,1,0]
	ds_write_b16 v68, v1 offset:36336
	v_lshlrev_b32_e32 v1, 9, v0
	v_and_b32_e32 v2, 0x38000, v1
	v_mov_b32_e32 v3, v67
	v_and_b32_e32 v1, 63, v0
	s_bfe_u32 s14, s2, 0x40003
	v_lshl_add_u64 v[2:3], s[18:19], 0, v[2:3]
	v_lshlrev_b32_e32 v58, 4, v1
	v_mov_b32_e32 v59, v67
	s_lshl_b32 s13, s14, 6
	v_lshl_add_u64 v[20:21], v[2:3], 0, v[58:59]
	s_lshl_b32 s26, s14, 10
	s_add_i32 s12, s13, 64
	v_lshl_add_u64 v[2:3], v[20:21], 0, s[26:27]
	s_and_b32 s15, s12, 0x3c0
	v_add_co_u32_e32 v4, vcc, s52, v2
	s_lshl_b32 s26, s15, 4
	s_lshl_b32 s12, s12, 4
	v_addc_co_u32_e32 v5, vcc, 0, v3, vcc
	global_load_dwordx4 v[28:31], v[2:3], off
	global_load_dwordx4 v[32:35], v[4:5], off
	v_lshl_add_u64 v[2:3], v[20:21], 0, s[26:27]
	s_or_b32 s26, s12, 0x4000
	s_add_i32 s12, s13, 0x80
	s_and_b32 s15, s12, 0x3c0
	v_lshl_add_u64 v[4:5], v[20:21], 0, s[26:27]
	s_lshl_b32 s26, s15, 4
	s_lshl_b32 s12, s12, 4
	global_load_dwordx4 v[36:39], v[2:3], off
	global_load_dwordx4 v[40:43], v[4:5], off
	v_lshl_add_u64 v[2:3], v[20:21], 0, s[26:27]
	s_or_b32 s26, s12, 0x4000
	s_add_i32 s12, s13, 0xc0
	s_and_b32 s15, s12, 0x3c0
	v_lshl_add_u64 v[4:5], v[20:21], 0, s[26:27]
	s_lshl_b32 s26, s15, 4
	s_lshl_b32 s12, s12, 4
	global_load_dwordx4 v[44:47], v[2:3], off
	global_load_dwordx4 v[48:51], v[4:5], off
	v_lshl_add_u64 v[2:3], v[20:21], 0, s[26:27]
	s_or_b32 s26, s12, 0x4000
	s_add_i32 s12, s13, 0x100
	s_and_b32 s15, s12, 0x3c0
	v_lshl_add_u64 v[4:5], v[20:21], 0, s[26:27]
	s_lshl_b32 s26, s15, 4
	s_lshl_b32 s12, s12, 4
	global_load_dwordx4 v[52:55], v[2:3], off
	global_load_dwordx4 v[60:63], v[4:5], off
	v_lshl_add_u64 v[2:3], v[20:21], 0, s[26:27]
	s_or_b32 s26, s12, 0x4000
	s_add_i32 s12, s13, 0x140
	s_and_b32 s15, s12, 0x3c0
	v_lshl_add_u64 v[4:5], v[20:21], 0, s[26:27]
	s_lshl_b32 s26, s15, 4
	s_lshl_b32 s12, s12, 4
	global_load_dwordx4 v[68:71], v[2:3], off
	global_load_dwordx4 v[72:75], v[4:5], off
	v_lshl_add_u64 v[2:3], v[20:21], 0, s[26:27]
	s_or_b32 s26, s12, 0x4000
	s_add_i32 s12, s13, 0x180
	s_and_b32 s15, s12, 0x3c0
	v_lshl_add_u64 v[4:5], v[20:21], 0, s[26:27]
	s_lshl_b32 s26, s15, 4
	s_lshl_b32 s12, s12, 4
	global_load_dwordx4 v[76:79], v[2:3], off
	global_load_dwordx4 v[82:85], v[4:5], off
	v_lshl_add_u64 v[2:3], v[20:21], 0, s[26:27]
	s_or_b32 s26, s12, 0x4000
	s_add_i32 s12, s13, 0x1c0
	s_and_b32 s15, s12, 0x3c0
	v_lshl_add_u64 v[4:5], v[20:21], 0, s[26:27]
	s_lshl_b32 s26, s15, 4
	s_lshl_b32 s12, s12, 4
	v_lshl_add_u64 v[18:19], v[20:21], 0, s[26:27]
	s_or_b32 s26, s12, 0x4000
	s_xor_b32 s15, s13, 0x200
	v_lshl_add_u64 v[22:23], v[20:21], 0, s[26:27]
	s_lshl_b32 s26, s15, 4
	global_load_dwordx4 v[14:17], v[2:3], off
	global_load_dwordx4 v[10:13], v[4:5], off
	global_load_dwordx4 v[6:9], v[18:19], off
	s_nop 0
	global_load_dwordx4 v[2:5], v[22:23], off
	v_lshl_add_u64 v[18:19], v[20:21], 0, s[26:27]
	v_add_co_u32_e32 v22, vcc, s52, v18
	s_waitcnt lgkmcnt(0)
	s_barrier
	v_addc_co_u32_e32 v23, vcc, 0, v19, vcc
	global_load_dwordx4 v[86:89], v[18:19], off
	global_load_dwordx4 v[90:93], v[22:23], off
	v_lshrrev_b32_e32 v118, 6, v0
	v_lshlrev_b32_e32 v22, 7, v118
	v_mov_b32_e32 v23, v67
	v_and_b32_e32 v81, 15, v0
	v_lshl_add_u64 v[24:25], s[4:5], 0, v[22:23]
	v_and_b32_e32 v18, 48, v0
	v_mov_b32_e32 v19, v67
	s_movk_i32 s12, 0x410
	v_lshl_add_u64 v[56:57], v[24:25], 0, v[18:19]
	v_mad_u32_u24 v19, v81, s12, v18
	v_add_u32_e32 v23, s13, v19
	ds_read_b128 v[94:97], v23 offset:4096
	ds_read_b128 v[98:101], v23 offset:20736
	v_or_b32_e32 v26, s28, v81
	v_mov_b32_e32 v27, v67
	v_lshlrev_b64 v[24:25], 10, v[26:27]
	v_or_b32_e32 v26, 16, v26
	v_lshlrev_b64 v[26:27], 10, v[26:27]
	v_lshrrev_b32_e32 v23, 1, v0
	v_lshl_add_u64 v[24:25], v[56:57], 0, v[24:25]
	v_lshl_add_u64 v[26:27], v[56:57], 0, v[26:27]
	v_and_b32_e32 v80, 24, v23
	s_lshl_b32 s14, s14, 5
	s_setprio 1
	s_waitcnt vmcnt(17) lgkmcnt(1)
	v_mfma_f32_16x16x32_f16 v[102:105], v[28:31], v[94:97], 0
	s_waitcnt lgkmcnt(0)
	v_mfma_f32_16x16x32_f16 v[28:31], v[28:31], v[98:101], 0
	s_waitcnt vmcnt(16)
	v_mfma_f32_16x16x32_f16 v[94:97], v[32:35], v[94:97], 0
	v_mfma_f32_16x16x32_f16 v[32:35], v[32:35], v[98:101], 0
	s_setprio 0
	s_add_i32 s16, s13, 0x240
	s_and_b32 s17, s16, 0x3c0
	s_lshl_b32 s26, s17, 4
	s_lshl_b32 s16, s16, 4
	v_lshl_add_u64 v[56:57], v[20:21], 0, s[26:27]
	s_or_b32 s26, s16, 0x4000
	v_lshl_add_u64 v[64:65], v[20:21], 0, s[26:27]
	global_load_dwordx4 v[98:101], v[56:57], off
	global_load_dwordx4 v[106:109], v[64:65], off
	s_add_i32 s16, s14, 32
	s_and_b32 s16, s16, 0x1e0
	v_lshl_add_u32 v23, s16, 1, v19
	ds_read_b128 v[110:113], v23 offset:4096
	ds_read_b128 v[114:117], v23 offset:20736
	s_setprio 1
	s_waitcnt vmcnt(17) lgkmcnt(1)
	v_mfma_f32_16x16x32_f16 v[102:105], v[36:39], v[110:113], v[102:105]
	s_waitcnt lgkmcnt(0)
	v_mfma_f32_16x16x32_f16 v[28:31], v[36:39], v[114:117], v[28:31]
	s_waitcnt vmcnt(16)
	v_mfma_f32_16x16x32_f16 v[36:39], v[40:43], v[110:113], v[94:97]
	v_mfma_f32_16x16x32_f16 v[32:35], v[40:43], v[114:117], v[32:35]
	s_setprio 0
	s_add_i32 s16, s13, 0x280
	s_and_b32 s17, s16, 0x3c0
	s_lshl_b32 s26, s17, 4
	s_lshl_b32 s16, s16, 4
	v_lshl_add_u64 v[56:57], v[20:21], 0, s[26:27]
	s_or_b32 s26, s16, 0x4000
	v_lshl_add_u64 v[64:65], v[20:21], 0, s[26:27]
	global_load_dwordx4 v[40:43], v[56:57], off
	global_load_dwordx4 v[94:97], v[64:65], off
	s_add_i32 s16, s14, 64
	s_and_b32 s16, s16, 0x1e0
	v_lshl_add_u32 v23, s16, 1, v19
	ds_read_b128 v[110:113], v23 offset:4096
	ds_read_b128 v[114:117], v23 offset:20736
	s_setprio 1
	s_waitcnt vmcnt(17) lgkmcnt(1)
	v_mfma_f32_16x16x32_f16 v[102:105], v[44:47], v[110:113], v[102:105]
	s_waitcnt lgkmcnt(0)
	v_mfma_f32_16x16x32_f16 v[28:31], v[44:47], v[114:117], v[28:31]
	s_waitcnt vmcnt(16)
	v_mfma_f32_16x16x32_f16 v[36:39], v[48:51], v[110:113], v[36:39]
	v_mfma_f32_16x16x32_f16 v[32:35], v[48:51], v[114:117], v[32:35]
	s_setprio 0
	s_add_i32 s16, s13, 0x2c0
	s_and_b32 s17, s16, 0x3c0
	s_lshl_b32 s26, s17, 4
	s_lshl_b32 s16, s16, 4
	v_lshl_add_u64 v[56:57], v[20:21], 0, s[26:27]
	s_or_b32 s26, s16, 0x4000
	v_lshl_add_u64 v[64:65], v[20:21], 0, s[26:27]
	global_load_dwordx4 v[44:47], v[56:57], off
	global_load_dwordx4 v[48:51], v[64:65], off
	s_add_i32 s16, s14, 0x60
	s_and_b32 s16, s16, 0x1e0
	v_lshl_add_u32 v23, s16, 1, v19
	ds_read_b128 v[110:113], v23 offset:4096
	ds_read_b128 v[114:117], v23 offset:20736
	s_setprio 1
	s_waitcnt vmcnt(17) lgkmcnt(1)
	v_mfma_f32_16x16x32_f16 v[102:105], v[52:55], v[110:113], v[102:105]
	s_waitcnt lgkmcnt(0)
	v_mfma_f32_16x16x32_f16 v[28:31], v[52:55], v[114:117], v[28:31]
	s_waitcnt vmcnt(16)
	v_mfma_f32_16x16x32_f16 v[36:39], v[60:63], v[110:113], v[36:39]
	v_mfma_f32_16x16x32_f16 v[32:35], v[60:63], v[114:117], v[32:35]
	s_setprio 0
	s_add_i32 s16, s13, 0x300
	s_and_b32 s17, s16, 0x3c0
	s_lshl_b32 s26, s17, 4
	s_lshl_b32 s16, s16, 4
	v_lshl_add_u64 v[56:57], v[20:21], 0, s[26:27]
	s_or_b32 s26, s16, 0x4000
	v_lshl_add_u64 v[64:65], v[20:21], 0, s[26:27]
	global_load_dwordx4 v[52:55], v[56:57], off
	global_load_dwordx4 v[60:63], v[64:65], off
	s_add_i32 s16, s14, 0x80
	s_and_b32 s16, s16, 0x1e0
	v_lshl_add_u32 v23, s16, 1, v19
	ds_read_b128 v[110:113], v23 offset:4096
	ds_read_b128 v[114:117], v23 offset:20736
	s_setprio 1
	s_waitcnt vmcnt(17) lgkmcnt(1)
	v_mfma_f32_16x16x32_f16 v[102:105], v[68:71], v[110:113], v[102:105]
	s_waitcnt lgkmcnt(0)
	v_mfma_f32_16x16x32_f16 v[28:31], v[68:71], v[114:117], v[28:31]
	s_waitcnt vmcnt(16)
	v_mfma_f32_16x16x32_f16 v[36:39], v[72:75], v[110:113], v[36:39]
	v_mfma_f32_16x16x32_f16 v[32:35], v[72:75], v[114:117], v[32:35]
	s_setprio 0
	s_add_i32 s16, s13, 0x340
	s_and_b32 s17, s16, 0x3c0
	s_lshl_b32 s26, s17, 4
	s_lshl_b32 s16, s16, 4
	v_lshl_add_u64 v[56:57], v[20:21], 0, s[26:27]
	s_or_b32 s26, s16, 0x4000
	v_lshl_add_u64 v[64:65], v[20:21], 0, s[26:27]
	global_load_dwordx4 v[68:71], v[56:57], off
	global_load_dwordx4 v[72:75], v[64:65], off
	s_add_i32 s16, s14, 0xa0
	s_and_b32 s16, s16, 0x1e0
	v_lshl_add_u32 v23, s16, 1, v19
	ds_read_b128 v[110:113], v23 offset:4096
	ds_read_b128 v[114:117], v23 offset:20736
	s_setprio 1
	s_waitcnt vmcnt(17) lgkmcnt(1)
	v_mfma_f32_16x16x32_f16 v[102:105], v[76:79], v[110:113], v[102:105]
	s_waitcnt lgkmcnt(0)
	v_mfma_f32_16x16x32_f16 v[28:31], v[76:79], v[114:117], v[28:31]
	s_waitcnt vmcnt(16)
	v_mfma_f32_16x16x32_f16 v[36:39], v[82:85], v[110:113], v[36:39]
	v_mfma_f32_16x16x32_f16 v[32:35], v[82:85], v[114:117], v[32:35]
	s_setprio 0
	s_add_i32 s16, s13, 0x380
	s_and_b32 s17, s16, 0x3c0
	s_lshl_b32 s26, s17, 4
	s_lshl_b32 s16, s16, 4
	v_lshl_add_u64 v[56:57], v[20:21], 0, s[26:27]
	s_or_b32 s26, s16, 0x4000
	v_lshl_add_u64 v[64:65], v[20:21], 0, s[26:27]
	global_load_dwordx4 v[76:79], v[56:57], off
	global_load_dwordx4 v[82:85], v[64:65], off
	s_add_i32 s16, s14, 0xc0
	s_and_b32 s16, s16, 0x1e0
	v_lshl_add_u32 v23, s16, 1, v19
	ds_read_b128 v[110:113], v23 offset:4096
	ds_read_b128 v[114:117], v23 offset:20736
	s_setprio 1
	s_waitcnt vmcnt(17) lgkmcnt(1)
	v_mfma_f32_16x16x32_f16 v[102:105], v[14:17], v[110:113], v[102:105]
	s_waitcnt lgkmcnt(0)
	v_mfma_f32_16x16x32_f16 v[14:17], v[14:17], v[114:117], v[28:31]
	s_waitcnt vmcnt(16)
	v_mfma_f32_16x16x32_f16 v[28:31], v[10:13], v[110:113], v[36:39]
	v_mfma_f32_16x16x32_f16 v[10:13], v[10:13], v[114:117], v[32:35]
	s_setprio 0
	s_addk_i32 s13, 0x3c0
	s_and_b32 s16, s13, 0x3c0
	s_lshl_b32 s26, s16, 4
	s_lshl_b32 s13, s13, 4
	v_lshl_add_u64 v[56:57], v[20:21], 0, s[26:27]
	s_or_b32 s26, s13, 0x4000
	v_lshl_add_u64 v[20:21], v[20:21], 0, s[26:27]
	global_load_dwordx4 v[32:35], v[56:57], off
	global_load_dwordx4 v[36:39], v[20:21], off
	s_add_i32 s13, s14, 0xe0
	s_and_b32 s13, s13, 0x1e0
	v_lshl_add_u32 v20, s13, 1, v19
	ds_read_b128 v[110:113], v20 offset:4096
	ds_read_b128 v[114:117], v20 offset:20736
	s_setprio 1
	s_waitcnt vmcnt(17) lgkmcnt(1)
	v_mfma_f32_16x16x32_f16 v[102:105], v[6:9], v[110:113], v[102:105]
	s_waitcnt lgkmcnt(0)
	v_mfma_f32_16x16x32_f16 v[6:9], v[6:9], v[114:117], v[14:17]
	s_waitcnt vmcnt(16)
	v_mfma_f32_16x16x32_f16 v[14:17], v[2:5], v[110:113], v[28:31]
	v_mfma_f32_16x16x32_f16 v[2:5], v[2:5], v[114:117], v[10:13]
	s_setprio 0
	v_add_u32_e32 v20, s15, v19
	s_nop 0
	ds_read_b128 v[10:13], v20 offset:4096
	ds_read_b128 v[28:31], v20 offset:20736
	s_setprio 1
	s_waitcnt vmcnt(15) lgkmcnt(1)
	v_mfma_f32_16x16x32_f16 v[102:105], v[86:89], v[10:13], v[102:105]
	s_waitcnt lgkmcnt(0)
	v_mfma_f32_16x16x32_f16 v[6:9], v[86:89], v[28:31], v[6:9]
	s_waitcnt vmcnt(14)
	v_mfma_f32_16x16x32_f16 v[10:13], v[90:93], v[10:13], v[14:17]
	v_mfma_f32_16x16x32_f16 v[2:5], v[90:93], v[28:31], v[2:5]
	s_setprio 0
	s_add_i32 s13, s14, 0x120
	s_and_b32 s13, s13, 0x1e0
	v_lshl_add_u32 v20, s13, 1, v19
	ds_read_b128 v[14:17], v20 offset:4096
	ds_read_b128 v[28:31], v20 offset:20736
	s_setprio 1
	s_waitcnt vmcnt(13) lgkmcnt(1)
	v_mfma_f32_16x16x32_f16 v[86:89], v[98:101], v[14:17], v[102:105]
	s_waitcnt lgkmcnt(0)
	v_mfma_f32_16x16x32_f16 v[6:9], v[98:101], v[28:31], v[6:9]
	s_waitcnt vmcnt(12)
	v_mfma_f32_16x16x32_f16 v[10:13], v[106:109], v[14:17], v[10:13]
	v_mfma_f32_16x16x32_f16 v[2:5], v[106:109], v[28:31], v[2:5]
	s_setprio 0
	s_add_i32 s13, s14, 0x140
	s_and_b32 s13, s13, 0x1e0
	v_lshl_add_u32 v20, s13, 1, v19
	ds_read_b128 v[14:17], v20 offset:4096
	ds_read_b128 v[28:31], v20 offset:20736
	s_setprio 1
	s_waitcnt vmcnt(11) lgkmcnt(1)
	v_mfma_f32_16x16x32_f16 v[86:89], v[40:43], v[14:17], v[86:89]
	s_waitcnt lgkmcnt(0)
	v_mfma_f32_16x16x32_f16 v[6:9], v[40:43], v[28:31], v[6:9]
	s_waitcnt vmcnt(10)
	v_mfma_f32_16x16x32_f16 v[10:13], v[94:97], v[14:17], v[10:13]
	v_mfma_f32_16x16x32_f16 v[2:5], v[94:97], v[28:31], v[2:5]
	s_setprio 0
	s_add_i32 s13, s14, 0x160
	s_and_b32 s13, s13, 0x1e0
	v_lshl_add_u32 v20, s13, 1, v19
	ds_read_b128 v[14:17], v20 offset:4096
	ds_read_b128 v[28:31], v20 offset:20736
	s_setprio 1
	s_waitcnt vmcnt(9) lgkmcnt(1)
	v_mfma_f32_16x16x32_f16 v[40:43], v[44:47], v[14:17], v[86:89]
	s_waitcnt lgkmcnt(0)
	v_mfma_f32_16x16x32_f16 v[6:9], v[44:47], v[28:31], v[6:9]
	s_waitcnt vmcnt(8)
	v_mfma_f32_16x16x32_f16 v[10:13], v[48:51], v[14:17], v[10:13]
	v_mfma_f32_16x16x32_f16 v[2:5], v[48:51], v[28:31], v[2:5]
	s_setprio 0
	s_add_i32 s13, s14, 0x180
	s_and_b32 s13, s13, 0x1e0
	v_lshl_add_u32 v20, s13, 1, v19
	ds_read_b128 v[14:17], v20 offset:4096
	ds_read_b128 v[28:31], v20 offset:20736
	s_setprio 1
	s_waitcnt vmcnt(7) lgkmcnt(1)
	v_mfma_f32_16x16x32_f16 v[40:43], v[52:55], v[14:17], v[40:43]
	s_waitcnt lgkmcnt(0)
	v_mfma_f32_16x16x32_f16 v[6:9], v[52:55], v[28:31], v[6:9]
	s_waitcnt vmcnt(6)
	v_mfma_f32_16x16x32_f16 v[10:13], v[60:63], v[14:17], v[10:13]
	v_mfma_f32_16x16x32_f16 v[2:5], v[60:63], v[28:31], v[2:5]
	s_setprio 0
	s_add_i32 s13, s14, 0x1a0
	s_and_b32 s13, s13, 0x1e0
	v_lshl_add_u32 v20, s13, 1, v19
	ds_read_b128 v[14:17], v20 offset:4096
	ds_read_b128 v[28:31], v20 offset:20736
	s_setprio 1
	s_waitcnt vmcnt(5) lgkmcnt(1)
	v_mfma_f32_16x16x32_f16 v[40:43], v[68:71], v[14:17], v[40:43]
	s_waitcnt lgkmcnt(0)
	v_mfma_f32_16x16x32_f16 v[6:9], v[68:71], v[28:31], v[6:9]
	s_waitcnt vmcnt(4)
	v_mfma_f32_16x16x32_f16 v[10:13], v[72:75], v[14:17], v[10:13]
	v_mfma_f32_16x16x32_f16 v[2:5], v[72:75], v[28:31], v[2:5]
	s_setprio 0
	s_add_i32 s13, s14, 0x1c0
	s_and_b32 s13, s13, 0x1e0
	v_lshl_add_u32 v20, s13, 1, v19
	ds_read_b128 v[14:17], v20 offset:4096
	ds_read_b128 v[28:31], v20 offset:20736
	s_setprio 1
	s_waitcnt vmcnt(3) lgkmcnt(1)
	v_mfma_f32_16x16x32_f16 v[40:43], v[76:79], v[14:17], v[40:43]
	s_waitcnt lgkmcnt(0)
	v_mfma_f32_16x16x32_f16 v[6:9], v[76:79], v[28:31], v[6:9]
	s_waitcnt vmcnt(2)
	v_mfma_f32_16x16x32_f16 v[10:13], v[82:85], v[14:17], v[10:13]
	v_mfma_f32_16x16x32_f16 v[2:5], v[82:85], v[28:31], v[2:5]
	s_setprio 0
	s_addk_i32 s14, 0x1e0
	s_and_b32 s13, s14, 0x1e0
	v_lshl_add_u32 v20, s13, 1, v19
	ds_read_b128 v[14:17], v20 offset:4096
	ds_read_b128 v[28:31], v20 offset:20736
	s_setprio 1
	s_waitcnt vmcnt(1) lgkmcnt(1)
	v_mfma_f32_16x16x32_f16 v[40:43], v[32:35], v[14:17], v[40:43]
	s_waitcnt lgkmcnt(0)
	v_mfma_f32_16x16x32_f16 v[6:9], v[32:35], v[28:31], v[6:9]
	s_waitcnt vmcnt(0)
	v_mfma_f32_16x16x32_f16 v[10:13], v[36:39], v[14:17], v[10:13]
	v_mfma_f32_16x16x32_f16 v[2:5], v[36:39], v[28:31], v[2:5]
	s_setprio 0
	v_add_u32_e32 v19, v19, v22
	v_lshlrev_b32_e32 v20, 15, v118
	v_mov_b32_e32 v21, v67
	s_bfe_u32 s22, s2, 0x30003
	v_lshl_add_u64 v[20:21], s[10:11], 0, v[20:21]
	s_lshl_b32 s26, s22, 10
	v_lshl_add_u64 v[64:65], v[20:21], 0, v[58:59]
	v_lshl_add_u64 v[52:53], v[64:65], 0, s[26:27]
	v_add_co_u32_e32 v76, vcc, s29, v52
	s_lshl_b32 s53, s22, 6
	s_nop 0
	v_addc_co_u32_e32 v77, vcc, 0, v53, vcc
	s_mov_b32 s14, 0x14000
	v_mov_b32_e32 v22, 0x14000
	v_mul_u32_u24_e32 v23, 0x210, v81
	s_add_i32 s38, s53, 64
	v_lshlrev_b32_e32 v83, 2, v118
	s_movk_i32 s16, 0x1040
	s_movk_i32 s18, 0x840
	v_lshl_or_b32 v1, v1, 3, v22
	v_add3_u32 v84, v23, v18, s14
	s_and_b32 s14, s38, 0x1c0
	s_movk_i32 s20, 0x210
	s_mov_b32 s19, s27
	v_mad_u32_u24 v56, v118, s16, v58
	v_or_b32_e32 v22, 1, v83
	v_mad_u32_u24 v98, v118, s18, v1
	s_lshl_b32 s18, s14, 4
	v_mad_u32_u24 v99, v22, s12, v58
	v_mad_u32_u24 v85, v22, s20, v1
	v_lshl_add_u64 v[54:55], v[64:65], 0, s[18:19]
	s_add_i32 s12, s53, 0xc0
	s_and_b32 s2, s3, 0x7ffffff
	s_lshl_b32 s3, s22, 5
	s_and_b32 s39, s12, 0x1c0
	s_lshl_b32 s14, s39, 4
	s_add_i32 s39, s3, 32
	s_and_b32 s39, s39, 0xe0
	v_lshl_add_u32 v82, s39, 1, v84
	s_add_i32 s11, s53, 0x80
	s_lshl_b32 s16, s38, 4
	s_mov_b32 s21, s27
	s_and_b32 s30, s11, 0x1c0
	s_lshl_b32 s11, s11, 4
	s_or_b32 s20, s16, 0x2000
	s_mov_b32 s23, s27
	s_mov_b32 s31, s27
	s_mov_b32 s35, s27
	s_or_b32 s22, s16, 0x6000
	s_lshl_b32 s30, s30, 4
	s_or_b32 s34, s11, 0x2000
	v_lshl_add_u64 v[26:27], v[64:65], 0, s[20:21]
	v_lshl_add_u64 v[28:29], v[64:65], 0, s[22:23]
	v_lshl_add_u64 v[30:31], v[64:65], 0, s[30:31]
	v_lshl_add_u64 v[32:33], v[64:65], 0, s[34:35]
	s_mov_b64 s[40:41], 0x40000
	v_lshl_add_u64 v[60:61], v[64:65], 0, s[40:41]
	s_mov_b32 s37, s27
	s_or_b32 s36, s11, 0x6000
	v_lshl_add_u64 v[74:75], v[64:65], 0, s[36:37]
	s_mov_b32 s15, s27
	s_lshl_b32 s12, s12, 4
	v_lshl_add_u64 v[70:71], v[64:65], 0, s[14:15]
	s_mov_b32 s17, s27
	s_or_b32 s16, s12, 0x2000
	s_mov_b32 s13, s27
	s_or_b32 s12, s12, 0x6000
	v_lshl_add_u64 v[72:73], v[64:65], 0, s[16:17]
	v_lshl_add_u64 v[68:69], v[64:65], 0, s[12:13]
	v_add_u32_e32 v1, s53, v84
	s_xor_b32 s10, s26, 0x1000
	s_mov_b32 s11, s27
	s_mov_b32 s49, s27
	s_mov_b32 s51, s27
	s_mov_b32 s47, s27
	v_pk_add_f32 v[14:15], v[180:181], v[40:41]
	v_pk_add_f32 v[16:17], v[182:183], v[42:43]
	v_pk_add_f32 v[10:11], v[184:185], v[10:11]
	v_pk_add_f32 v[12:13], v[186:187], v[12:13]
	v_pk_add_f32 v[6:7], v[188:189], v[6:7]
	v_pk_add_f32 v[8:9], v[190:191], v[8:9]
	v_pk_add_f32 v[2:3], v[192:193], v[2:3]
	v_pk_add_f32 v[4:5], v[194:195], v[4:5]
	ds_write_b128 v19, v[14:17] offset:37376
	ds_write_b128 v19, v[10:13] offset:37440
	ds_write_b128 v19, v[6:9] offset:54016
	ds_write_b128 v19, v[2:5] offset:54080
	v_mov_b64_e32 v[34:35], v[204:205]
	v_mov_b64_e32 v[36:37], v[206:207]
	v_mov_b64_e32 v[38:39], v[208:209]
	v_mov_b64_e32 v[40:41], v[210:211]
	v_add_co_u32_e32 v2, vcc, s52, v52
	s_waitcnt lgkmcnt(0)
	s_nop 0
	v_addc_co_u32_e32 v3, vcc, 0, v53, vcc
	v_add_co_u32_e32 v4, vcc, s33, v52
	s_barrier
	s_nop 0
	v_addc_co_u32_e32 v5, vcc, 0, v53, vcc
	global_load_dwordx4 v[14:17], v[2:3], off
	global_load_dwordx4 v[18:21], v[4:5], off
	global_load_dwordx4 v[22:25], v[52:53], off
	global_load_dwordx4 v[10:13], v[54:55], off
	ds_read_b128 v[2:5], v56 offset:37376
	ds_read_b128 v[6:9], v99 offset:37376
	v_add_co_u32_e32 v78, vcc, s52, v54
	s_mov_b32 s43, s27
	s_waitcnt lgkmcnt(1)
	v_add_f32_e32 v42, v2, v3
	v_add_f32_e32 v42, v42, v4
	v_add_f32_e32 v42, v42, v5
	v_addc_co_u32_e32 v79, vcc, 0, v55, vcc
	s_nop 0
	v_add_f32_dpp v42, v42, v42 quad_perm:[1,0,3,2] row_mask:0xf bank_mask:0xf bound_ctrl:1
	s_mov_b32 s45, s27
	s_mov_b32 s41, s27
	v_add_f32_dpp v42, v42, v42 quad_perm:[2,3,0,1] row_mask:0xf bank_mask:0xf bound_ctrl:1
	v_lshl_add_u64 v[62:63], v[64:65], 0, s[10:11]
	v_lshl_add_u64 v[58:59], s[4:5], 0, v[58:59]
	v_add_f32_dpp v42, v42, v42 row_half_mirror row_mask:0xf bank_mask:0xf bound_ctrl:1
	v_lshl_add_u64 v[152:153], v[60:61], 0, s[26:27]
	v_lshl_add_u64 v[154:155], v[60:61], 0, s[18:19]
	v_add_f32_dpp v42, v42, v42 row_mirror row_mask:0xf bank_mask:0xf bound_ctrl:1
	v_lshl_add_u64 v[156:157], v[60:61], 0, s[20:21]
	v_readlane_b32 s8, v42, 16
	v_readlane_b32 s9, v42, 48
	v_readlane_b32 s6, v42, 0
	v_readlane_b32 s7, v42, 32
	v_mov_b32_e32 v42, s8
	v_mov_b32_e32 v43, s9
	v_pk_add_f32 v[42:43], s[6:7], v[42:43]
	s_mov_b32 s6, 0x3b800000
	v_add_f32_e32 v42, v42, v43
	v_mul_f32_e32 v42, 0x3b800000, v42
	v_pk_add_f32 v[86:87], v[2:3], v[42:43] op_sel_hi:[1,0] neg_lo:[0,1] neg_hi:[0,1]
	v_pk_add_f32 v[88:89], v[4:5], v[42:43] op_sel_hi:[1,0] neg_lo:[0,1] neg_hi:[0,1]
	v_pk_mul_f32 v[42:43], v[86:87], v[86:87]
	v_pk_mul_f32 v[44:45], v[88:89], v[88:89]
	v_add_f32_e32 v42, v42, v43
	v_add_f32_e32 v42, v44, v42
	s_waitcnt lgkmcnt(0)
	v_add_f32_e32 v44, v6, v7
	v_add_f32_e32 v42, v45, v42
	v_add_f32_e32 v44, v44, v8
	v_add_f32_e32 v44, v44, v9
	v_add_f32_dpp v42, v42, v42 quad_perm:[1,0,3,2] row_mask:0xf bank_mask:0xf bound_ctrl:1
	v_lshl_add_u64 v[158:159], v[60:61], 0, s[22:23]
	v_add_f32_dpp v44, v44, v44 quad_perm:[1,0,3,2] row_mask:0xf bank_mask:0xf bound_ctrl:1
	v_add_f32_dpp v42, v42, v42 quad_perm:[2,3,0,1] row_mask:0xf bank_mask:0xf bound_ctrl:1
	v_lshl_add_u64 v[160:161], v[60:61], 0, s[30:31]
	v_add_f32_dpp v44, v44, v44 quad_perm:[2,3,0,1] row_mask:0xf bank_mask:0xf bound_ctrl:1
	v_add_f32_dpp v42, v42, v42 row_half_mirror row_mask:0xf bank_mask:0xf bound_ctrl:1
	v_lshl_add_u64 v[162:163], v[60:61], 0, s[34:35]
	v_add_f32_dpp v44, v44, v44 row_half_mirror row_mask:0xf bank_mask:0xf bound_ctrl:1
	v_add_f32_dpp v42, v42, v42 row_mirror row_mask:0xf bank_mask:0xf bound_ctrl:1
	v_lshl_add_u64 v[164:165], v[60:61], 0, s[36:37]
	v_readlane_b32 s7, v42, 16
	v_readlane_b32 s39, v42, 48
	v_add_f32_dpp v44, v44, v44 row_mirror row_mask:0xf bank_mask:0xf bound_ctrl:1
	v_readlane_b32 s8, v42, 0
	v_readlane_b32 s9, v42, 32
	v_mov_b32_e32 v42, s7
	v_mov_b32_e32 v43, s39
	v_readlane_b32 s7, v44, 16
	v_readlane_b32 s39, v44, 48
	v_pk_add_f32 v[42:43], s[8:9], v[42:43]
	v_readlane_b32 s8, v44, 0
	v_readlane_b32 s9, v44, 32
	v_mov_b32_e32 v44, s7
	v_mov_b32_e32 v45, s39
	v_pk_add_f32 v[44:45], s[8:9], v[44:45]
	s_nop 0
	v_add_f32_e32 v44, v44, v45
	v_mul_f32_e32 v44, 0x3b800000, v44
	v_pk_add_f32 v[90:91], v[6:7], v[44:45] op_sel_hi:[1,0] neg_lo:[0,1] neg_hi:[0,1]
	v_pk_add_f32 v[92:93], v[8:9], v[44:45] op_sel_hi:[1,0] neg_lo:[0,1] neg_hi:[0,1]
	v_pk_mul_f32 v[46:47], v[90:91], v[90:91]
	v_pk_mul_f32 v[44:45], v[92:93], v[92:93]
	v_add_f32_e32 v46, v46, v47
	v_add_f32_e32 v44, v44, v46
	v_add_f32_e32 v44, v45, v44
	v_mov_b32_e32 v47, v42
	s_nop 0
	v_add_f32_dpp v44, v44, v44 quad_perm:[1,0,3,2] row_mask:0xf bank_mask:0xf bound_ctrl:1
	s_nop 1
	v_add_f32_dpp v44, v44, v44 quad_perm:[2,3,0,1] row_mask:0xf bank_mask:0xf bound_ctrl:1
	s_nop 1
	v_add_f32_dpp v44, v44, v44 row_half_mirror row_mask:0xf bank_mask:0xf bound_ctrl:1
	s_nop 1
	v_add_f32_dpp v44, v44, v44 row_mirror row_mask:0xf bank_mask:0xf bound_ctrl:1
	s_nop 0
	v_readlane_b32 s7, v44, 16
	v_readlane_b32 s39, v44, 48
	v_readlane_b32 s8, v44, 0
	v_readlane_b32 s9, v44, 32
	v_mov_b32_e32 v44, s7
	v_mov_b32_e32 v45, s39
	v_pk_add_f32 v[44:45], s[8:9], v[44:45]
	s_mov_b32 s8, 0x3727c5ac
	v_mov_b32_e32 v46, v44
	v_mov_b32_e32 v42, v45
	v_pk_add_f32 v[42:43], v[46:47], v[42:43]
	v_mov_b64_e32 v[94:95], s[8:9]
	v_pk_fma_f32 v[96:97], v[42:43], s[6:7], v[94:95] op_sel_hi:[1,0,0]
	s_mov_b32 s7, 0x800000
	v_mul_f32_e32 v42, 0x4b800000, v97
	v_cmp_gt_f32_e32 vcc, s7, v97
	s_nop 1
	v_cndmask_b32_e32 v42, v97, v42, vcc
	v_rsq_f32_e32 v97, v42
	global_load_dwordx4 v[54:57], v[26:27], off
	global_load_dwordx4 v[50:53], v[28:29], off
	global_load_dwordx4 v[46:49], v[30:31], off
	global_load_dwordx4 v[42:45], v[32:33], off
	v_mul_f32_e32 v26, 0x45800000, v97
	v_cndmask_b32_e32 v26, v97, v26, vcc
	v_pk_mul_f32 v[28:29], v[86:87], v[26:27] op_sel_hi:[1,0]
	v_cmp_gt_f32_e32 vcc, s7, v96
	s_waitcnt vmcnt(8)
	v_pk_fma_f32 v[28:29], v[34:35], v[28:29], v[38:39]
	v_pk_mul_f32 v[26:27], v[88:89], v[26:27] op_sel_hi:[1,0]
	v_cvt_pk_f16_f32 v28, v28, v29
	v_mul_f32_e32 v29, 0x4b800000, v96
	v_cndmask_b32_e32 v29, v96, v29, vcc
	v_rsq_f32_e32 v32, v29
	v_pk_fma_f32 v[26:27], v[36:37], v[26:27], v[40:41]
	s_nop 0
	v_cvt_pk_f16_f32 v29, v26, v27
	v_mul_f32_e32 v26, 0x45800000, v32
	v_cndmask_b32_e32 v26, v32, v26, vcc
	ds_write_b64 v98, v[28:29]
	v_pk_mul_f32 v[28:29], v[90:91], v[26:27] op_sel_hi:[1,0]
	v_pk_mul_f32 v[26:27], v[92:93], v[26:27] op_sel_hi:[1,0]
	v_pk_fma_f32 v[28:29], v[34:35], v[28:29], v[38:39]
	v_pk_fma_f32 v[26:27], v[36:37], v[26:27], v[40:41]
	v_cvt_pk_f16_f32 v28, v28, v29
	v_cvt_pk_f16_f32 v29, v26, v27
	ds_write_b64 v85, v[28:29]
	ds_read_b128 v[26:29], v99 offset:38416
	v_add_co_u32_e32 v102, vcc, s52, v30
	s_nop 1
	v_addc_co_u32_e32 v103, vcc, 0, v31, vcc
	ds_read_b128 v[30:33], v99 offset:39456
	s_waitcnt lgkmcnt(1)
	v_add_f32_e32 v86, v26, v27
	v_add_f32_e32 v86, v86, v28
	v_add_f32_e32 v86, v86, v29
	s_nop 1
	v_add_f32_dpp v86, v86, v86 quad_perm:[1,0,3,2] row_mask:0xf bank_mask:0xf bound_ctrl:1
	s_nop 1
	v_add_f32_dpp v86, v86, v86 quad_perm:[2,3,0,1] row_mask:0xf bank_mask:0xf bound_ctrl:1
	s_nop 1
	v_add_f32_dpp v86, v86, v86 row_half_mirror row_mask:0xf bank_mask:0xf bound_ctrl:1
	s_nop 1
	v_add_f32_dpp v86, v86, v86 row_mirror row_mask:0xf bank_mask:0xf bound_ctrl:1
	s_nop 0
	v_readlane_b32 s39, v86, 16
	v_readlane_b32 s40, v86, 48
	v_readlane_b32 s8, v86, 0
	v_readlane_b32 s9, v86, 32
	v_mov_b32_e32 v86, s39
	v_mov_b32_e32 v87, s40
	v_pk_add_f32 v[86:87], s[8:9], v[86:87]
	s_nop 0
	v_add_f32_e32 v86, v86, v87
	v_mul_f32_e32 v86, 0x3b800000, v86
	v_pk_add_f32 v[104:105], v[26:27], v[86:87] op_sel_hi:[1,0] neg_lo:[0,1] neg_hi:[0,1]
	v_pk_add_f32 v[106:107], v[28:29], v[86:87] op_sel_hi:[1,0] neg_lo:[0,1] neg_hi:[0,1]
	v_pk_mul_f32 v[88:89], v[104:105], v[104:105]
	v_pk_mul_f32 v[86:87], v[106:107], v[106:107]
	v_add_f32_e32 v88, v88, v89
	v_add_f32_e32 v86, v86, v88
	s_waitcnt lgkmcnt(0)
	v_add_f32_e32 v88, v30, v31
	v_add_f32_e32 v86, v87, v86
	v_add_f32_e32 v88, v88, v32
	v_add_f32_e32 v88, v88, v33
	v_add_f32_dpp v86, v86, v86 quad_perm:[1,0,3,2] row_mask:0xf bank_mask:0xf bound_ctrl:1
	s_nop 0
	v_add_f32_dpp v88, v88, v88 quad_perm:[1,0,3,2] row_mask:0xf bank_mask:0xf bound_ctrl:1
	v_add_f32_dpp v86, v86, v86 quad_perm:[2,3,0,1] row_mask:0xf bank_mask:0xf bound_ctrl:1
	s_nop 0
	v_add_f32_dpp v88, v88, v88 quad_perm:[2,3,0,1] row_mask:0xf bank_mask:0xf bound_ctrl:1
	v_add_f32_dpp v86, v86, v86 row_half_mirror row_mask:0xf bank_mask:0xf bound_ctrl:1
	s_nop 0
	v_add_f32_dpp v88, v88, v88 row_half_mirror row_mask:0xf bank_mask:0xf bound_ctrl:1
	v_add_f32_dpp v86, v86, v86 row_mirror row_mask:0xf bank_mask:0xf bound_ctrl:1
	s_nop 0
	v_readlane_b32 s39, v86, 16
	v_readlane_b32 s40, v86, 48
	v_add_f32_dpp v88, v88, v88 row_mirror row_mask:0xf bank_mask:0xf bound_ctrl:1
	v_readlane_b32 s8, v86, 0
	v_readlane_b32 s9, v86, 32
	v_mov_b32_e32 v86, s39
	v_mov_b32_e32 v87, s40
	v_readlane_b32 s39, v88, 16
	v_readlane_b32 s40, v88, 48
	v_pk_add_f32 v[86:87], s[8:9], v[86:87]
	v_readlane_b32 s8, v88, 0
	v_readlane_b32 s9, v88, 32
	v_mov_b32_e32 v88, s39
	v_mov_b32_e32 v89, s40
	v_pk_add_f32 v[88:89], s[8:9], v[88:89]
	s_nop 0
	v_add_f32_e32 v88, v88, v89
	v_mul_f32_e32 v88, 0x3b800000, v88
	v_pk_add_f32 v[108:109], v[30:31], v[88:89] op_sel_hi:[1,0] neg_lo:[0,1] neg_hi:[0,1]
	v_pk_add_f32 v[110:111], v[32:33], v[88:89] op_sel_hi:[1,0] neg_lo:[0,1] neg_hi:[0,1]
	v_pk_mul_f32 v[90:91], v[108:109], v[108:109]
	v_pk_mul_f32 v[88:89], v[110:111], v[110:111]
	v_add_f32_e32 v90, v90, v91
	v_add_f32_e32 v88, v88, v90
	v_add_f32_e32 v88, v89, v88
	v_mov_b32_e32 v91, v86
	s_nop 0
	v_add_f32_dpp v88, v88, v88 quad_perm:[1,0,3,2] row_mask:0xf bank_mask:0xf bound_ctrl:1
	s_nop 1
	v_add_f32_dpp v88, v88, v88 quad_perm:[2,3,0,1] row_mask:0xf bank_mask:0xf bound_ctrl:1
	s_nop 1
	v_add_f32_dpp v88, v88, v88 row_half_mirror row_mask:0xf bank_mask:0xf bound_ctrl:1
	s_nop 1
	v_add_f32_dpp v88, v88, v88 row_mirror row_mask:0xf bank_mask:0xf bound_ctrl:1
	s_nop 0
	v_readlane_b32 s39, v88, 16
	v_readlane_b32 s40, v88, 48
	v_readlane_b32 s8, v88, 0
	v_readlane_b32 s9, v88, 32
	v_mov_b32_e32 v88, s39
	v_mov_b32_e32 v89, s40
	v_pk_add_f32 v[88:89], s[8:9], v[88:89]
	s_mov_b32 s9, s27
	v_mov_b32_e32 v90, v88
	v_mov_b32_e32 v86, v89
	v_pk_add_f32 v[86:87], v[90:91], v[86:87]
	s_mov_b32 s39, s27
	v_pk_fma_f32 v[112:113], v[86:87], s[6:7], v[94:95] op_sel_hi:[1,0,0]
	s_add_i32 s6, s53, 0x140
	v_mul_f32_e32 v86, 0x4b800000, v113
	v_cmp_gt_f32_e32 vcc, s7, v113
	s_nop 1
	v_cndmask_b32_e32 v86, v113, v86, vcc
	v_rsq_f32_e32 v113, v86
	global_load_dwordx4 v[86:89], v[78:79], off
	global_load_dwordx4 v[90:93], v[102:103], off
	global_load_dwordx4 v[94:97], v[76:77], off
	global_load_dwordx4 v[98:101], v[74:75], off
	v_mul_f32_e32 v74, 0x45800000, v113
	v_cndmask_b32_e32 v74, v113, v74, vcc
	v_pk_mul_f32 v[76:77], v[104:105], v[74:75] op_sel_hi:[1,0]
	v_mul_f32_e32 v75, 0x4b800000, v112
	v_cmp_gt_f32_e32 vcc, s7, v112
	v_pk_fma_f32 v[76:77], v[34:35], v[76:77], v[38:39]
	s_and_b32 s7, s6, 0x1c0
	v_cndmask_b32_e32 v75, v112, v75, vcc
	v_rsq_f32_e32 v78, v75
	v_pk_mul_f32 v[74:75], v[106:107], v[74:75] op_sel_hi:[1,0]
	v_cvt_pk_f16_f32 v76, v76, v77
	v_pk_fma_f32 v[74:75], v[36:37], v[74:75], v[40:41]
	s_lshl_b32 s6, s6, 4
	v_cvt_pk_f16_f32 v77, v74, v75
	v_mul_f32_e32 v74, 0x45800000, v78
	v_cndmask_b32_e32 v74, v78, v74, vcc
	v_pk_mul_f32 v[78:79], v[108:109], v[74:75] op_sel_hi:[1,0]
	s_or_b32 s50, s6, 0x2000
	v_pk_fma_f32 v[34:35], v[34:35], v[78:79], v[38:39]
	v_pk_mul_f32 v[38:39], v[110:111], v[74:75] op_sel_hi:[1,0]
	v_add_co_u32_e32 v78, vcc, s52, v70
	v_pk_fma_f32 v[36:37], v[36:37], v[38:39], v[40:41]
	v_cvt_pk_f16_f32 v34, v34, v35
	v_cvt_pk_f16_f32 v35, v36, v37
	v_addc_co_u32_e32 v79, vcc, 0, v71, vcc
	ds_write2_b64 v85, v[76:77], v[34:35] offset0:66 offset1:132
	s_waitcnt lgkmcnt(0)
	s_barrier
	global_load_dwordx4 v[34:37], v[70:71], off
	global_load_dwordx4 v[38:41], v[72:73], off
	s_nop 0
	global_load_dwordx4 v[70:73], v[78:79], off
	global_load_dwordx4 v[74:77], v[68:69], off
	s_or_b32 s46, s6, 0x6000
	s_sub_i32 s6, s38, s3
	s_and_b32 s6, s6, 0xe0
	v_lshl_add_u32 v172, s6, 1, v84
	s_add_i32 s6, s53, 0x180
	s_lshl_b32 s48, s7, 4
	s_and_b32 s7, s6, 0x1c0
	s_lshl_b32 s6, s6, 4
	s_or_b32 s44, s6, 0x2000
	s_or_b32 s40, s6, 0x6000
	s_add_i32 s6, s3, 0x60
	s_and_b32 s6, s6, 0xe0
	v_lshl_add_u32 v173, s6, 1, v84
	s_add_i32 s6, s53, 0x1c0
	s_xor_b32 s53, s53, 0x100
	v_add_u32_e32 v174, s53, v84
	s_add_i32 s53, s3, 0xa0
	s_lshl_b32 s42, s7, 4
	s_and_b32 s7, s6, 0x1c0
	s_lshl_b32 s6, s6, 4
	s_and_b32 s53, s53, 0xe0
	s_lshl_b32 s8, s7, 4
	s_or_b32 s38, s6, 0x2000
	s_or_b32 s6, s6, 0x6000
	s_mov_b32 s7, s27
	v_lshl_add_u32 v175, s53, 1, v84
	s_add_i32 s53, s3, 0xc0
	s_addk_i32 s3, 0xe0
	v_lshl_add_u64 v[68:69], v[64:65], 0, s[48:49]
	v_lshl_add_u64 v[78:79], v[64:65], 0, s[50:51]
	v_lshl_add_u64 v[138:139], v[64:65], 0, s[46:47]
	v_lshl_add_u64 v[140:141], v[64:65], 0, s[42:43]
	v_lshl_add_u64 v[142:143], v[64:65], 0, s[44:45]
	v_lshl_add_u64 v[144:145], v[64:65], 0, s[40:41]
	v_lshl_add_u64 v[146:147], v[64:65], 0, s[8:9]
	v_lshl_add_u64 v[148:149], v[64:65], 0, s[38:39]
	v_lshl_add_u64 v[150:151], v[64:65], 0, s[6:7]
	s_and_b32 s53, s53, 0xe0
	s_and_b32 s3, s3, 0xe0
	v_add_u32_e32 v64, s28, v83
	v_mov_b32_e32 v65, v67
	v_lshl_add_u32 v176, s53, 1, v84
	v_lshl_add_u32 v177, s3, 1, v84
	v_lshlrev_b64 v[84:85], 10, v[64:65]
	ds_read_b128 v[102:105], v1
	ds_read_b128 v[106:109], v1 offset:8448
	v_lshl_add_u64 v[166:167], v[58:59], 0, v[84:85]
	v_or_b32_e32 v84, 1, v64
	v_mov_b32_e32 v85, v67
	v_lshlrev_b64 v[84:85], 10, v[84:85]
	v_lshl_add_u64 v[168:169], v[58:59], 0, v[84:85]
	v_or_b32_e32 v84, 2, v64
	v_mov_b32_e32 v85, v67
	v_or_b32_e32 v64, 3, v64
	v_lshlrev_b64 v[84:85], 10, v[84:85]
	v_lshlrev_b64 v[64:65], 10, v[64:65]
	v_lshl_add_u64 v[170:171], v[58:59], 0, v[84:85]
	v_lshl_add_u64 v[58:59], v[58:59], 0, v[64:65]
	s_setprio 1
	s_waitcnt vmcnt(13) lgkmcnt(1)
	v_mfma_f32_16x16x32_f16 v[110:113], v[102:105], v[22:25], 0
	s_waitcnt lgkmcnt(0)
	v_mfma_f32_16x16x32_f16 v[22:25], v[106:109], v[22:25], 0
	s_waitcnt vmcnt(5)
	v_mfma_f32_16x16x32_f16 v[114:117], v[102:105], v[94:97], 0
	v_mfma_f32_16x16x32_f16 v[94:97], v[106:109], v[94:97], 0
	v_mfma_f32_16x16x32_f16 v[118:121], v[102:105], v[14:17], 0
	v_mfma_f32_16x16x32_f16 v[14:17], v[106:109], v[14:17], 0
	v_mfma_f32_16x16x32_f16 v[102:105], v[102:105], v[18:21], 0
	v_mfma_f32_16x16x32_f16 v[18:21], v[106:109], v[18:21], 0
	s_setprio 0
	v_add_co_u32_e32 v64, vcc, s29, v62
	global_load_dwordx4 v[106:109], v[62:63], off
	s_nop 0
	v_addc_co_u32_e32 v65, vcc, 0, v63, vcc
	v_add_co_u32_e32 v84, vcc, s52, v62
	s_nop 1
	v_addc_co_u32_e32 v85, vcc, 0, v63, vcc
	v_add_co_u32_e32 v62, vcc, s33, v62
	global_load_dwordx4 v[122:125], v[64:65], off
	global_load_dwordx4 v[126:129], v[84:85], off
	v_addc_co_u32_e32 v63, vcc, 0, v63, vcc
	global_load_dwordx4 v[62:65], v[62:63], off
	ds_read_b128 v[130:133], v82
	ds_read_b128 v[134:137], v82 offset:8448
	s_setprio 1
	s_waitcnt lgkmcnt(1)
	v_mfma_f32_16x16x32_f16 v[110:113], v[130:133], v[10:13], v[110:113]
	s_waitcnt lgkmcnt(0)
	v_mfma_f32_16x16x32_f16 v[10:13], v[134:137], v[10:13], v[22:25]
	v_mfma_f32_16x16x32_f16 v[22:25], v[130:133], v[54:57], v[114:117]
	v_mfma_f32_16x16x32_f16 v[54:57], v[134:137], v[54:57], v[94:97]
	v_mfma_f32_16x16x32_f16 v[94:97], v[130:133], v[86:89], v[118:121]
	v_mfma_f32_16x16x32_f16 v[14:17], v[134:137], v[86:89], v[14:17]
	v_mfma_f32_16x16x32_f16 v[84:87], v[130:133], v[50:53], v[102:105]
	v_mfma_f32_16x16x32_f16 v[18:21], v[134:137], v[50:53], v[18:21]
	s_setprio 0
	global_load_dwordx4 v[50:53], v[68:69], off
	global_load_dwordx4 v[102:105], v[78:79], off
	v_add_co_u32_e32 v68, vcc, s52, v68
	s_nop 1
	v_addc_co_u32_e32 v69, vcc, 0, v69, vcc
	global_load_dwordx4 v[114:117], v[68:69], off
	global_load_dwordx4 v[118:121], v[138:139], off
	ds_read_b128 v[130:133], v172
	ds_read_b128 v[134:137], v172 offset:8448
	s_setprio 1
	s_waitcnt lgkmcnt(1)
	v_mfma_f32_16x16x32_f16 v[110:113], v[130:133], v[46:49], v[110:113]
	s_waitcnt lgkmcnt(0)
	v_mfma_f32_16x16x32_f16 v[10:13], v[134:137], v[46:49], v[10:13]
	v_mfma_f32_16x16x32_f16 v[22:25], v[130:133], v[42:45], v[22:25]
	v_mfma_f32_16x16x32_f16 v[42:45], v[134:137], v[42:45], v[54:57]
	v_mfma_f32_16x16x32_f16 v[46:49], v[130:133], v[90:93], v[94:97]
	v_mfma_f32_16x16x32_f16 v[14:17], v[134:137], v[90:93], v[14:17]
	s_waitcnt vmcnt(12)
	v_mfma_f32_16x16x32_f16 v[54:57], v[130:133], v[98:101], v[84:87]
	v_mfma_f32_16x16x32_f16 v[18:21], v[134:137], v[98:101], v[18:21]
	s_setprio 0
	v_add_co_u32_e32 v68, vcc, s52, v140
	global_load_dwordx4 v[84:87], v[140:141], off
	global_load_dwordx4 v[88:91], v[142:143], off
	v_addc_co_u32_e32 v69, vcc, 0, v141, vcc
	global_load_dwordx4 v[92:95], v[68:69], off
	global_load_dwordx4 v[96:99], v[144:145], off
	ds_read_b128 v[130:133], v173
	ds_read_b128 v[134:137], v173 offset:8448
	s_setprio 1
	s_waitcnt vmcnt(15) lgkmcnt(1)
	v_mfma_f32_16x16x32_f16 v[110:113], v[130:133], v[34:37], v[110:113]
	s_waitcnt lgkmcnt(0)
	v_mfma_f32_16x16x32_f16 v[10:13], v[134:137], v[34:37], v[10:13]
	s_waitcnt vmcnt(14)
	v_mfma_f32_16x16x32_f16 v[22:25], v[130:133], v[38:41], v[22:25]
	v_mfma_f32_16x16x32_f16 v[34:37], v[134:137], v[38:41], v[42:45]
	s_waitcnt vmcnt(13)
	v_mfma_f32_16x16x32_f16 v[38:41], v[130:133], v[70:73], v[46:49]
	v_mfma_f32_16x16x32_f16 v[14:17], v[134:137], v[70:73], v[14:17]
	s_waitcnt vmcnt(12)
	v_mfma_f32_16x16x32_f16 v[42:45], v[130:133], v[74:77], v[54:57]
	v_mfma_f32_16x16x32_f16 v[18:21], v[134:137], v[74:77], v[18:21]
	s_setprio 0
	v_add_co_u32_e32 v68, vcc, s52, v146
	global_load_dwordx4 v[46:49], v[146:147], off
	global_load_dwordx4 v[54:57], v[148:149], off
	v_addc_co_u32_e32 v69, vcc, 0, v147, vcc
	global_load_dwordx4 v[68:71], v[68:69], off
	s_nop 0
	global_load_dwordx4 v[72:75], v[150:151], off
	ds_read_b128 v[76:79], v174
	ds_read_b128 v[130:133], v174 offset:8448
	s_setprio 1
	s_waitcnt vmcnt(15) lgkmcnt(1)
	v_mfma_f32_16x16x32_f16 v[110:113], v[76:79], v[106:109], v[110:113]
	s_waitcnt lgkmcnt(0)
	v_mfma_f32_16x16x32_f16 v[10:13], v[130:133], v[106:109], v[10:13]
	s_waitcnt vmcnt(14)
	v_mfma_f32_16x16x32_f16 v[22:25], v[76:79], v[122:125], v[22:25]
	v_mfma_f32_16x16x32_f16 v[34:37], v[130:133], v[122:125], v[34:37]
	s_waitcnt vmcnt(13)
	v_mfma_f32_16x16x32_f16 v[38:41], v[76:79], v[126:129], v[38:41]
	v_mfma_f32_16x16x32_f16 v[14:17], v[130:133], v[126:129], v[14:17]
	s_waitcnt vmcnt(12)
	v_mfma_f32_16x16x32_f16 v[42:45], v[76:79], v[62:65], v[42:45]
	v_mfma_f32_16x16x32_f16 v[18:21], v[130:133], v[62:65], v[18:21]
	s_setprio 0
	ds_read_b128 v[62:65], v175
	ds_read_b128 v[76:79], v175 offset:8448
	s_setprio 1
	s_waitcnt vmcnt(11) lgkmcnt(1)
	v_mfma_f32_16x16x32_f16 v[106:109], v[62:65], v[50:53], v[110:113]
	s_waitcnt lgkmcnt(0)
	v_mfma_f32_16x16x32_f16 v[10:13], v[76:79], v[50:53], v[10:13]
	s_waitcnt vmcnt(10)
	v_mfma_f32_16x16x32_f16 v[22:25], v[62:65], v[102:105], v[22:25]
	v_mfma_f32_16x16x32_f16 v[34:37], v[76:79], v[102:105], v[34:37]
	s_waitcnt vmcnt(9)
	v_mfma_f32_16x16x32_f16 v[38:41], v[62:65], v[114:117], v[38:41]
	v_mfma_f32_16x16x32_f16 v[14:17], v[76:79], v[114:117], v[14:17]
	s_waitcnt vmcnt(8)
	v_mfma_f32_16x16x32_f16 v[42:45], v[62:65], v[118:121], v[42:45]
	v_mfma_f32_16x16x32_f16 v[18:21], v[76:79], v[118:121], v[18:21]
	s_setprio 0
	ds_read_b128 v[50:53], v176
	ds_read_b128 v[62:65], v176 offset:8448
	s_setprio 1
	s_waitcnt vmcnt(7) lgkmcnt(1)
	v_mfma_f32_16x16x32_f16 v[76:79], v[50:53], v[84:87], v[106:109]
	s_waitcnt lgkmcnt(0)
	v_mfma_f32_16x16x32_f16 v[10:13], v[62:65], v[84:87], v[10:13]
	s_waitcnt vmcnt(6)
	v_mfma_f32_16x16x32_f16 v[22:25], v[50:53], v[88:91], v[22:25]
	v_mfma_f32_16x16x32_f16 v[34:37], v[62:65], v[88:91], v[34:37]
	s_waitcnt vmcnt(5)
	v_mfma_f32_16x16x32_f16 v[38:41], v[50:53], v[92:95], v[38:41]
	v_mfma_f32_16x16x32_f16 v[14:17], v[62:65], v[92:95], v[14:17]
	s_waitcnt vmcnt(4)
	v_mfma_f32_16x16x32_f16 v[42:45], v[50:53], v[96:99], v[42:45]
	v_mfma_f32_16x16x32_f16 v[18:21], v[62:65], v[96:99], v[18:21]
	s_setprio 0
	ds_read_b128 v[50:53], v177
	ds_read_b128 v[62:65], v177 offset:8448
	s_setprio 1
	s_waitcnt vmcnt(3) lgkmcnt(1)
	v_mfma_f32_16x16x32_f16 v[76:79], v[50:53], v[46:49], v[76:79]
	s_waitcnt lgkmcnt(0)
	v_mfma_f32_16x16x32_f16 v[10:13], v[62:65], v[46:49], v[10:13]
	s_waitcnt vmcnt(2)
	v_mfma_f32_16x16x32_f16 v[22:25], v[50:53], v[54:57], v[22:25]
	v_mfma_f32_16x16x32_f16 v[34:37], v[62:65], v[54:57], v[34:37]
	s_waitcnt vmcnt(1)
	v_mfma_f32_16x16x32_f16 v[38:41], v[50:53], v[68:71], v[38:41]
	v_mfma_f32_16x16x32_f16 v[14:17], v[62:65], v[68:71], v[14:17]
	s_waitcnt vmcnt(0)
	v_mfma_f32_16x16x32_f16 v[42:45], v[50:53], v[72:75], v[42:45]
	v_mfma_f32_16x16x32_f16 v[18:21], v[62:65], v[72:75], v[18:21]
	s_setprio 0
	v_add_co_u32_e32 v108, vcc, s29, v152
	v_and_b32_e32 v67, 0x1c0, v0
	s_nop 0
	v_addc_co_u32_e32 v109, vcc, 0, v153, vcc
	v_add_co_u32_e32 v46, vcc, s52, v152
	s_movk_i32 s4, 0x50
	s_nop 0
	v_addc_co_u32_e32 v47, vcc, 0, v153, vcc
	v_add_co_u32_e32 v68, vcc, s33, v152
	v_or_b32_e32 v116, 16, v67
	s_nop 0
	v_addc_co_u32_e32 v69, vcc, 0, v153, vcc
	v_add_co_u32_e32 v110, vcc, s52, v154
	global_load_dwordx4 v[46:49], v[46:47], off
	s_nop 0
	global_load_dwordx4 v[50:53], v[68:69], off
	global_load_dwordx4 v[54:57], v[152:153], off
	global_load_dwordx4 v[62:65], v[154:155], off
	v_addc_co_u32_e32 v111, vcc, 0, v155, vcc
	v_add_co_u32_e32 v112, vcc, s52, v160
	global_load_dwordx4 v[68:71], v[156:157], off
	global_load_dwordx4 v[72:75], v[158:159], off
	global_load_dwordx4 v[84:87], v[160:161], off
	global_load_dwordx4 v[88:91], v[162:163], off
	v_addc_co_u32_e32 v113, vcc, 0, v161, vcc
	global_load_dwordx4 v[92:95], v[110:111], off
	global_load_dwordx4 v[96:99], v[112:113], off
	global_load_dwordx4 v[100:103], v[108:109], off
	global_load_dwordx4 v[104:107], v[164:165], off
	s_nop 0
	global_store_dwordx4 v[166:167], v[2:5], off sc0 sc1
	global_store_dwordx4 v[168:169], v[6:9], off sc0 sc1
	global_store_dwordx4 v[170:171], v[26:29], off sc0 sc1
	global_store_dwordx4 v[58:59], v[30:33], off sc0 sc1
	v_and_b32_e32 v4, 0x1cf, v0
	v_cvt_pk_f16_f32 v3, v78, v79
	v_cvt_pk_f16_f32 v2, v76, v77
	v_mad_u32_u24 v4, v4, s4, v80
	v_or_b32_e32 v5, v116, v81
	v_or_b32_e32 v117, 32, v67
	ds_write_b64 v4, v[2:3]
	v_cvt_pk_f16_f32 v3, v24, v25
	v_cvt_pk_f16_f32 v2, v22, v23
	v_mad_u32_u24 v5, v5, s4, v80
	v_or_b32_e32 v6, v117, v81
	v_or_b32_e32 v118, 48, v67
	ds_write_b64 v5, v[2:3]
	v_cvt_pk_f16_f32 v3, v40, v41
	v_cvt_pk_f16_f32 v2, v38, v39
	v_mad_u32_u24 v6, v6, s4, v80
	v_or_b32_e32 v7, v118, v81
	ds_write_b64 v6, v[2:3]
	v_cvt_pk_f16_f32 v3, v44, v45
	v_cvt_pk_f16_f32 v2, v42, v43
	v_mad_u32_u24 v7, v7, s4, v80
	ds_write_b64 v7, v[2:3]
	v_cvt_pk_f16_f32 v3, v12, v13
	v_cvt_pk_f16_f32 v2, v10, v11
	ds_write_b64 v4, v[2:3] offset:32
	v_cvt_pk_f16_f32 v3, v36, v37
	v_cvt_pk_f16_f32 v2, v34, v35
	ds_write_b64 v5, v[2:3] offset:32
	v_cvt_pk_f16_f32 v3, v16, v17
	v_cvt_pk_f16_f32 v2, v14, v15
	v_lshl_add_u64 v[10:11], v[60:61], 0, s[14:15]
	ds_write_b64 v6, v[2:3] offset:32
	v_cvt_pk_f16_f32 v2, v18, v19
	v_add_co_u32_e32 v18, vcc, s52, v10
	v_cvt_pk_f16_f32 v3, v20, v21
	v_lshl_add_u64 v[12:13], v[60:61], 0, s[16:17]
	v_addc_co_u32_e32 v19, vcc, 0, v11, vcc
	ds_write_b64 v7, v[2:3] offset:32
	s_waitcnt lgkmcnt(0)
	s_barrier
	global_load_dwordx4 v[2:5], v[10:11], off
	global_load_dwordx4 v[6:9], v[12:13], off
	v_lshl_add_u64 v[20:21], v[60:61], 0, s[12:13]
	global_load_dwordx4 v[10:13], v[18:19], off
	global_load_dwordx4 v[14:17], v[20:21], off
	ds_read_b128 v[18:21], v1
	ds_read_b128 v[22:25], v1 offset:8448
	s_mov_b32 s3, s27
	s_setprio 1
	s_waitcnt vmcnt(17) lgkmcnt(1)
	v_mfma_f32_16x16x32_f16 v[26:29], v[18:21], v[54:57], 0
	s_waitcnt lgkmcnt(0)
	v_mfma_f32_16x16x32_f16 v[30:33], v[22:25], v[54:57], 0
	s_waitcnt vmcnt(9)
	v_mfma_f32_16x16x32_f16 v[34:37], v[18:21], v[100:103], 0
	v_mfma_f32_16x16x32_f16 v[38:41], v[22:25], v[100:103], 0
	v_mfma_f32_16x16x32_f16 v[42:45], v[18:21], v[46:49], 0
	v_mfma_f32_16x16x32_f16 v[46:49], v[22:25], v[46:49], 0
	v_mfma_f32_16x16x32_f16 v[18:21], v[18:21], v[50:53], 0
	v_mfma_f32_16x16x32_f16 v[22:25], v[22:25], v[50:53], 0
	s_setprio 0
	v_lshl_add_u64 v[58:59], v[60:61], 0, s[10:11]
	v_add_co_u32_e32 v76, vcc, s29, v58
	s_nop 1
	v_addc_co_u32_e32 v77, vcc, 0, v59, vcc
	v_add_co_u32_e32 v108, vcc, s52, v58
	global_load_dwordx4 v[50:53], v[58:59], off
	global_load_dwordx4 v[54:57], v[76:77], off
	v_addc_co_u32_e32 v109, vcc, 0, v59, vcc
	v_add_co_u32_e32 v58, vcc, s33, v58
	s_nop 1
	v_addc_co_u32_e32 v59, vcc, 0, v59, vcc
	global_load_dwordx4 v[76:79], v[108:109], off
	global_load_dwordx4 v[100:103], v[58:59], off
	ds_read_b128 v[108:111], v82
	ds_read_b128 v[112:115], v82 offset:8448
	s_setprio 1
	s_waitcnt lgkmcnt(1)
	v_mfma_f32_16x16x32_f16 v[26:29], v[108:111], v[62:65], v[26:29]
	s_waitcnt lgkmcnt(0)
	v_mfma_f32_16x16x32_f16 v[30:33], v[112:115], v[62:65], v[30:33]
	v_mfma_f32_16x16x32_f16 v[34:37], v[108:111], v[68:71], v[34:37]
	v_mfma_f32_16x16x32_f16 v[38:41], v[112:115], v[68:71], v[38:41]
	v_mfma_f32_16x16x32_f16 v[42:45], v[108:111], v[92:95], v[42:45]
	v_mfma_f32_16x16x32_f16 v[46:49], v[112:115], v[92:95], v[46:49]
	v_mfma_f32_16x16x32_f16 v[18:21], v[108:111], v[72:75], v[18:21]
	v_mfma_f32_16x16x32_f16 v[22:25], v[112:115], v[72:75], v[22:25]
	s_setprio 0
	v_lshl_add_u64 v[58:59], v[60:61], 0, s[48:49]
	v_lshl_add_u64 v[72:73], v[60:61], 0, s[50:51]
	global_load_dwordx4 v[62:65], v[58:59], off
	global_load_dwordx4 v[68:71], v[72:73], off
	v_add_co_u32_e32 v58, vcc, s52, v58
	v_lshl_add_u64 v[82:83], v[60:61], 0, s[46:47]
	s_nop 0
	v_addc_co_u32_e32 v59, vcc, 0, v59, vcc
	global_load_dwordx4 v[72:75], v[58:59], off
	global_load_dwordx4 v[92:95], v[82:83], off
	ds_read_b128 v[108:111], v172
	ds_read_b128 v[112:115], v172 offset:8448
	s_setprio 1
	s_waitcnt lgkmcnt(1)
	v_mfma_f32_16x16x32_f16 v[26:29], v[108:111], v[84:87], v[26:29]
	s_waitcnt lgkmcnt(0)
	v_mfma_f32_16x16x32_f16 v[30:33], v[112:115], v[84:87], v[30:33]
	v_mfma_f32_16x16x32_f16 v[34:37], v[108:111], v[88:91], v[34:37]
	v_mfma_f32_16x16x32_f16 v[38:41], v[112:115], v[88:91], v[38:41]
	v_mfma_f32_16x16x32_f16 v[42:45], v[108:111], v[96:99], v[42:45]
	v_mfma_f32_16x16x32_f16 v[46:49], v[112:115], v[96:99], v[46:49]
	s_waitcnt vmcnt(16)
	v_mfma_f32_16x16x32_f16 v[18:21], v[108:111], v[104:107], v[18:21]
	v_mfma_f32_16x16x32_f16 v[22:25], v[112:115], v[104:107], v[22:25]
	s_setprio 0
	v_lshl_add_u64 v[58:59], v[60:61], 0, s[42:43]
	v_lshl_add_u64 v[90:91], v[60:61], 0, s[44:45]
	global_load_dwordx4 v[82:85], v[58:59], off
	global_load_dwordx4 v[86:89], v[90:91], off
	v_add_co_u32_e32 v58, vcc, s52, v58
	v_lshl_add_u64 v[90:91], v[60:61], 0, s[40:41]
	s_nop 0
	v_addc_co_u32_e32 v59, vcc, 0, v59, vcc
	global_load_dwordx4 v[96:99], v[58:59], off
	global_load_dwordx4 v[104:107], v[90:91], off
	ds_read_b128 v[108:111], v173
	ds_read_b128 v[112:115], v173 offset:8448
	s_setprio 1
	s_waitcnt vmcnt(15) lgkmcnt(1)
	v_mfma_f32_16x16x32_f16 v[26:29], v[108:111], v[2:5], v[26:29]
	s_waitcnt lgkmcnt(0)
	v_mfma_f32_16x16x32_f16 v[2:5], v[112:115], v[2:5], v[30:33]
	s_waitcnt vmcnt(14)
	v_mfma_f32_16x16x32_f16 v[30:33], v[108:111], v[6:9], v[34:37]
	v_mfma_f32_16x16x32_f16 v[6:9], v[112:115], v[6:9], v[38:41]
	s_waitcnt vmcnt(13)
	v_mfma_f32_16x16x32_f16 v[34:37], v[108:111], v[10:13], v[42:45]
	v_mfma_f32_16x16x32_f16 v[10:13], v[112:115], v[10:13], v[46:49]
	s_waitcnt vmcnt(12)
	v_mfma_f32_16x16x32_f16 v[18:21], v[108:111], v[14:17], v[18:21]
	v_mfma_f32_16x16x32_f16 v[14:17], v[112:115], v[14:17], v[22:25]
	s_setprio 0
	v_lshl_add_u64 v[42:43], v[60:61], 0, s[8:9]
	v_add_co_u32_e32 v58, vcc, s52, v42
	v_lshl_add_u64 v[44:45], v[60:61], 0, s[38:39]
	s_nop 0
	v_addc_co_u32_e32 v59, vcc, 0, v43, vcc
	global_load_dwordx4 v[22:25], v[42:43], off
	global_load_dwordx4 v[38:41], v[44:45], off
	v_lshl_add_u64 v[60:61], v[60:61], 0, s[6:7]
	global_load_dwordx4 v[42:45], v[58:59], off
	global_load_dwordx4 v[46:49], v[60:61], off
	ds_read_b128 v[58:61], v174
	ds_read_b128 v[108:111], v174 offset:8448
	s_setprio 1
	s_waitcnt vmcnt(15) lgkmcnt(1)
	v_mfma_f32_16x16x32_f16 v[26:29], v[58:61], v[50:53], v[26:29]
	s_waitcnt lgkmcnt(0)
	v_mfma_f32_16x16x32_f16 v[2:5], v[108:111], v[50:53], v[2:5]
	s_waitcnt vmcnt(14)
	v_mfma_f32_16x16x32_f16 v[30:33], v[58:61], v[54:57], v[30:33]
	v_mfma_f32_16x16x32_f16 v[6:9], v[108:111], v[54:57], v[6:9]
	s_waitcnt vmcnt(13)
	v_mfma_f32_16x16x32_f16 v[34:37], v[58:61], v[76:79], v[34:37]
	v_mfma_f32_16x16x32_f16 v[10:13], v[108:111], v[76:79], v[10:13]
	s_waitcnt vmcnt(12)
	v_mfma_f32_16x16x32_f16 v[18:21], v[58:61], v[100:103], v[18:21]
	v_mfma_f32_16x16x32_f16 v[14:17], v[108:111], v[100:103], v[14:17]
	s_setprio 0
	ds_read_b128 v[50:53], v175
	ds_read_b128 v[54:57], v175 offset:8448
	s_setprio 1
	s_waitcnt vmcnt(11) lgkmcnt(1)
	v_mfma_f32_16x16x32_f16 v[26:29], v[50:53], v[62:65], v[26:29]
	s_waitcnt lgkmcnt(0)
	v_mfma_f32_16x16x32_f16 v[2:5], v[54:57], v[62:65], v[2:5]
	s_waitcnt vmcnt(10)
	v_mfma_f32_16x16x32_f16 v[30:33], v[50:53], v[68:71], v[30:33]
	v_mfma_f32_16x16x32_f16 v[6:9], v[54:57], v[68:71], v[6:9]
	s_waitcnt vmcnt(9)
	v_mfma_f32_16x16x32_f16 v[34:37], v[50:53], v[72:75], v[34:37]
	v_mfma_f32_16x16x32_f16 v[10:13], v[54:57], v[72:75], v[10:13]
	s_waitcnt vmcnt(8)
	v_mfma_f32_16x16x32_f16 v[18:21], v[50:53], v[92:95], v[18:21]
	v_mfma_f32_16x16x32_f16 v[14:17], v[54:57], v[92:95], v[14:17]
	s_setprio 0
	ds_read_b128 v[50:53], v176
	ds_read_b128 v[54:57], v176 offset:8448
	s_setprio 1
	s_waitcnt vmcnt(7) lgkmcnt(1)
	v_mfma_f32_16x16x32_f16 v[26:29], v[50:53], v[82:85], v[26:29]
	s_waitcnt lgkmcnt(0)
	v_mfma_f32_16x16x32_f16 v[2:5], v[54:57], v[82:85], v[2:5]
	s_waitcnt vmcnt(6)
	v_mfma_f32_16x16x32_f16 v[30:33], v[50:53], v[86:89], v[30:33]
	v_mfma_f32_16x16x32_f16 v[6:9], v[54:57], v[86:89], v[6:9]
	s_waitcnt vmcnt(5)
	v_mfma_f32_16x16x32_f16 v[34:37], v[50:53], v[96:99], v[34:37]
	v_mfma_f32_16x16x32_f16 v[58:61], v[54:57], v[96:99], v[10:13]
	s_waitcnt vmcnt(4)
	v_mfma_f32_16x16x32_f16 v[18:21], v[50:53], v[104:107], v[18:21]
	v_mfma_f32_16x16x32_f16 v[50:53], v[54:57], v[104:107], v[14:17]
	s_setprio 0
	ds_read_b128 v[54:57], v177
	ds_read_b128 v[62:65], v177 offset:8448
	s_setprio 1
	s_waitcnt vmcnt(3) lgkmcnt(1)
	v_mfma_f32_16x16x32_f16 v[26:29], v[54:57], v[22:25], v[26:29]
	s_waitcnt lgkmcnt(0)
	v_mfma_f32_16x16x32_f16 v[14:17], v[62:65], v[22:25], v[2:5]
	s_waitcnt vmcnt(2)
	v_mfma_f32_16x16x32_f16 v[22:25], v[54:57], v[38:41], v[30:33]
	v_mfma_f32_16x16x32_f16 v[10:13], v[62:65], v[38:41], v[6:9]
	s_waitcnt vmcnt(1)
	v_mfma_f32_16x16x32_f16 v[30:33], v[54:57], v[42:45], v[34:37]
	v_mfma_f32_16x16x32_f16 v[6:9], v[62:65], v[42:45], v[58:61]
	s_waitcnt vmcnt(0)
	v_mfma_f32_16x16x32_f16 v[34:37], v[54:57], v[46:49], v[18:21]
	v_mfma_f32_16x16x32_f16 v[2:5], v[62:65], v[46:49], v[50:53]
	s_setprio 0
	s_nop 1
	v_mul_u32_u24_e32 v52, 0x50, v0
	ds_read_b128 v[18:21], v52
	s_lshl_b64 s[2:3], s[2:3], 15
	v_or_b32_e32 v0, s2, v66
	v_mov_b32_e32 v1, s3
	v_lshl_add_u64 v[50:51], s[24:25], 0, v[0:1]
	ds_read_b128 v[38:41], v52 offset:16
	ds_read_b128 v[42:45], v52 offset:32
	ds_read_b128 v[46:49], v52 offset:48
	s_waitcnt lgkmcnt(3)
	global_store_dwordx4 v[50:51], v[18:21], off sc0 sc1
	s_nop 1
	v_add_co_u32_e32 v18, vcc, s29, v50
	s_nop 1
	v_addc_co_u32_e32 v19, vcc, 0, v51, vcc
	s_waitcnt lgkmcnt(2)
	global_store_dwordx4 v[18:19], v[38:41], off sc0 sc1
	v_or_b32_e32 v18, 0x4000, v0
	v_mov_b32_e32 v19, s3
	v_lshl_add_u64 v[20:21], s[24:25], 0, v[18:19]
	s_waitcnt lgkmcnt(1)
	global_store_dwordx4 v[20:21], v[42:45], off sc0 sc1
	v_mul_f32_e32 v20, 0xbfb8aa3b, v26
	v_exp_f32_e32 v38, v20
	v_add_co_u32_e32 v20, vcc, s33, v50
	v_or_b32_e32 v39, 0x200, v81
	s_nop 0
	v_addc_co_u32_e32 v21, vcc, 0, v51, vcc
	s_waitcnt lgkmcnt(0)
	global_store_dwordx4 v[20:21], v[46:49], off sc0 sc1
	v_add_f32_e32 v20, 1.0, v38
	v_rcp_f32_e32 v20, v20
	v_mul_f32_e32 v21, 0xbfb8aa3b, v27
	v_mul_f32_e32 v38, 0xbfb8aa3b, v28
	v_exp_f32_e32 v21, v21
	v_exp_f32_e32 v38, v38
	v_fma_mixlo_f16 v40, v26, v20, 0
	v_mul_f32_e32 v26, 0xbfb8aa3b, v29
	v_add_f32_e32 v20, 1.0, v21
	v_add_f32_e32 v21, 1.0, v38
	v_exp_f32_e32 v38, v26
	v_rcp_f32_e32 v20, v20
	v_rcp_f32_e32 v21, v21
	v_mov_b32_e32 v26, v27
	v_mov_b32_e32 v27, v28
	v_add_f32_e32 v28, 1.0, v38
	v_rcp_f32_e32 v28, v28
	v_pk_mul_f32 v[20:21], v[26:27], v[20:21]
	v_or_b32_e32 v27, v39, v67
	v_cvt_pk_f16_f32 v21, v20, v21
	v_fma_mixlo_f16 v26, v29, v28, 0
	v_pack_b32_f16 v20, v40, v21
	v_alignbit_b32 v21, v26, v21, 16
	v_mul_f32_e32 v26, 0xbfb8aa3b, v22
	v_exp_f32_e32 v26, v26
	v_mad_u32_u24 v27, v27, s4, v80
	ds_write_b64 v27, v[20:21]
	v_mul_f32_e32 v21, 0xbfb8aa3b, v23
	v_add_f32_e32 v20, 1.0, v26
	v_rcp_f32_e32 v20, v20
	v_mul_f32_e32 v26, 0xbfb8aa3b, v24
	v_exp_f32_e32 v21, v21
	v_exp_f32_e32 v26, v26
	v_fma_mixlo_f16 v28, v22, v20, 0
	v_mul_f32_e32 v22, 0xbfb8aa3b, v25
	v_add_f32_e32 v20, 1.0, v21
	v_add_f32_e32 v21, 1.0, v26
	v_exp_f32_e32 v26, v22
	v_rcp_f32_e32 v20, v20
	v_rcp_f32_e32 v21, v21
	v_mov_b32_e32 v22, v23
	v_mov_b32_e32 v23, v24
	v_add_f32_e32 v24, 1.0, v26
	v_rcp_f32_e32 v24, v24
	v_pk_mul_f32 v[20:21], v[22:23], v[20:21]
	v_or_b32_e32 v23, v116, v39
	v_cvt_pk_f16_f32 v21, v20, v21
	v_fma_mixlo_f16 v22, v25, v24, 0
	v_pack_b32_f16 v20, v28, v21
	v_alignbit_b32 v21, v22, v21, 16
	v_mul_f32_e32 v22, 0xbfb8aa3b, v30
	v_exp_f32_e32 v22, v22
	v_mad_u32_u24 v24, v23, s4, v80
	ds_write_b64 v24, v[20:21]
	v_mul_f32_e32 v21, 0xbfb8aa3b, v31
	v_add_f32_e32 v20, 1.0, v22
	v_mul_f32_e32 v22, 0xbfb8aa3b, v32
	v_rcp_f32_e32 v20, v20
	v_exp_f32_e32 v21, v21
	v_exp_f32_e32 v22, v22
	v_mov_b32_e32 v23, v32
	v_fma_mixlo_f16 v25, v30, v20, 0
	v_add_f32_e32 v20, 1.0, v21
	v_add_f32_e32 v21, 1.0, v22
	v_mul_f32_e32 v22, 0xbfb8aa3b, v33
	v_exp_f32_e32 v26, v22
	v_rcp_f32_e32 v20, v20
	v_rcp_f32_e32 v21, v21
	v_mov_b32_e32 v22, v31
	v_add_f32_e32 v26, 1.0, v26
	v_rcp_f32_e32 v26, v26
	v_pk_mul_f32 v[20:21], v[22:23], v[20:21]
	v_or_b32_e32 v23, v117, v39
	v_cvt_pk_f16_f32 v21, v20, v21
	v_fma_mixlo_f16 v22, v33, v26, 0
	v_pack_b32_f16 v20, v25, v21
	v_alignbit_b32 v21, v22, v21, 16
	v_mul_f32_e32 v22, 0xbfb8aa3b, v34
	v_exp_f32_e32 v22, v22
	v_mad_u32_u24 v25, v23, s4, v80
	ds_write_b64 v25, v[20:21]
	v_mul_f32_e32 v21, 0xbfb8aa3b, v35
	v_add_f32_e32 v20, 1.0, v22
	v_mul_f32_e32 v22, 0xbfb8aa3b, v36
	v_rcp_f32_e32 v20, v20
	v_exp_f32_e32 v21, v21
	v_exp_f32_e32 v22, v22
	v_mov_b32_e32 v23, v36
	v_fma_mixlo_f16 v26, v34, v20, 0
	v_add_f32_e32 v20, 1.0, v21
	v_add_f32_e32 v21, 1.0, v22
	v_mul_f32_e32 v22, 0xbfb8aa3b, v37
	v_exp_f32_e32 v28, v22
	v_rcp_f32_e32 v20, v20
	v_rcp_f32_e32 v21, v21
	v_mov_b32_e32 v22, v35
	v_add_f32_e32 v28, 1.0, v28
	v_rcp_f32_e32 v28, v28
	v_pk_mul_f32 v[20:21], v[22:23], v[20:21]
	v_or_b32_e32 v23, v118, v39
	v_cvt_pk_f16_f32 v21, v20, v21
	v_fma_mixlo_f16 v22, v37, v28, 0
	v_pack_b32_f16 v20, v26, v21
	v_alignbit_b32 v21, v22, v21, 16
	v_mul_f32_e32 v22, 0xbfb8aa3b, v14
	v_exp_f32_e32 v22, v22
	v_mad_u32_u24 v23, v23, s4, v80
	ds_write_b64 v23, v[20:21]
	v_mul_f32_e32 v21, 0xbfb8aa3b, v15
	v_add_f32_e32 v20, 1.0, v22
	v_rcp_f32_e32 v20, v20
	v_exp_f32_e32 v21, v21
	v_mul_f32_e32 v22, 0xbfb8aa3b, v16
	v_exp_f32_e32 v22, v22
	v_fma_mixlo_f16 v26, v14, v20, 0
	v_add_f32_e32 v14, 1.0, v21
	v_rcp_f32_e32 v20, v14
	v_add_f32_e32 v14, 1.0, v22
	v_rcp_f32_e32 v21, v14
	v_mov_b32_e32 v14, v15
	v_mul_f32_e32 v15, 0xbfb8aa3b, v17
	v_exp_f32_e32 v22, v15
	v_mov_b32_e32 v15, v16
	v_pk_mul_f32 v[14:15], v[14:15], v[20:21]
	v_mul_f32_e32 v20, 0xbfb8aa3b, v10
	v_cvt_pk_f16_f32 v15, v14, v15
	v_add_f32_e32 v14, 1.0, v22
	v_rcp_f32_e32 v16, v14
	v_exp_f32_e32 v20, v20
	v_pack_b32_f16 v14, v26, v15
	v_lshl_add_u64 v[0:1], s[0:1], 0, v[0:1]
	v_fma_mixlo_f16 v16, v17, v16, 0
	v_alignbit_b32 v15, v16, v15, 16
	ds_write_b64 v27, v[14:15] offset:32
	v_add_f32_e32 v14, 1.0, v20
	v_mul_f32_e32 v15, 0xbfb8aa3b, v11
	v_rcp_f32_e32 v14, v14
	v_exp_f32_e32 v15, v15
	v_mul_f32_e32 v16, 0xbfb8aa3b, v12
	v_exp_f32_e32 v16, v16
	v_fma_mixlo_f16 v17, v10, v14, 0
	v_add_f32_e32 v10, 1.0, v15
	v_rcp_f32_e32 v14, v10
	v_add_f32_e32 v10, 1.0, v16
	v_rcp_f32_e32 v15, v10
	v_mov_b32_e32 v10, v11
	v_mul_f32_e32 v11, 0xbfb8aa3b, v13
	v_exp_f32_e32 v16, v11
	v_mov_b32_e32 v11, v12
	v_pk_mul_f32 v[10:11], v[10:11], v[14:15]
	v_mul_f32_e32 v14, 0xbfb8aa3b, v6
	v_cvt_pk_f16_f32 v11, v10, v11
	v_add_f32_e32 v10, 1.0, v16
	v_rcp_f32_e32 v12, v10
	v_exp_f32_e32 v14, v14
	v_pack_b32_f16 v10, v17, v11
	v_fma_mixlo_f16 v12, v13, v12, 0
	v_alignbit_b32 v11, v12, v11, 16
	ds_write_b64 v24, v[10:11] offset:32
	v_add_f32_e32 v10, 1.0, v14
	v_mul_f32_e32 v11, 0xbfb8aa3b, v7
	v_rcp_f32_e32 v10, v10
	v_exp_f32_e32 v11, v11
	v_mul_f32_e32 v12, 0xbfb8aa3b, v8
	v_exp_f32_e32 v12, v12
	v_fma_mixlo_f16 v13, v6, v10, 0
	v_add_f32_e32 v6, 1.0, v11
	v_rcp_f32_e32 v10, v6
	v_add_f32_e32 v6, 1.0, v12
	v_rcp_f32_e32 v11, v6
	v_mov_b32_e32 v6, v7
	v_mul_f32_e32 v7, 0xbfb8aa3b, v9
	v_exp_f32_e32 v12, v7
	v_mov_b32_e32 v7, v8
	v_pk_mul_f32 v[6:7], v[6:7], v[10:11]
	v_mul_f32_e32 v10, 0xbfb8aa3b, v2
	v_cvt_pk_f16_f32 v7, v6, v7
	v_add_f32_e32 v6, 1.0, v12
	v_rcp_f32_e32 v8, v6
	v_exp_f32_e32 v10, v10
	v_pack_b32_f16 v6, v13, v7
	v_fma_mixlo_f16 v8, v9, v8, 0
	v_alignbit_b32 v7, v8, v7, 16
	ds_write_b64 v25, v[6:7] offset:32
	v_add_f32_e32 v6, 1.0, v10
	v_mul_f32_e32 v7, 0xbfb8aa3b, v3
	v_rcp_f32_e32 v6, v6
	v_exp_f32_e32 v7, v7
	v_mul_f32_e32 v8, 0xbfb8aa3b, v4
	v_exp_f32_e32 v8, v8
	v_fma_mixlo_f16 v9, v2, v6, 0
	v_add_f32_e32 v2, 1.0, v7
	v_mul_f32_e32 v7, 0xbfb8aa3b, v5
	v_rcp_f32_e32 v6, v2
	v_add_f32_e32 v2, 1.0, v8
	v_exp_f32_e32 v8, v7
	v_rcp_f32_e32 v7, v2
	v_mov_b32_e32 v2, v3
	v_mov_b32_e32 v3, v4
	v_add_f32_e32 v4, 1.0, v8
	v_rcp_f32_e32 v4, v4
	v_pk_mul_f32 v[2:3], v[2:3], v[6:7]
	v_fma_mixlo_f16 v4, v5, v4, 0
	v_cvt_pk_f16_f32 v3, v2, v3
	v_pack_b32_f16 v2, v9, v3
	v_alignbit_b32 v3, v4, v3, 16
	ds_write_b64 v23, v[2:3] offset:32
	s_waitcnt lgkmcnt(0)
	s_barrier
	ds_read_b128 v[2:5], v52 offset:40960
	ds_read_b128 v[6:9], v52 offset:40976
	ds_read_b128 v[10:13], v52 offset:40992
	ds_read_b128 v[14:17], v52 offset:41008
	s_waitcnt lgkmcnt(3)
	global_store_dwordx4 v[0:1], v[2:5], off sc0 sc1
	s_nop 1
	v_add_co_u32_e32 v2, vcc, 0x2000, v0
	s_nop 1
	v_addc_co_u32_e32 v3, vcc, 0, v1, vcc
	v_add_co_u32_e32 v0, vcc, 0x6000, v0
	s_waitcnt lgkmcnt(2)
	global_store_dwordx4 v[2:3], v[6:9], off sc0 sc1
	v_lshl_add_u64 v[2:3], s[0:1], 0, v[18:19]
	v_addc_co_u32_e32 v1, vcc, 0, v1, vcc
	s_waitcnt lgkmcnt(1)
	global_store_dwordx4 v[2:3], v[10:13], off sc0 sc1
	s_waitcnt lgkmcnt(0)
	global_store_dwordx4 v[0:1], v[14:17], off sc0 sc1
	s_endpgm
	.p2align	8
